# xor-butterfly ds_bpermute lane exchanges in GEMM epilogues / row sums replaced by DPP movs (xor 1,2,4,8) and v_permlane16/32_swap pairs (xor 16,32); on top of v11
# baseline (speedup 1.0000x reference)
; #define GAS __attribute__((address_space(1)))
; __device__ __forceinline__ float wave_sum(float v) {
; #pragma unroll
;     for (int o = 1; o < 64; o <<= 1) v += __shfl_xor(v, o);
;     return v;
; __global__ void __launch_bounds__(NWAVES * 64, 2) mk_fwd(Args args) {
;     ...
;         for (int m = gw; m < MTOK; m += NGW) {
;             const GAS f32x4* xr = (const GAS f32x4*)(x + (size_t)m * DMODEL) + lane;
;             f32x4 v[16]; float s = 0.f;
; #pragma unroll
;             for (int j = 0; j < 16; ++j) { v[j] = __builtin_nontemporal_load(xr + 64 * j); s += (v[j].x * v[j].x + v[j].y * v[j].y) + (v[j].z * v[j].z + v[j].w * v[j].w); }
;             s = wave_sum(s);
;             if (lane == 0) SS0[m] = s;
.LBB0_44:
	v_add_co_u32_e32 v2, vcc, s16, v72
	s_nop 1
	v_addc_co_u32_e32 v3, vcc, -1, v73, vcc
	global_load_dwordx4 v[46:49], v[2:3], off offset:-3072 nt
	global_load_dwordx4 v[42:45], v[2:3], off offset:-2048 nt
	global_load_dwordx4 v[38:41], v[2:3], off offset:-1024 nt
	global_load_dwordx4 v[34:37], v[2:3], off nt
	v_add_co_u32_e32 v2, vcc, s17, v72
	s_waitcnt vmcnt(3)
	v_mul_f32_e32 v74, v47, v47
	v_addc_co_u32_e32 v3, vcc, -1, v73, vcc
	global_load_dwordx4 v[30:33], v[2:3], off offset:-3072 nt
	global_load_dwordx4 v[22:25], v[2:3], off offset:-2048 nt
	global_load_dwordx4 v[14:17], v[2:3], off offset:-1024 nt
	global_load_dwordx4 v[6:9], v[72:73], off offset:-4096 nt
	v_add_co_u32_e32 v2, vcc, 0xffffd000, v72
	v_mul_f32_e32 v75, v49, v49
	s_nop 0
	v_addc_co_u32_e32 v3, vcc, -1, v73, vcc
	global_load_dwordx4 v[62:65], v[2:3], off offset:-3072 nt
	global_load_dwordx4 v[54:57], v[2:3], off offset:-2048 nt
	global_load_dwordx4 v[58:61], v[2:3], off offset:-1024 nt
	global_load_dwordx4 v[50:53], v[2:3], off nt
	global_load_dwordx4 v[26:29], v[72:73], off offset:-3072 nt
	global_load_dwordx4 v[18:21], v[72:73], off offset:-2048 nt
	global_load_dwordx4 v[10:13], v[72:73], off offset:-1024 nt
	s_nop 0
	global_load_dwordx4 v[2:5], v[72:73], off nt
	s_waitcnt vmcnt(14)
	v_mul_f32_e32 v76, v43, v43
	v_mul_f32_e32 v77, v45, v45
	s_waitcnt vmcnt(13)
	v_mul_f32_e32 v86, v39, v39
	v_mul_f32_e32 v87, v41, v41
	v_fmac_f32_e32 v74, v46, v46
	v_fmac_f32_e32 v75, v48, v48
	v_fmac_f32_e32 v76, v42, v42
	v_fmac_f32_e32 v77, v44, v44
	v_fmac_f32_e32 v86, v38, v38
	v_fmac_f32_e32 v87, v40, v40
	v_add_f32_e32 v74, v74, v75
	v_add_f32_e32 v75, v76, v77
	v_add_f32_e32 v76, v86, v87
	s_waitcnt vmcnt(12)
	v_mul_f32_e32 v88, v35, v35
	v_mul_f32_e32 v89, v37, v37
	v_fmac_f32_e32 v88, v34, v34
	v_fmac_f32_e32 v89, v36, v36
	v_add_f32_e32 v77, v88, v89
	s_waitcnt vmcnt(11)
	v_mul_f32_e32 v90, v31, v31
	v_mul_f32_e32 v91, v33, v33
	s_waitcnt vmcnt(10)
	v_mul_f32_e32 v92, v23, v23
	v_mul_f32_e32 v93, v25, v25
	s_waitcnt vmcnt(7)
	v_mul_f32_e32 v98, v63, v63
	v_mul_f32_e32 v99, v65, v65
	s_waitcnt vmcnt(6)
	v_mul_f32_e32 v100, v55, v55
	v_mul_f32_e32 v101, v57, v57
	v_fmac_f32_e32 v90, v30, v30
	v_fmac_f32_e32 v91, v32, v32
	v_fmac_f32_e32 v92, v22, v22
	v_fmac_f32_e32 v93, v24, v24
	s_waitcnt vmcnt(5)
	v_mul_f32_e32 v102, v59, v59
	v_mul_f32_e32 v103, v61, v61
	v_fmac_f32_e32 v98, v62, v62
	v_fmac_f32_e32 v99, v64, v64
	v_fmac_f32_e32 v100, v54, v54
	v_fmac_f32_e32 v101, v56, v56
	s_waitcnt vmcnt(4)
	v_mul_f32_e32 v104, v51, v51
	v_add_f32_e32 v86, v90, v91
	v_add_f32_e32 v87, v92, v93
	v_fmac_f32_e32 v102, v58, v58
	v_fmac_f32_e32 v103, v60, v60
	v_add_f32_e32 v90, v98, v99
	v_add_f32_e32 v91, v100, v101
	v_mul_f32_e32 v93, v53, v53
	v_add_f32_e32 v92, v102, v103
	v_fmac_f32_e32 v104, v50, v50
	v_fmac_f32_e32 v93, v52, v52
	v_add_f32_e32 v90, v90, v91
	v_add_f32_e32 v93, v104, v93
	v_add_f32_e32 v90, v90, v92
	v_add_f32_e32 v90, v90, v93
	v_add_f32_e32 v74, v90, v74
	v_add_f32_e32 v74, v74, v75
	v_add_f32_e32 v74, v74, v76
	v_mul_f32_e32 v94, v15, v15
	v_mul_f32_e32 v95, v17, v17
	v_add_f32_e32 v74, v74, v77
	v_mul_f32_e32 v96, v7, v7
	v_mul_f32_e32 v97, v9, v9
	v_fmac_f32_e32 v94, v14, v14
	v_fmac_f32_e32 v95, v16, v16
	v_add_f32_e32 v74, v74, v86
	v_fmac_f32_e32 v96, v6, v6
	v_fmac_f32_e32 v97, v8, v8
	v_add_f32_e32 v88, v94, v95
	v_add_f32_e32 v74, v74, v87
	s_waitcnt vmcnt(3)
	v_mul_f32_e32 v75, v27, v27
	v_mul_f32_e32 v76, v29, v29
	v_add_f32_e32 v89, v96, v97
	v_add_f32_e32 v74, v74, v88
	v_fmac_f32_e32 v75, v26, v26
	v_fmac_f32_e32 v76, v28, v28
	v_add_f32_e32 v74, v74, v89
	v_add_f32_e32 v75, v75, v76
	v_add_f32_e32 v74, v74, v75
	s_waitcnt vmcnt(2)
	v_mul_f32_e32 v75, v19, v19
	v_mul_f32_e32 v76, v21, v21
	v_fmac_f32_e32 v75, v18, v18
	v_fmac_f32_e32 v76, v20, v20
	v_add_f32_e32 v75, v75, v76
	v_add_f32_e32 v74, v74, v75
	s_waitcnt vmcnt(1)
	v_mul_f32_e32 v75, v11, v11
	v_mul_f32_e32 v76, v13, v13
	v_fmac_f32_e32 v75, v10, v10
	v_fmac_f32_e32 v76, v12, v12
	v_add_f32_e32 v75, v75, v76
	v_add_f32_e32 v74, v74, v75
	s_waitcnt vmcnt(0)
	v_mul_f32_e32 v75, v3, v3
	v_mul_f32_e32 v76, v5, v5
	v_fmac_f32_e32 v75, v2, v2
	v_fmac_f32_e32 v76, v4, v4
	v_add_f32_e32 v75, v75, v76
	v_add_f32_e32 v74, v74, v75
	s_nop 1
	v_mov_b32_dpp v75, v74 quad_perm:[1,0,3,2] row_mask:0xf bank_mask:0xf
	s_waitcnt lgkmcnt(0)
	v_add_f32_e32 v74, v74, v75
	s_nop 1
	v_mov_b32_dpp v75, v74 quad_perm:[2,3,0,1] row_mask:0xf bank_mask:0xf
	s_waitcnt lgkmcnt(0)
	v_add_f32_e32 v74, v74, v75
	s_nop 1
	v_mov_b32_dpp v75, v74 row_half_mirror row_mask:0xf bank_mask:0xf
	s_nop 1
	v_mov_b32_dpp v75, v75 quad_perm:[3,2,1,0] row_mask:0xf bank_mask:0xf
	s_waitcnt lgkmcnt(0)
	v_add_f32_e32 v74, v74, v75
	s_nop 1
	v_mov_b32_dpp v75, v74 row_mirror row_mask:0xf bank_mask:0xf
	s_nop 1
	v_mov_b32_dpp v75, v75 row_half_mirror row_mask:0xf bank_mask:0xf
	s_waitcnt lgkmcnt(0)
	v_add_f32_e32 v74, v74, v75
	v_mov_b32_e32 v75, v74
	s_nop 1
	v_permlane16_swap_b32_e32 v74, v75
	s_waitcnt lgkmcnt(0)
	v_add_f32_e32 v74, v74, v75
	v_mov_b32_e32 v75, v74
	s_nop 1
	v_permlane32_swap_b32_e32 v74, v75
	s_and_saveexec_b64 s[12:13], s[0:1]
	s_cbranch_execz .LBB0_43
	s_add_u32 s26, s78, s14
	s_addc_u32 s27, s79, s15
	s_waitcnt lgkmcnt(0)
	v_add_f32_e32 v74, v74, v75
	global_store_dword v67, v74, s[26:27]
	s_branch .LBB0_43

;     __device__ __forceinline__ void operator()(const f32x4 (&acc)[2][2][4][2], const Unit& u, int wr, int wc, int fr, int fq) const {
;     ...
;         if (g == 1) {
; #pragma unroll
;             for (int bj = 0; bj < 2; ++bj)
; #pragma unroll
;                 for (int n = 0; n < 2; ++n)
; #pragma unroll
;                     for (int j = 0; j < 4; ++j) { float t = ksum[bj][n][j]; t += __shfl_xor(t, 1); t += __shfl_xor(t, 2); t += __shfl_xor(t, 4); t += __shfl_xor(t, 8);
;                         if (fr == 0) unsafeAtomicAdd(kmf + (((size_t)(b * 16 + (u.pn & 7) * 2 + bj) * 16 + (u.pm & 15)) * 128 + wc * 32 + 8 * fq + 4 * n + j), t); }
.LBB0_477:
	v_pk_add_f32 v[18:19], v[182:183], 0 op_sel_hi:[1,0]
	v_xor_b32_e32 v23, 8, v199
	v_pk_add_f32 v[18:19], v[18:19], v[142:143]
	s_and_b32 s14, s22, -16
	v_pk_add_f32 v[18:19], v[18:19], v[126:127]
	s_nop 0
	v_pk_add_f32 v[18:19], v[18:19], v[110:111]
	s_nop 0
	v_pk_add_f32 v[18:19], v[18:19], v[94:95]
	s_nop 0
	v_pk_add_f32 v[18:19], v[18:19], v[78:79]
	s_nop 0
	v_pk_add_f32 v[18:19], v[18:19], v[62:63]
	s_nop 0
	v_pk_add_f32 v[14:15], v[18:19], v[14:15]
	v_and_b32_e32 v19, 64, v199
	v_xor_b32_e32 v18, 1, v199
	v_add_u32_e32 v21, 64, v19
	v_cmp_lt_i32_e32 vcc, v18, v21
	v_cndmask_b32_e64 v14, 0, v14, s[10:11]
	v_xor_b32_e32 v19, 2, v199
	v_cndmask_b32_e32 v18, v199, v18, vcc
	v_lshlrev_b32_e32 v18, 2, v18
	s_nop 1
	v_mov_b32_dpp v20, v14 quad_perm:[1,0,3,2] row_mask:0xf bank_mask:0xf
	v_cmp_lt_i32_e32 vcc, v19, v21
	s_waitcnt lgkmcnt(0)
	v_add_f32_e32 v14, v14, v20
	v_cndmask_b32_e32 v19, v199, v19, vcc
	v_lshlrev_b32_e32 v19, 2, v19
	s_nop 1
	v_mov_b32_dpp v22, v14 quad_perm:[2,3,0,1] row_mask:0xf bank_mask:0xf
	v_xor_b32_e32 v20, 4, v199
	v_cmp_lt_i32_e32 vcc, v20, v21
	s_waitcnt lgkmcnt(0)
	v_add_f32_e32 v14, v14, v22
	v_cndmask_b32_e32 v20, v199, v20, vcc
	v_lshlrev_b32_e32 v20, 2, v20
	s_nop 1
	v_mov_b32_dpp v22, v14 row_half_mirror row_mask:0xf bank_mask:0xf
	s_nop 1
	v_mov_b32_dpp v22, v22 quad_perm:[3,2,1,0] row_mask:0xf bank_mask:0xf
	v_cmp_lt_i32_e32 vcc, v23, v21
	s_waitcnt lgkmcnt(0)
	v_add_f32_e32 v22, v14, v22
	v_cndmask_b32_e32 v21, v199, v23, vcc
	v_lshlrev_b32_e32 v21, 2, v21
	s_nop 1
	v_mov_b32_dpp v23, v22 row_mirror row_mask:0xf bank_mask:0xf
	s_nop 1
	v_mov_b32_dpp v23, v23 row_half_mirror row_mask:0xf bank_mask:0xf
	v_lshlrev_b32_e32 v14, 2, v154
	s_and_saveexec_b64 s[12:13], s[6:7]
	s_cbranch_execz .LBB0_479
	s_lshl_b32 s15, s26, 1
	s_and_b32 s15, s15, 14
	s_or_b32 s16, s15, s14
	s_ashr_i32 s17, s16, 31
	s_lshl_b64 s[16:17], s[16:17], 13
	v_readlane_b32 s15, v253, 48
	s_add_u32 s15, s15, s16
	v_readlane_b32 s16, v253, 49
	s_addc_u32 s16, s16, s17
	s_lshl_b32 s17, s22, 9
	s_and_b32 s17, s17, 0x1e00
	s_add_u32 s15, s15, s17
	s_addc_u32 s17, s16, 0
	s_lshl_b32 s16, s34, 2
	s_add_u32 s16, s15, s16
	s_waitcnt lgkmcnt(0)
	v_add_f32_e32 v22, v22, v23
	s_addc_u32 s17, s17, 0
	global_atomic_add_f32 v14, v22, s[16:17]
.LBB0_479:
	s_or_b64 exec, exec, s[12:13]
	v_cndmask_b32_e64 v15, 0, v15, s[10:11]
	s_nop 1
	v_mov_b32_dpp v22, v15 quad_perm:[1,0,3,2] row_mask:0xf bank_mask:0xf
	s_waitcnt lgkmcnt(0)
	v_add_f32_e32 v15, v15, v22
	s_nop 1
	v_mov_b32_dpp v24, v15 quad_perm:[2,3,0,1] row_mask:0xf bank_mask:0xf
	v_pk_add_f32 v[22:23], v[178:179], 0 op_sel_hi:[1,0]
	s_waitcnt lgkmcnt(0)
	v_add_f32_e32 v15, v15, v24
	s_nop 1
	v_mov_b32_dpp v26, v15 row_half_mirror row_mask:0xf bank_mask:0xf
	s_nop 1
	v_mov_b32_dpp v26, v26 quad_perm:[3,2,1,0] row_mask:0xf bank_mask:0xf
	v_pk_add_f32 v[22:23], v[22:23], v[138:139]
	s_nop 0
	v_pk_add_f32 v[22:23], v[22:23], v[122:123]
	s_nop 0
	v_pk_add_f32 v[22:23], v[22:23], v[106:107]
	s_nop 0
	v_pk_add_f32 v[22:23], v[22:23], v[90:91]
	s_nop 0
	v_pk_add_f32 v[24:25], v[22:23], v[74:75]
	s_waitcnt lgkmcnt(0)
	v_add_f32_e32 v22, v15, v26
	s_nop 1
	v_mov_b32_dpp v23, v22 row_mirror row_mask:0xf bank_mask:0xf
	s_nop 1
	v_mov_b32_dpp v23, v23 row_half_mirror row_mask:0xf bank_mask:0xf
	v_pk_add_f32 v[24:25], v[24:25], v[58:59]
	s_nop 0
	v_pk_add_f32 v[16:17], v[24:25], v[16:17]
	s_nop 0
	v_cndmask_b32_e64 v15, 0, v17, s[10:11]
	v_cndmask_b32_e64 v16, 0, v16, s[10:11]
	s_and_saveexec_b64 s[12:13], s[6:7]
	s_cbranch_execz .LBB0_481
	s_lshl_b32 s15, s26, 1
	s_and_b32 s15, s15, 14
	s_or_b32 s16, s15, s14
	s_ashr_i32 s17, s16, 31
	s_lshl_b64 s[16:17], s[16:17], 13
	v_readlane_b32 s15, v253, 48
	s_add_u32 s15, s15, s16
	v_readlane_b32 s16, v253, 49
	s_addc_u32 s16, s16, s17
	s_lshl_b32 s17, s22, 9
	s_and_b32 s17, s17, 0x1e00
	s_add_u32 s15, s15, s17
	s_addc_u32 s17, s16, 0
	s_lshl_b32 s16, s34, 2
	s_add_u32 s16, s15, s16
	s_waitcnt lgkmcnt(0)
	v_add_f32_e32 v17, v22, v23
	s_addc_u32 s17, s17, 0
	global_atomic_add_f32 v14, v17, s[16:17] offset:4
.LBB0_481:
	s_or_b64 exec, exec, s[12:13]
	s_nop 1
	v_mov_b32_dpp v17, v16 quad_perm:[1,0,3,2] row_mask:0xf bank_mask:0xf
	s_waitcnt lgkmcnt(0)
	v_add_f32_e32 v16, v16, v17
	s_nop 1
	v_mov_b32_dpp v17, v16 quad_perm:[2,3,0,1] row_mask:0xf bank_mask:0xf
	s_waitcnt lgkmcnt(0)
	v_add_f32_e32 v16, v16, v17
	s_nop 1
	v_mov_b32_dpp v17, v16 row_half_mirror row_mask:0xf bank_mask:0xf
	s_nop 1
	v_mov_b32_dpp v17, v17 quad_perm:[3,2,1,0] row_mask:0xf bank_mask:0xf
	s_waitcnt lgkmcnt(0)
	v_add_f32_e32 v16, v16, v17
	s_nop 1
	v_mov_b32_dpp v17, v16 row_mirror row_mask:0xf bank_mask:0xf
	s_nop 1
	v_mov_b32_dpp v17, v17 row_half_mirror row_mask:0xf bank_mask:0xf
	s_and_saveexec_b64 s[12:13], s[6:7]
	s_cbranch_execz .LBB0_483
	s_lshl_b32 s15, s26, 1
	s_and_b32 s15, s15, 14
	s_or_b32 s16, s15, s14
	s_ashr_i32 s17, s16, 31
	s_lshl_b64 s[16:17], s[16:17], 13
	v_readlane_b32 s15, v253, 48
	s_add_u32 s15, s15, s16
	v_readlane_b32 s16, v253, 49
	s_addc_u32 s16, s16, s17
	s_lshl_b32 s17, s22, 9
	s_and_b32 s17, s17, 0x1e00
	s_add_u32 s15, s15, s17
	s_addc_u32 s17, s16, 0
	s_lshl_b32 s16, s34, 2
	s_add_u32 s16, s15, s16
	s_waitcnt lgkmcnt(0)
	v_add_f32_e32 v16, v16, v17
	s_addc_u32 s17, s17, 0
	global_atomic_add_f32 v14, v16, s[16:17] offset:8
;     __device__ __forceinline__ void operator()(const f32x4 (&acc)[2][2][4][2], const Unit& u, int wr, int wc, int fr, int fq) const {
;     ...
;         if (g == 1) {
; #pragma unroll
;             for (int bj = 0; bj < 2; ++bj)
; #pragma unroll
;                 for (int n = 0; n < 2; ++n)
; #pragma unroll
;                     for (int j = 0; j < 4; ++j) { float t = ksum[bj][n][j]; t += __shfl_xor(t, 1); t += __shfl_xor(t, 2); t += __shfl_xor(t, 4); t += __shfl_xor(t, 8);
;                         if (fr == 0) unsafeAtomicAdd(kmf + (((size_t)(b * 16 + (u.pn & 7) * 2 + bj) * 16 + (u.pm & 15)) * 128 + wc * 32 + 8 * fq + 4 * n + j), t); }
.LBB0_483:
	s_or_b64 exec, exec, s[12:13]
	s_nop 1
	v_mov_b32_dpp v16, v15 quad_perm:[1,0,3,2] row_mask:0xf bank_mask:0xf
	s_waitcnt lgkmcnt(0)
	v_add_f32_e32 v15, v15, v16
	s_nop 1
	v_mov_b32_dpp v16, v15 quad_perm:[2,3,0,1] row_mask:0xf bank_mask:0xf
	s_waitcnt lgkmcnt(0)
	v_add_f32_e32 v15, v15, v16
	s_nop 1
	v_mov_b32_dpp v16, v15 row_half_mirror row_mask:0xf bank_mask:0xf
	s_nop 1
	v_mov_b32_dpp v16, v16 quad_perm:[3,2,1,0] row_mask:0xf bank_mask:0xf
	s_waitcnt lgkmcnt(0)
	v_add_f32_e32 v15, v15, v16
	s_nop 1
	v_mov_b32_dpp v16, v15 row_mirror row_mask:0xf bank_mask:0xf
	s_nop 1
	v_mov_b32_dpp v16, v16 row_half_mirror row_mask:0xf bank_mask:0xf
	s_and_saveexec_b64 s[12:13], s[6:7]
	s_cbranch_execz .LBB0_485
	s_lshl_b32 s15, s26, 1
	s_and_b32 s15, s15, 14
	s_or_b32 s16, s15, s14
	s_ashr_i32 s17, s16, 31
	s_lshl_b64 s[16:17], s[16:17], 13
	v_readlane_b32 s15, v253, 48
	s_add_u32 s15, s15, s16
	v_readlane_b32 s16, v253, 49
	s_addc_u32 s16, s16, s17
	s_lshl_b32 s17, s22, 9
	s_and_b32 s17, s17, 0x1e00
	s_add_u32 s15, s15, s17
	s_addc_u32 s17, s16, 0
	s_lshl_b32 s16, s34, 2
	s_add_u32 s16, s15, s16
	s_waitcnt lgkmcnt(0)
	v_add_f32_e32 v15, v15, v16
	s_addc_u32 s17, s17, 0
	global_atomic_add_f32 v14, v15, s[16:17] offset:12
.LBB0_485:
	s_or_b64 exec, exec, s[12:13]
	s_waitcnt lgkmcnt(0)
	v_pk_add_f32 v[16:17], v[174:175], 0 op_sel_hi:[1,0]
	s_nop 0
	v_pk_add_f32 v[16:17], v[16:17], v[134:135]
	s_nop 0
	v_pk_add_f32 v[16:17], v[16:17], v[118:119]
	s_nop 0
	v_pk_add_f32 v[16:17], v[16:17], v[102:103]
	s_nop 0
	v_pk_add_f32 v[16:17], v[16:17], v[86:87]
	s_nop 0
	v_pk_add_f32 v[16:17], v[16:17], v[70:71]
	s_nop 0
	v_pk_add_f32 v[16:17], v[16:17], v[54:55]
	s_nop 0
	v_pk_add_f32 v[10:11], v[16:17], v[10:11]
	s_nop 0
	v_cndmask_b32_e64 v10, 0, v10, s[10:11]
	s_nop 1
	v_mov_b32_dpp v15, v10 quad_perm:[1,0,3,2] row_mask:0xf bank_mask:0xf
	s_waitcnt lgkmcnt(0)
	v_add_f32_e32 v10, v10, v15
	s_nop 1
	v_mov_b32_dpp v15, v10 quad_perm:[2,3,0,1] row_mask:0xf bank_mask:0xf
	s_waitcnt lgkmcnt(0)
	v_add_f32_e32 v10, v10, v15
	s_nop 1
	v_mov_b32_dpp v15, v10 row_half_mirror row_mask:0xf bank_mask:0xf
	s_nop 1
	v_mov_b32_dpp v15, v15 quad_perm:[3,2,1,0] row_mask:0xf bank_mask:0xf
	s_waitcnt lgkmcnt(0)
	v_add_f32_e32 v10, v10, v15
	s_nop 1
	v_mov_b32_dpp v15, v10 row_mirror row_mask:0xf bank_mask:0xf
	s_nop 1
	v_mov_b32_dpp v15, v15 row_half_mirror row_mask:0xf bank_mask:0xf
	s_and_saveexec_b64 s[12:13], s[6:7]
	s_cbranch_execz .LBB0_487
	s_lshl_b32 s15, s26, 1
	s_and_b32 s15, s15, 14
	s_or_b32 s16, s15, s14
	s_ashr_i32 s17, s16, 31
	s_lshl_b64 s[16:17], s[16:17], 13
	v_readlane_b32 s15, v253, 48
	s_add_u32 s15, s15, s16
	v_readlane_b32 s16, v253, 49
	s_addc_u32 s16, s16, s17
	s_lshl_b32 s17, s22, 9
	s_and_b32 s17, s17, 0x1e00
	s_add_u32 s15, s15, s17
	s_addc_u32 s17, s16, 0
	s_lshl_b32 s16, s34, 2
	s_add_u32 s16, s15, s16
	s_waitcnt lgkmcnt(0)
	v_add_f32_e32 v10, v10, v15
	s_addc_u32 s17, s17, 0
	global_atomic_add_f32 v14, v10, s[16:17] offset:16
.LBB0_487:
	s_or_b64 exec, exec, s[12:13]
	v_cndmask_b32_e64 v10, 0, v11, s[10:11]
	s_nop 1
	v_mov_b32_dpp v11, v10 quad_perm:[1,0,3,2] row_mask:0xf bank_mask:0xf
	s_waitcnt lgkmcnt(0)
	v_add_f32_e32 v15, v10, v11
	s_nop 1
	v_mov_b32_dpp v16, v15 quad_perm:[2,3,0,1] row_mask:0xf bank_mask:0xf
	v_pk_add_f32 v[10:11], v[170:171], 0 op_sel_hi:[1,0]
	s_waitcnt lgkmcnt(0)
	v_add_f32_e32 v15, v15, v16
	s_nop 1
	v_mov_b32_dpp v16, v15 row_half_mirror row_mask:0xf bank_mask:0xf
	s_nop 1
	v_mov_b32_dpp v16, v16 quad_perm:[3,2,1,0] row_mask:0xf bank_mask:0xf
	v_pk_add_f32 v[10:11], v[10:11], v[130:131]
	s_waitcnt lgkmcnt(0)
	v_add_f32_e32 v15, v15, v16
	v_pk_add_f32 v[10:11], v[10:11], v[114:115]
	s_nop 1
	v_mov_b32_dpp v16, v15 row_mirror row_mask:0xf bank_mask:0xf
	s_nop 1
	v_mov_b32_dpp v16, v16 row_half_mirror row_mask:0xf bank_mask:0xf
	v_pk_add_f32 v[10:11], v[10:11], v[98:99]
	s_nop 0
	v_pk_add_f32 v[10:11], v[10:11], v[82:83]
	s_nop 0
	v_pk_add_f32 v[10:11], v[10:11], v[66:67]
	s_nop 0
	v_pk_add_f32 v[10:11], v[10:11], v[50:51]
	s_nop 0
	v_pk_add_f32 v[12:13], v[10:11], v[12:13]
	s_nop 0
	v_cndmask_b32_e64 v10, 0, v13, s[10:11]
	v_cndmask_b32_e64 v11, 0, v12, s[10:11]
	s_and_saveexec_b64 s[12:13], s[6:7]
	s_cbranch_execz .LBB0_489
	s_lshl_b32 s15, s26, 1
	s_and_b32 s15, s15, 14
	s_or_b32 s16, s15, s14
	s_ashr_i32 s17, s16, 31
	s_lshl_b64 s[16:17], s[16:17], 13
	v_readlane_b32 s15, v253, 48
	s_add_u32 s15, s15, s16
	v_readlane_b32 s16, v253, 49
	s_addc_u32 s16, s16, s17
	s_lshl_b32 s17, s22, 9
	s_and_b32 s17, s17, 0x1e00
	s_add_u32 s15, s15, s17
	s_addc_u32 s17, s16, 0
	s_lshl_b32 s16, s34, 2
	s_add_u32 s16, s15, s16
	s_waitcnt lgkmcnt(0)
	v_add_f32_e32 v12, v15, v16
	s_addc_u32 s17, s17, 0
	global_atomic_add_f32 v14, v12, s[16:17] offset:20
.LBB0_489:
	s_or_b64 exec, exec, s[12:13]
	s_nop 1
	v_mov_b32_dpp v12, v11 quad_perm:[1,0,3,2] row_mask:0xf bank_mask:0xf
	s_waitcnt lgkmcnt(0)
	v_add_f32_e32 v11, v11, v12
	s_nop 1
	v_mov_b32_dpp v12, v11 quad_perm:[2,3,0,1] row_mask:0xf bank_mask:0xf
	s_waitcnt lgkmcnt(0)
	v_add_f32_e32 v11, v11, v12
	s_nop 1
	v_mov_b32_dpp v12, v11 row_half_mirror row_mask:0xf bank_mask:0xf
	s_nop 1
	v_mov_b32_dpp v12, v12 quad_perm:[3,2,1,0] row_mask:0xf bank_mask:0xf
	s_waitcnt lgkmcnt(0)
	v_add_f32_e32 v11, v11, v12
	s_nop 1
	v_mov_b32_dpp v12, v11 row_mirror row_mask:0xf bank_mask:0xf
	s_nop 1
	v_mov_b32_dpp v12, v12 row_half_mirror row_mask:0xf bank_mask:0xf
	s_and_saveexec_b64 s[12:13], s[6:7]
	s_cbranch_execz .LBB0_491
	s_lshl_b32 s15, s26, 1
	s_and_b32 s15, s15, 14
	s_or_b32 s16, s15, s14
	s_ashr_i32 s17, s16, 31
	s_lshl_b64 s[16:17], s[16:17], 13
	v_readlane_b32 s15, v253, 48
	s_add_u32 s15, s15, s16
	v_readlane_b32 s16, v253, 49
	s_addc_u32 s16, s16, s17
	s_lshl_b32 s17, s22, 9
	s_and_b32 s17, s17, 0x1e00
	s_add_u32 s15, s15, s17
	s_addc_u32 s17, s16, 0
	s_lshl_b32 s16, s34, 2
	s_add_u32 s16, s15, s16
	s_waitcnt lgkmcnt(0)
	v_add_f32_e32 v11, v11, v12
	s_addc_u32 s17, s17, 0
	global_atomic_add_f32 v14, v11, s[16:17] offset:24
;     __device__ __forceinline__ void operator()(const f32x4 (&acc)[2][2][4][2], const Unit& u, int wr, int wc, int fr, int fq) const {
;     ...
;         if (g == 1) {
; #pragma unroll
;             for (int bj = 0; bj < 2; ++bj)
; #pragma unroll
;                 for (int n = 0; n < 2; ++n)
; #pragma unroll
;                     for (int j = 0; j < 4; ++j) { float t = ksum[bj][n][j]; t += __shfl_xor(t, 1); t += __shfl_xor(t, 2); t += __shfl_xor(t, 4); t += __shfl_xor(t, 8);
;                         if (fr == 0) unsafeAtomicAdd(kmf + (((size_t)(b * 16 + (u.pn & 7) * 2 + bj) * 16 + (u.pm & 15)) * 128 + wc * 32 + 8 * fq + 4 * n + j), t); }
.LBB0_491:
	s_or_b64 exec, exec, s[12:13]
	s_nop 1
	v_mov_b32_dpp v11, v10 quad_perm:[1,0,3,2] row_mask:0xf bank_mask:0xf
	s_waitcnt lgkmcnt(0)
	v_add_f32_e32 v10, v10, v11
	s_nop 1
	v_mov_b32_dpp v11, v10 quad_perm:[2,3,0,1] row_mask:0xf bank_mask:0xf
	s_waitcnt lgkmcnt(0)
	v_add_f32_e32 v10, v10, v11
	s_nop 1
	v_mov_b32_dpp v11, v10 row_half_mirror row_mask:0xf bank_mask:0xf
	s_nop 1
	v_mov_b32_dpp v11, v11 quad_perm:[3,2,1,0] row_mask:0xf bank_mask:0xf
	s_waitcnt lgkmcnt(0)
	v_add_f32_e32 v10, v10, v11
	s_nop 1
	v_mov_b32_dpp v11, v10 row_mirror row_mask:0xf bank_mask:0xf
	s_nop 1
	v_mov_b32_dpp v11, v11 row_half_mirror row_mask:0xf bank_mask:0xf
	s_and_saveexec_b64 s[12:13], s[6:7]
	s_cbranch_execz .LBB0_493
	s_lshl_b32 s15, s26, 1
	s_and_b32 s15, s15, 14
	s_or_b32 s16, s15, s14
	s_ashr_i32 s17, s16, 31
	s_lshl_b64 s[16:17], s[16:17], 13
	v_readlane_b32 s15, v253, 48
	s_add_u32 s15, s15, s16
	v_readlane_b32 s16, v253, 49
	s_addc_u32 s16, s16, s17
	s_lshl_b32 s17, s22, 9
	s_and_b32 s17, s17, 0x1e00
	s_add_u32 s15, s15, s17
	s_addc_u32 s17, s16, 0
	s_lshl_b32 s16, s34, 2
	s_add_u32 s16, s15, s16
	s_waitcnt lgkmcnt(0)
	v_add_f32_e32 v10, v10, v11
	s_addc_u32 s17, s17, 0
	global_atomic_add_f32 v14, v10, s[16:17] offset:28
.LBB0_493:
	s_or_b64 exec, exec, s[12:13]
	s_waitcnt lgkmcnt(0)
	v_pk_add_f32 v[10:11], v[184:185], 0 op_sel_hi:[1,0]
	s_nop 0
	v_pk_add_f32 v[10:11], v[10:11], v[144:145]
	s_nop 0
	v_pk_add_f32 v[10:11], v[10:11], v[128:129]
	s_nop 0
	v_pk_add_f32 v[10:11], v[10:11], v[112:113]
	s_nop 0
	v_pk_add_f32 v[10:11], v[10:11], v[96:97]
	s_nop 0
	v_pk_add_f32 v[10:11], v[10:11], v[80:81]
	s_nop 0
	v_pk_add_f32 v[10:11], v[10:11], v[64:65]
	s_nop 0
	v_pk_add_f32 v[6:7], v[10:11], v[6:7]
	s_nop 0
	v_cndmask_b32_e64 v6, 0, v6, s[10:11]
	s_nop 1
	v_mov_b32_dpp v10, v6 quad_perm:[1,0,3,2] row_mask:0xf bank_mask:0xf
	s_waitcnt lgkmcnt(0)
	v_add_f32_e32 v6, v6, v10
	s_nop 1
	v_mov_b32_dpp v10, v6 quad_perm:[2,3,0,1] row_mask:0xf bank_mask:0xf
	s_waitcnt lgkmcnt(0)
	v_add_f32_e32 v6, v6, v10
	s_nop 1
	v_mov_b32_dpp v10, v6 row_half_mirror row_mask:0xf bank_mask:0xf
	s_nop 1
	v_mov_b32_dpp v10, v10 quad_perm:[3,2,1,0] row_mask:0xf bank_mask:0xf
	s_waitcnt lgkmcnt(0)
	v_add_f32_e32 v6, v6, v10
	s_nop 1
	v_mov_b32_dpp v10, v6 row_mirror row_mask:0xf bank_mask:0xf
	s_nop 1
	v_mov_b32_dpp v10, v10 row_half_mirror row_mask:0xf bank_mask:0xf
	s_and_saveexec_b64 s[12:13], s[6:7]
	s_cbranch_execz .LBB0_495
	s_lshl_b32 s15, s26, 1
	s_and_b32 s15, s15, 14
	s_or_b32 s15, s14, s15
	s_or_b32 s16, s15, 1
	s_ashr_i32 s17, s16, 31
	s_lshl_b64 s[16:17], s[16:17], 13
	v_readlane_b32 s15, v253, 48
	s_add_u32 s15, s15, s16
	v_readlane_b32 s16, v253, 49
	s_addc_u32 s16, s16, s17
	s_lshl_b32 s17, s22, 9
	s_and_b32 s17, s17, 0x1e00
	s_add_u32 s15, s15, s17
	s_addc_u32 s17, s16, 0
	s_lshl_b32 s16, s34, 2
	s_add_u32 s16, s15, s16
	s_waitcnt lgkmcnt(0)
	v_add_f32_e32 v6, v6, v10
	s_addc_u32 s17, s17, 0
	global_atomic_add_f32 v14, v6, s[16:17]
.LBB0_495:
	s_or_b64 exec, exec, s[12:13]
	v_cndmask_b32_e64 v6, 0, v7, s[10:11]
	s_nop 1
	v_mov_b32_dpp v7, v6 quad_perm:[1,0,3,2] row_mask:0xf bank_mask:0xf
	s_waitcnt lgkmcnt(0)
	v_add_f32_e32 v10, v6, v7
	s_nop 1
	v_mov_b32_dpp v11, v10 quad_perm:[2,3,0,1] row_mask:0xf bank_mask:0xf
	v_pk_add_f32 v[6:7], v[180:181], 0 op_sel_hi:[1,0]
	s_waitcnt lgkmcnt(0)
	v_add_f32_e32 v10, v10, v11
	s_nop 1
	v_mov_b32_dpp v11, v10 row_half_mirror row_mask:0xf bank_mask:0xf
	s_nop 1
	v_mov_b32_dpp v11, v11 quad_perm:[3,2,1,0] row_mask:0xf bank_mask:0xf
	v_pk_add_f32 v[6:7], v[6:7], v[140:141]
	s_waitcnt lgkmcnt(0)
	v_add_f32_e32 v10, v10, v11
	v_pk_add_f32 v[6:7], v[6:7], v[124:125]
	s_nop 1
	v_mov_b32_dpp v11, v10 row_mirror row_mask:0xf bank_mask:0xf
	s_nop 1
	v_mov_b32_dpp v11, v11 row_half_mirror row_mask:0xf bank_mask:0xf
	v_pk_add_f32 v[6:7], v[6:7], v[108:109]
	s_nop 0
	v_pk_add_f32 v[6:7], v[6:7], v[92:93]
	s_nop 0
	v_pk_add_f32 v[6:7], v[6:7], v[76:77]
	s_nop 0
	v_pk_add_f32 v[6:7], v[6:7], v[60:61]
	s_nop 0
	v_pk_add_f32 v[8:9], v[6:7], v[8:9]
	s_nop 0
	v_cndmask_b32_e64 v6, 0, v9, s[10:11]
	v_cndmask_b32_e64 v7, 0, v8, s[10:11]
	s_and_saveexec_b64 s[12:13], s[6:7]
	s_cbranch_execz .LBB0_497
	s_lshl_b32 s15, s26, 1
	s_and_b32 s15, s15, 14
	s_or_b32 s15, s14, s15
	s_or_b32 s16, s15, 1
	s_ashr_i32 s17, s16, 31
	s_lshl_b64 s[16:17], s[16:17], 13
	v_readlane_b32 s15, v253, 48
	s_add_u32 s15, s15, s16
	v_readlane_b32 s16, v253, 49
	s_addc_u32 s16, s16, s17
	s_lshl_b32 s17, s22, 9
	s_and_b32 s17, s17, 0x1e00
	s_add_u32 s15, s15, s17
	s_addc_u32 s17, s16, 0
	s_lshl_b32 s16, s34, 2
	s_add_u32 s16, s15, s16
	s_waitcnt lgkmcnt(0)
	v_add_f32_e32 v8, v10, v11
	s_addc_u32 s17, s17, 0
	global_atomic_add_f32 v14, v8, s[16:17] offset:4
.LBB0_497:
	s_or_b64 exec, exec, s[12:13]
	s_nop 1
	v_mov_b32_dpp v8, v7 quad_perm:[1,0,3,2] row_mask:0xf bank_mask:0xf
	s_waitcnt lgkmcnt(0)
	v_add_f32_e32 v7, v7, v8
	s_nop 1
	v_mov_b32_dpp v8, v7 quad_perm:[2,3,0,1] row_mask:0xf bank_mask:0xf
	s_waitcnt lgkmcnt(0)
	v_add_f32_e32 v7, v7, v8
	s_nop 1
	v_mov_b32_dpp v8, v7 row_half_mirror row_mask:0xf bank_mask:0xf
	s_nop 1
	v_mov_b32_dpp v8, v8 quad_perm:[3,2,1,0] row_mask:0xf bank_mask:0xf
	s_waitcnt lgkmcnt(0)
	v_add_f32_e32 v7, v7, v8
	s_nop 1
	v_mov_b32_dpp v8, v7 row_mirror row_mask:0xf bank_mask:0xf
	s_nop 1
	v_mov_b32_dpp v8, v8 row_half_mirror row_mask:0xf bank_mask:0xf
	s_and_saveexec_b64 s[12:13], s[6:7]
	s_cbranch_execz .LBB0_499
	s_lshl_b32 s15, s26, 1
	s_and_b32 s15, s15, 14
	s_or_b32 s15, s14, s15
	s_or_b32 s16, s15, 1
	s_ashr_i32 s17, s16, 31
	s_lshl_b64 s[16:17], s[16:17], 13
	v_readlane_b32 s15, v253, 48
	s_add_u32 s15, s15, s16
	v_readlane_b32 s16, v253, 49
	s_addc_u32 s16, s16, s17
	s_lshl_b32 s17, s22, 9
	s_and_b32 s17, s17, 0x1e00
	s_add_u32 s15, s15, s17
	s_addc_u32 s17, s16, 0
	s_lshl_b32 s16, s34, 2
	s_add_u32 s16, s15, s16
	s_waitcnt lgkmcnt(0)
	v_add_f32_e32 v7, v7, v8
	s_addc_u32 s17, s17, 0
	global_atomic_add_f32 v14, v7, s[16:17] offset:8
;     __device__ __forceinline__ void operator()(const f32x4 (&acc)[2][2][4][2], const Unit& u, int wr, int wc, int fr, int fq) const {
;     ...
;                     if (g == 1) { ksum[bj][0] += v0; ksum[bj][1] += v1; }
;                 }
;             }
;         if (g == 1) {
; #pragma unroll
;             for (int bj = 0; bj < 2; ++bj)
; #pragma unroll
;                 for (int n = 0; n < 2; ++n)
; #pragma unroll
;                     for (int j = 0; j < 4; ++j) { float t = ksum[bj][n][j]; t += __shfl_xor(t, 1); t += __shfl_xor(t, 2); t += __shfl_xor(t, 4); t += __shfl_xor(t, 8);
;                         if (fr == 0) unsafeAtomicAdd(kmf + (((size_t)(b * 16 + (u.pn & 7) * 2 + bj) * 16 + (u.pm & 15)) * 128 + wc * 32 + 8 * fq + 4 * n + j), t); }
.LBB0_499:
	s_or_b64 exec, exec, s[12:13]
	s_nop 1
	v_mov_b32_dpp v7, v6 quad_perm:[1,0,3,2] row_mask:0xf bank_mask:0xf
	s_waitcnt lgkmcnt(0)
	v_add_f32_e32 v6, v6, v7
	s_nop 1
	v_mov_b32_dpp v7, v6 quad_perm:[2,3,0,1] row_mask:0xf bank_mask:0xf
	s_waitcnt lgkmcnt(0)
	v_add_f32_e32 v6, v6, v7
	s_nop 1
	v_mov_b32_dpp v7, v6 row_half_mirror row_mask:0xf bank_mask:0xf
	s_nop 1
	v_mov_b32_dpp v7, v7 quad_perm:[3,2,1,0] row_mask:0xf bank_mask:0xf
	s_waitcnt lgkmcnt(0)
	v_add_f32_e32 v6, v6, v7
	s_nop 1
	v_mov_b32_dpp v7, v6 row_mirror row_mask:0xf bank_mask:0xf
	s_nop 1
	v_mov_b32_dpp v7, v7 row_half_mirror row_mask:0xf bank_mask:0xf
	s_and_saveexec_b64 s[12:13], s[6:7]
	s_cbranch_execz .LBB0_501
	s_lshl_b32 s15, s26, 1
	s_and_b32 s15, s15, 14
	s_or_b32 s15, s14, s15
	s_or_b32 s16, s15, 1
	s_ashr_i32 s17, s16, 31
	s_lshl_b64 s[16:17], s[16:17], 13
	v_readlane_b32 s15, v253, 48
	s_add_u32 s15, s15, s16
	v_readlane_b32 s16, v253, 49
	s_addc_u32 s16, s16, s17
	s_lshl_b32 s17, s22, 9
	s_and_b32 s17, s17, 0x1e00
	s_add_u32 s15, s15, s17
	s_addc_u32 s17, s16, 0
	s_lshl_b32 s16, s34, 2
	s_add_u32 s16, s15, s16
	s_waitcnt lgkmcnt(0)
	v_add_f32_e32 v6, v6, v7
	s_addc_u32 s17, s17, 0
	global_atomic_add_f32 v14, v6, s[16:17] offset:12
.LBB0_501:
	s_or_b64 exec, exec, s[12:13]
	s_waitcnt lgkmcnt(0)
	v_pk_add_f32 v[6:7], v[176:177], 0 op_sel_hi:[1,0]
	s_nop 0
	v_pk_add_f32 v[6:7], v[6:7], v[136:137]
	s_nop 0
	v_pk_add_f32 v[6:7], v[6:7], v[120:121]
	s_nop 0
	v_pk_add_f32 v[6:7], v[6:7], v[104:105]
	s_nop 0
	v_pk_add_f32 v[6:7], v[6:7], v[88:89]
	s_nop 0
	v_pk_add_f32 v[6:7], v[6:7], v[72:73]
	s_nop 0
	v_pk_add_f32 v[6:7], v[6:7], v[56:57]
	s_nop 0
	v_pk_add_f32 v[2:3], v[6:7], v[2:3]
	s_nop 0
	v_cndmask_b32_e64 v2, 0, v2, s[10:11]
	s_nop 1
	v_mov_b32_dpp v6, v2 quad_perm:[1,0,3,2] row_mask:0xf bank_mask:0xf
	s_waitcnt lgkmcnt(0)
	v_add_f32_e32 v2, v2, v6
	s_nop 1
	v_mov_b32_dpp v6, v2 quad_perm:[2,3,0,1] row_mask:0xf bank_mask:0xf
	s_waitcnt lgkmcnt(0)
	v_add_f32_e32 v2, v2, v6
	s_nop 1
	v_mov_b32_dpp v6, v2 row_half_mirror row_mask:0xf bank_mask:0xf
	s_nop 1
	v_mov_b32_dpp v6, v6 quad_perm:[3,2,1,0] row_mask:0xf bank_mask:0xf
	s_waitcnt lgkmcnt(0)
	v_add_f32_e32 v2, v2, v6
	s_nop 1
	v_mov_b32_dpp v6, v2 row_mirror row_mask:0xf bank_mask:0xf
	s_nop 1
	v_mov_b32_dpp v6, v6 row_half_mirror row_mask:0xf bank_mask:0xf
	s_and_saveexec_b64 s[12:13], s[6:7]
	s_cbranch_execz .LBB0_503
	s_lshl_b32 s15, s26, 1
	s_and_b32 s15, s15, 14
	s_or_b32 s15, s14, s15
	s_or_b32 s16, s15, 1
	s_ashr_i32 s17, s16, 31
	s_lshl_b64 s[16:17], s[16:17], 13
	v_readlane_b32 s15, v253, 48
	s_add_u32 s15, s15, s16
	v_readlane_b32 s16, v253, 49
	s_addc_u32 s16, s16, s17
	s_lshl_b32 s17, s22, 9
	s_and_b32 s17, s17, 0x1e00
	s_add_u32 s15, s15, s17
	s_addc_u32 s17, s16, 0
	s_lshl_b32 s16, s34, 2
	s_add_u32 s16, s15, s16
	s_waitcnt lgkmcnt(0)
	v_add_f32_e32 v2, v2, v6
	s_addc_u32 s17, s17, 0
	global_atomic_add_f32 v14, v2, s[16:17] offset:16
;     __device__ __forceinline__ void operator()(const f32x4 (&acc)[2][2][4][2], const Unit& u, int wr, int wc, int fr, int fq) const {
;     ...
;                     if (g == 1) { ksum[bj][0] += v0; ksum[bj][1] += v1; }
;                 }
;             }
;         if (g == 1) {
; #pragma unroll
;             for (int bj = 0; bj < 2; ++bj)
; #pragma unroll
;                 for (int n = 0; n < 2; ++n)
; #pragma unroll
;                     for (int j = 0; j < 4; ++j) { float t = ksum[bj][n][j]; t += __shfl_xor(t, 1); t += __shfl_xor(t, 2); t += __shfl_xor(t, 4); t += __shfl_xor(t, 8);
;                         if (fr == 0) unsafeAtomicAdd(kmf + (((size_t)(b * 16 + (u.pn & 7) * 2 + bj) * 16 + (u.pm & 15)) * 128 + wc * 32 + 8 * fq + 4 * n + j), t); }
.LBB0_503:
	s_or_b64 exec, exec, s[12:13]
	v_cndmask_b32_e64 v2, 0, v3, s[10:11]
	s_nop 1
	v_mov_b32_dpp v3, v2 quad_perm:[1,0,3,2] row_mask:0xf bank_mask:0xf
	s_waitcnt lgkmcnt(0)
	v_add_f32_e32 v6, v2, v3
	s_nop 1
	v_mov_b32_dpp v7, v6 quad_perm:[2,3,0,1] row_mask:0xf bank_mask:0xf
	v_pk_add_f32 v[2:3], v[172:173], 0 op_sel_hi:[1,0]
	s_waitcnt lgkmcnt(0)
	v_add_f32_e32 v6, v6, v7
	s_nop 1
	v_mov_b32_dpp v7, v6 row_half_mirror row_mask:0xf bank_mask:0xf
	s_nop 1
	v_mov_b32_dpp v7, v7 quad_perm:[3,2,1,0] row_mask:0xf bank_mask:0xf
	v_pk_add_f32 v[2:3], v[2:3], v[132:133]
	s_waitcnt lgkmcnt(0)
	v_add_f32_e32 v6, v6, v7
	v_pk_add_f32 v[2:3], v[2:3], v[116:117]
	s_nop 1
	v_mov_b32_dpp v7, v6 row_mirror row_mask:0xf bank_mask:0xf
	s_nop 1
	v_mov_b32_dpp v7, v7 row_half_mirror row_mask:0xf bank_mask:0xf
	v_pk_add_f32 v[2:3], v[2:3], v[100:101]
	s_nop 0
	v_pk_add_f32 v[2:3], v[2:3], v[84:85]
	s_nop 0
	v_pk_add_f32 v[2:3], v[2:3], v[68:69]
	s_nop 0
	v_pk_add_f32 v[2:3], v[2:3], v[52:53]
	s_nop 0
	v_pk_add_f32 v[4:5], v[2:3], v[4:5]
	s_nop 0
	v_cndmask_b32_e64 v2, 0, v5, s[10:11]
	v_cndmask_b32_e64 v3, 0, v4, s[10:11]
	s_and_saveexec_b64 s[10:11], s[6:7]
	s_cbranch_execz .LBB0_505
	s_lshl_b32 s12, s26, 1
	s_and_b32 s12, s12, 14
	s_or_b32 s12, s14, s12
	s_or_b32 s12, s12, 1
	s_ashr_i32 s13, s12, 31
	s_lshl_b64 s[12:13], s[12:13], 13
	v_readlane_b32 s15, v253, 48
	s_add_u32 s12, s15, s12
	v_readlane_b32 s15, v253, 49
	s_addc_u32 s13, s15, s13
	s_lshl_b32 s15, s22, 9
	s_and_b32 s15, s15, 0x1e00
	s_add_u32 s12, s12, s15
	s_addc_u32 s13, s13, 0
	s_lshl_b32 s15, s34, 2
	s_add_u32 s12, s12, s15
	s_waitcnt lgkmcnt(0)
	v_add_f32_e32 v4, v6, v7
	s_addc_u32 s13, s13, 0
	global_atomic_add_f32 v14, v4, s[12:13] offset:20
.LBB0_505:
	s_or_b64 exec, exec, s[10:11]
	s_nop 1
	v_mov_b32_dpp v4, v3 quad_perm:[1,0,3,2] row_mask:0xf bank_mask:0xf
	s_waitcnt lgkmcnt(0)
	v_add_f32_e32 v3, v3, v4
	s_nop 1
	v_mov_b32_dpp v4, v3 quad_perm:[2,3,0,1] row_mask:0xf bank_mask:0xf
	s_waitcnt lgkmcnt(0)
	v_add_f32_e32 v3, v3, v4
	s_nop 1
	v_mov_b32_dpp v4, v3 row_half_mirror row_mask:0xf bank_mask:0xf
	s_nop 1
	v_mov_b32_dpp v4, v4 quad_perm:[3,2,1,0] row_mask:0xf bank_mask:0xf
	s_waitcnt lgkmcnt(0)
	v_add_f32_e32 v3, v3, v4
	s_nop 1
	v_mov_b32_dpp v4, v3 row_mirror row_mask:0xf bank_mask:0xf
	s_nop 1
	v_mov_b32_dpp v4, v4 row_half_mirror row_mask:0xf bank_mask:0xf
	s_and_saveexec_b64 s[10:11], s[6:7]
	s_cbranch_execz .LBB0_507
	s_lshl_b32 s12, s26, 1
	s_and_b32 s12, s12, 14
	s_or_b32 s12, s14, s12
	s_or_b32 s12, s12, 1
	s_ashr_i32 s13, s12, 31
	s_lshl_b64 s[12:13], s[12:13], 13
	v_readlane_b32 s15, v253, 48
	s_add_u32 s12, s15, s12
	v_readlane_b32 s15, v253, 49
	s_addc_u32 s13, s15, s13
	s_lshl_b32 s15, s22, 9
	s_and_b32 s15, s15, 0x1e00
	s_add_u32 s12, s12, s15
	s_addc_u32 s13, s13, 0
	s_lshl_b32 s15, s34, 2
	s_add_u32 s12, s12, s15
	s_waitcnt lgkmcnt(0)
	v_add_f32_e32 v3, v3, v4
	s_addc_u32 s13, s13, 0
	global_atomic_add_f32 v14, v3, s[12:13] offset:24
.LBB0_507:
	s_or_b64 exec, exec, s[10:11]
	s_nop 1
	v_mov_b32_dpp v3, v2 quad_perm:[1,0,3,2] row_mask:0xf bank_mask:0xf
	s_waitcnt lgkmcnt(0)
	v_add_f32_e32 v2, v2, v3
	s_nop 1
	v_mov_b32_dpp v3, v2 quad_perm:[2,3,0,1] row_mask:0xf bank_mask:0xf
	s_waitcnt lgkmcnt(0)
	v_add_f32_e32 v2, v2, v3
	s_nop 1
	v_mov_b32_dpp v3, v2 row_half_mirror row_mask:0xf bank_mask:0xf
	s_nop 1
	v_mov_b32_dpp v3, v3 quad_perm:[3,2,1,0] row_mask:0xf bank_mask:0xf
	s_waitcnt lgkmcnt(0)
	v_add_f32_e32 v2, v2, v3
	s_nop 1
	v_mov_b32_dpp v3, v2 row_mirror row_mask:0xf bank_mask:0xf
	s_nop 1
	v_mov_b32_dpp v3, v3 row_half_mirror row_mask:0xf bank_mask:0xf
	s_and_saveexec_b64 s[10:11], s[6:7]
	s_cbranch_execz .LBB0_509
	s_lshl_b32 s12, s26, 1
	s_and_b32 s12, s12, 14
	s_or_b32 s12, s14, s12
	s_or_b32 s12, s12, 1
	s_ashr_i32 s13, s12, 31
	s_lshl_b64 s[12:13], s[12:13], 13
	v_readlane_b32 s14, v253, 48
	s_add_u32 s12, s14, s12
	v_readlane_b32 s14, v253, 49
	s_addc_u32 s13, s14, s13
	s_lshl_b32 s14, s22, 9
	s_and_b32 s14, s14, 0x1e00
	s_add_u32 s12, s12, s14
	s_addc_u32 s13, s13, 0
	s_lshl_b32 s14, s34, 2
	s_add_u32 s12, s12, s14
	s_waitcnt lgkmcnt(0)
	v_add_f32_e32 v2, v2, v3
	s_addc_u32 s13, s13, 0
	global_atomic_add_f32 v14, v2, s[12:13] offset:28

;     __device__ __forceinline__ void operator()(const f32x4 (&acc)[2][2][4][2], const Unit& u, int wr, int wc, int fr, int fq) const {
;     ...
;                     if (g == 1) { ksum[bj][0] += v0; ksum[bj][1] += v1; }
;                 }
;             }
;         if (g == 1) {
; #pragma unroll
;             for (int bj = 0; bj < 2; ++bj)
; #pragma unroll
;                 for (int n = 0; n < 2; ++n)
; #pragma unroll
;                     for (int j = 0; j < 4; ++j) { float t = ksum[bj][n][j]; t += __shfl_xor(t, 1); t += __shfl_xor(t, 2); t += __shfl_xor(t, 4); t += __shfl_xor(t, 8);
;                         if (fr == 0) unsafeAtomicAdd(kmf + (((size_t)(b * 16 + (u.pn & 7) * 2 + bj) * 16 + (u.pm & 15)) * 128 + wc * 32 + 8 * fq + 4 * n + j), t); }
.LBB0_844:
	v_pk_add_f32 v[2:3], v[30:31], 0 op_sel_hi:[1,0]
	v_and_b32_e32 v5, 64, v207
	v_pk_add_f32 v[2:3], v[2:3], v[142:143]
	v_xor_b32_e32 v4, 1, v207
	v_pk_add_f32 v[2:3], v[2:3], v[126:127]
	v_add_u32_e32 v8, 64, v5
	v_pk_add_f32 v[2:3], v[2:3], v[110:111]
	v_cmp_lt_i32_e32 vcc, v4, v8
	v_pk_add_f32 v[2:3], v[2:3], v[94:95]
	v_xor_b32_e32 v6, 2, v207
	v_pk_add_f32 v[2:3], v[2:3], v[78:79]
	v_cndmask_b32_e32 v4, v207, v4, vcc
	v_pk_add_f32 v[2:3], v[2:3], v[62:63]
	v_lshlrev_b32_e32 v5, 2, v4
	v_pk_add_f32 v[2:3], v[2:3], v[46:47]
	v_cmp_lt_i32_e32 vcc, v6, v8
	v_cndmask_b32_e64 v2, 0, v2, s[8:9]
	s_nop 1
	v_mov_b32_dpp v4, v2 quad_perm:[1,0,3,2] row_mask:0xf bank_mask:0xf
	v_cndmask_b32_e32 v6, v207, v6, vcc
	v_lshlrev_b32_e32 v6, 2, v6
	v_xor_b32_e32 v7, 4, v207
	v_cmp_lt_i32_e32 vcc, v7, v8
	s_waitcnt lgkmcnt(0)
	v_add_f32_e32 v2, v2, v4
	s_nop 1
	v_mov_b32_dpp v4, v2 quad_perm:[2,3,0,1] row_mask:0xf bank_mask:0xf
	v_cndmask_b32_e32 v7, v207, v7, vcc
	v_lshlrev_b32_e32 v7, 2, v7
	v_xor_b32_e32 v9, 8, v207
	v_cmp_lt_i32_e32 vcc, v9, v8
	s_waitcnt lgkmcnt(0)
	v_add_f32_e32 v2, v2, v4
	s_nop 1
	v_mov_b32_dpp v4, v2 row_half_mirror row_mask:0xf bank_mask:0xf
	s_nop 1
	v_mov_b32_dpp v4, v4 quad_perm:[3,2,1,0] row_mask:0xf bank_mask:0xf
	v_cndmask_b32_e32 v8, v207, v9, vcc
	v_lshlrev_b32_e32 v8, 2, v8
	s_and_b32 s3, s16, -16
	s_waitcnt lgkmcnt(0)
	v_add_f32_e32 v2, v2, v4
	s_nop 1
	v_mov_b32_dpp v9, v2 row_mirror row_mask:0xf bank_mask:0xf
	s_nop 1
	v_mov_b32_dpp v9, v9 row_half_mirror row_mask:0xf bank_mask:0xf
	v_lshlrev_b32_e32 v4, 2, v170
	s_and_saveexec_b64 s[10:11], s[4:5]
	s_cbranch_execz .LBB0_846
	s_lshl_b32 s12, s22, 1
	s_and_b32 s12, s12, 14
	s_or_b32 s12, s12, s3
	s_ashr_i32 s13, s12, 31
	s_lshl_b64 s[12:13], s[12:13], 13
	v_readlane_b32 s14, v253, 48
	s_add_u32 s12, s14, s12
	v_readlane_b32 s14, v253, 49
	s_addc_u32 s13, s14, s13
	s_lshl_b32 s14, s16, 9
	s_and_b32 s14, s14, 0x1e00
	s_add_u32 s12, s12, s14
	s_addc_u32 s13, s13, 0
	s_lshl_b32 s14, s28, 2
	s_add_u32 s12, s12, s14
	s_waitcnt lgkmcnt(0)
	v_add_f32_e32 v2, v2, v9
	s_addc_u32 s13, s13, 0
	global_atomic_add_f32 v4, v2, s[12:13]
.LBB0_846:
	s_or_b64 exec, exec, s[10:11]
	v_cndmask_b32_e64 v2, 0, v3, s[8:9]
	s_nop 1
	v_mov_b32_dpp v3, v2 quad_perm:[1,0,3,2] row_mask:0xf bank_mask:0xf
	s_waitcnt lgkmcnt(0)
	v_add_f32_e32 v9, v2, v3
	s_nop 1
	v_mov_b32_dpp v10, v9 quad_perm:[2,3,0,1] row_mask:0xf bank_mask:0xf
	v_pk_add_f32 v[2:3], v[26:27], 0 op_sel_hi:[1,0]
	s_waitcnt lgkmcnt(0)
	v_add_f32_e32 v9, v9, v10
	s_nop 1
	v_mov_b32_dpp v10, v9 row_half_mirror row_mask:0xf bank_mask:0xf
	s_nop 1
	v_mov_b32_dpp v10, v10 quad_perm:[3,2,1,0] row_mask:0xf bank_mask:0xf
	v_pk_add_f32 v[2:3], v[2:3], v[144:145]
	s_waitcnt lgkmcnt(0)
	v_add_f32_e32 v9, v9, v10
	v_pk_add_f32 v[2:3], v[2:3], v[128:129]
	s_nop 1
	v_mov_b32_dpp v10, v9 row_mirror row_mask:0xf bank_mask:0xf
	s_nop 1
	v_mov_b32_dpp v10, v10 row_half_mirror row_mask:0xf bank_mask:0xf
	v_pk_add_f32 v[2:3], v[2:3], v[112:113]
	s_nop 0
	v_pk_add_f32 v[2:3], v[2:3], v[96:97]
	s_nop 0
	v_pk_add_f32 v[2:3], v[2:3], v[80:81]
	s_nop 0
	v_pk_add_f32 v[2:3], v[2:3], v[64:65]
	s_nop 0
	v_pk_add_f32 v[12:13], v[2:3], v[48:49]
	s_nop 0
	v_cndmask_b32_e64 v2, 0, v13, s[8:9]
	v_cndmask_b32_e64 v3, 0, v12, s[8:9]
	s_and_saveexec_b64 s[10:11], s[4:5]
	s_cbranch_execz .LBB0_848
	s_lshl_b32 s12, s22, 1
	s_and_b32 s12, s12, 14
	s_or_b32 s12, s12, s3
	s_ashr_i32 s13, s12, 31
	s_lshl_b64 s[12:13], s[12:13], 13
	v_readlane_b32 s14, v253, 48
	s_add_u32 s12, s14, s12
	v_readlane_b32 s14, v253, 49
	s_addc_u32 s13, s14, s13
	s_lshl_b32 s14, s16, 9
	s_and_b32 s14, s14, 0x1e00
	s_add_u32 s12, s12, s14
	s_addc_u32 s13, s13, 0
	s_lshl_b32 s14, s28, 2
	s_add_u32 s12, s12, s14
	s_waitcnt lgkmcnt(0)
	v_add_f32_e32 v9, v9, v10
	s_addc_u32 s13, s13, 0
	global_atomic_add_f32 v4, v9, s[12:13] offset:4
.LBB0_848:
	s_or_b64 exec, exec, s[10:11]
	s_nop 1
	v_mov_b32_dpp v9, v3 quad_perm:[1,0,3,2] row_mask:0xf bank_mask:0xf
	s_waitcnt lgkmcnt(0)
	v_add_f32_e32 v3, v3, v9
	s_nop 1
	v_mov_b32_dpp v9, v3 quad_perm:[2,3,0,1] row_mask:0xf bank_mask:0xf
	s_waitcnt lgkmcnt(0)
	v_add_f32_e32 v3, v3, v9
	s_nop 1
	v_mov_b32_dpp v9, v3 row_half_mirror row_mask:0xf bank_mask:0xf
	s_nop 1
	v_mov_b32_dpp v9, v9 quad_perm:[3,2,1,0] row_mask:0xf bank_mask:0xf
	s_waitcnt lgkmcnt(0)
	v_add_f32_e32 v3, v3, v9
	s_nop 1
	v_mov_b32_dpp v9, v3 row_mirror row_mask:0xf bank_mask:0xf
	s_nop 1
	v_mov_b32_dpp v9, v9 row_half_mirror row_mask:0xf bank_mask:0xf
	s_and_saveexec_b64 s[10:11], s[4:5]
	s_cbranch_execz .LBB0_850
	s_lshl_b32 s12, s22, 1
	s_and_b32 s12, s12, 14
	s_or_b32 s12, s12, s3
	s_ashr_i32 s13, s12, 31
	s_lshl_b64 s[12:13], s[12:13], 13
	v_readlane_b32 s14, v253, 48
	s_add_u32 s12, s14, s12
	v_readlane_b32 s14, v253, 49
	s_addc_u32 s13, s14, s13
	s_lshl_b32 s14, s16, 9
	s_and_b32 s14, s14, 0x1e00
	s_add_u32 s12, s12, s14
	s_addc_u32 s13, s13, 0
	s_lshl_b32 s14, s28, 2
	s_add_u32 s12, s12, s14
	s_waitcnt lgkmcnt(0)
	v_add_f32_e32 v3, v3, v9
	s_addc_u32 s13, s13, 0
	global_atomic_add_f32 v4, v3, s[12:13] offset:8
;     __device__ __forceinline__ void operator()(const f32x4 (&acc)[2][2][4][2], const Unit& u, int wr, int wc, int fr, int fq) const {
;     ...
;                     if (g == 1) { ksum[bj][0] += v0; ksum[bj][1] += v1; }
;                 }
;             }
;         if (g == 1) {
; #pragma unroll
;             for (int bj = 0; bj < 2; ++bj)
; #pragma unroll
;                 for (int n = 0; n < 2; ++n)
; #pragma unroll
;                     for (int j = 0; j < 4; ++j) { float t = ksum[bj][n][j]; t += __shfl_xor(t, 1); t += __shfl_xor(t, 2); t += __shfl_xor(t, 4); t += __shfl_xor(t, 8);
;                         if (fr == 0) unsafeAtomicAdd(kmf + (((size_t)(b * 16 + (u.pn & 7) * 2 + bj) * 16 + (u.pm & 15)) * 128 + wc * 32 + 8 * fq + 4 * n + j), t); }
.LBB0_850:
	s_or_b64 exec, exec, s[10:11]
	s_nop 1
	v_mov_b32_dpp v3, v2 quad_perm:[1,0,3,2] row_mask:0xf bank_mask:0xf
	s_waitcnt lgkmcnt(0)
	v_add_f32_e32 v2, v2, v3
	s_nop 1
	v_mov_b32_dpp v3, v2 quad_perm:[2,3,0,1] row_mask:0xf bank_mask:0xf
	s_waitcnt lgkmcnt(0)
	v_add_f32_e32 v2, v2, v3
	s_nop 1
	v_mov_b32_dpp v3, v2 row_half_mirror row_mask:0xf bank_mask:0xf
	s_nop 1
	v_mov_b32_dpp v3, v3 quad_perm:[3,2,1,0] row_mask:0xf bank_mask:0xf
	s_waitcnt lgkmcnt(0)
	v_add_f32_e32 v2, v2, v3
	s_nop 1
	v_mov_b32_dpp v3, v2 row_mirror row_mask:0xf bank_mask:0xf
	s_nop 1
	v_mov_b32_dpp v3, v3 row_half_mirror row_mask:0xf bank_mask:0xf
	s_and_saveexec_b64 s[10:11], s[4:5]
	s_cbranch_execz .LBB0_852
	s_lshl_b32 s12, s22, 1
	s_and_b32 s12, s12, 14
	s_or_b32 s12, s12, s3
	s_ashr_i32 s13, s12, 31
	s_lshl_b64 s[12:13], s[12:13], 13
	v_readlane_b32 s14, v253, 48
	s_add_u32 s12, s14, s12
	v_readlane_b32 s14, v253, 49
	s_addc_u32 s13, s14, s13
	s_lshl_b32 s14, s16, 9
	s_and_b32 s14, s14, 0x1e00
	s_add_u32 s12, s12, s14
	s_addc_u32 s13, s13, 0
	s_lshl_b32 s14, s28, 2
	s_add_u32 s12, s12, s14
	s_waitcnt lgkmcnt(0)
	v_add_f32_e32 v2, v2, v3
	s_addc_u32 s13, s13, 0
	global_atomic_add_f32 v4, v2, s[12:13] offset:12
.LBB0_852:
	s_or_b64 exec, exec, s[10:11]
	s_waitcnt lgkmcnt(0)
	v_pk_add_f32 v[2:3], v[22:23], 0 op_sel_hi:[1,0]
	s_nop 0
	v_pk_add_f32 v[2:3], v[2:3], v[138:139]
	s_nop 0
	v_pk_add_f32 v[2:3], v[2:3], v[122:123]
	s_nop 0
	v_pk_add_f32 v[2:3], v[2:3], v[106:107]
	s_nop 0
	v_pk_add_f32 v[2:3], v[2:3], v[90:91]
	s_nop 0
	v_pk_add_f32 v[2:3], v[2:3], v[74:75]
	s_nop 0
	v_pk_add_f32 v[2:3], v[2:3], v[58:59]
	s_nop 0
	v_pk_add_f32 v[2:3], v[2:3], v[42:43]
	s_nop 0
	v_cndmask_b32_e64 v2, 0, v2, s[8:9]
	s_nop 1
	v_mov_b32_dpp v9, v2 quad_perm:[1,0,3,2] row_mask:0xf bank_mask:0xf
	s_waitcnt lgkmcnt(0)
	v_add_f32_e32 v2, v2, v9
	s_nop 1
	v_mov_b32_dpp v9, v2 quad_perm:[2,3,0,1] row_mask:0xf bank_mask:0xf
	s_waitcnt lgkmcnt(0)
	v_add_f32_e32 v2, v2, v9
	s_nop 1
	v_mov_b32_dpp v9, v2 row_half_mirror row_mask:0xf bank_mask:0xf
	s_nop 1
	v_mov_b32_dpp v9, v9 quad_perm:[3,2,1,0] row_mask:0xf bank_mask:0xf
	s_waitcnt lgkmcnt(0)
	v_add_f32_e32 v2, v2, v9
	s_nop 1
	v_mov_b32_dpp v9, v2 row_mirror row_mask:0xf bank_mask:0xf
	s_nop 1
	v_mov_b32_dpp v9, v9 row_half_mirror row_mask:0xf bank_mask:0xf
	s_and_saveexec_b64 s[10:11], s[4:5]
	s_cbranch_execz .LBB0_854
	s_lshl_b32 s12, s22, 1
	s_and_b32 s12, s12, 14
	s_or_b32 s12, s12, s3
	s_ashr_i32 s13, s12, 31
	s_lshl_b64 s[12:13], s[12:13], 13
	v_readlane_b32 s14, v253, 48
	s_add_u32 s12, s14, s12
	v_readlane_b32 s14, v253, 49
	s_addc_u32 s13, s14, s13
	s_lshl_b32 s14, s16, 9
	s_and_b32 s14, s14, 0x1e00
	s_add_u32 s12, s12, s14
	s_addc_u32 s13, s13, 0
	s_lshl_b32 s14, s28, 2
	s_add_u32 s12, s12, s14
	s_waitcnt lgkmcnt(0)
	v_add_f32_e32 v2, v2, v9
	s_addc_u32 s13, s13, 0
	global_atomic_add_f32 v4, v2, s[12:13] offset:16
.LBB0_854:
	s_or_b64 exec, exec, s[10:11]
	v_cndmask_b32_e64 v2, 0, v3, s[8:9]
	s_nop 1
	v_mov_b32_dpp v3, v2 quad_perm:[1,0,3,2] row_mask:0xf bank_mask:0xf
	s_waitcnt lgkmcnt(0)
	v_add_f32_e32 v9, v2, v3
	s_nop 1
	v_mov_b32_dpp v10, v9 quad_perm:[2,3,0,1] row_mask:0xf bank_mask:0xf
	v_pk_add_f32 v[2:3], v[18:19], 0 op_sel_hi:[1,0]
	s_waitcnt lgkmcnt(0)
	v_add_f32_e32 v9, v9, v10
	s_nop 1
	v_mov_b32_dpp v10, v9 row_half_mirror row_mask:0xf bank_mask:0xf
	s_nop 1
	v_mov_b32_dpp v10, v10 quad_perm:[3,2,1,0] row_mask:0xf bank_mask:0xf
	v_pk_add_f32 v[2:3], v[2:3], v[140:141]
	s_waitcnt lgkmcnt(0)
	v_add_f32_e32 v9, v9, v10
	v_pk_add_f32 v[2:3], v[2:3], v[124:125]
	s_nop 1
	v_mov_b32_dpp v10, v9 row_mirror row_mask:0xf bank_mask:0xf
	s_nop 1
	v_mov_b32_dpp v10, v10 row_half_mirror row_mask:0xf bank_mask:0xf
	v_pk_add_f32 v[2:3], v[2:3], v[108:109]
	s_nop 0
	v_pk_add_f32 v[2:3], v[2:3], v[92:93]
	s_nop 0
	v_pk_add_f32 v[2:3], v[2:3], v[76:77]
	s_nop 0
	v_pk_add_f32 v[2:3], v[2:3], v[60:61]
	s_nop 0
	v_pk_add_f32 v[12:13], v[2:3], v[44:45]
	s_nop 0
	v_cndmask_b32_e64 v2, 0, v13, s[8:9]
	v_cndmask_b32_e64 v3, 0, v12, s[8:9]
	s_and_saveexec_b64 s[10:11], s[4:5]
	s_cbranch_execz .LBB0_856
	s_lshl_b32 s12, s22, 1
	s_and_b32 s12, s12, 14
	s_or_b32 s12, s12, s3
	s_ashr_i32 s13, s12, 31
	s_lshl_b64 s[12:13], s[12:13], 13
	v_readlane_b32 s14, v253, 48
	s_add_u32 s12, s14, s12
	v_readlane_b32 s14, v253, 49
	s_addc_u32 s13, s14, s13
	s_lshl_b32 s14, s16, 9
	s_and_b32 s14, s14, 0x1e00
	s_add_u32 s12, s12, s14
	s_addc_u32 s13, s13, 0
	s_lshl_b32 s14, s28, 2
	s_add_u32 s12, s12, s14
	s_waitcnt lgkmcnt(0)
	v_add_f32_e32 v9, v9, v10
	s_addc_u32 s13, s13, 0
	global_atomic_add_f32 v4, v9, s[12:13] offset:20
.LBB0_856:
	s_or_b64 exec, exec, s[10:11]
	s_nop 1
	v_mov_b32_dpp v9, v3 quad_perm:[1,0,3,2] row_mask:0xf bank_mask:0xf
	s_waitcnt lgkmcnt(0)
	v_add_f32_e32 v3, v3, v9
	s_nop 1
	v_mov_b32_dpp v9, v3 quad_perm:[2,3,0,1] row_mask:0xf bank_mask:0xf
	s_waitcnt lgkmcnt(0)
	v_add_f32_e32 v3, v3, v9
	s_nop 1
	v_mov_b32_dpp v9, v3 row_half_mirror row_mask:0xf bank_mask:0xf
	s_nop 1
	v_mov_b32_dpp v9, v9 quad_perm:[3,2,1,0] row_mask:0xf bank_mask:0xf
	s_waitcnt lgkmcnt(0)
	v_add_f32_e32 v3, v3, v9
	s_nop 1
	v_mov_b32_dpp v9, v3 row_mirror row_mask:0xf bank_mask:0xf
	s_nop 1
	v_mov_b32_dpp v9, v9 row_half_mirror row_mask:0xf bank_mask:0xf
	s_and_saveexec_b64 s[10:11], s[4:5]
	s_cbranch_execz .LBB0_858
	s_lshl_b32 s12, s22, 1
	s_and_b32 s12, s12, 14
	s_or_b32 s12, s12, s3
	s_ashr_i32 s13, s12, 31
	s_lshl_b64 s[12:13], s[12:13], 13
	v_readlane_b32 s14, v253, 48
	s_add_u32 s12, s14, s12
	v_readlane_b32 s14, v253, 49
	s_addc_u32 s13, s14, s13
	s_lshl_b32 s14, s16, 9
	s_and_b32 s14, s14, 0x1e00
	s_add_u32 s12, s12, s14
	s_addc_u32 s13, s13, 0
	s_lshl_b32 s14, s28, 2
	s_add_u32 s12, s12, s14
	s_waitcnt lgkmcnt(0)
	v_add_f32_e32 v3, v3, v9
	s_addc_u32 s13, s13, 0
	global_atomic_add_f32 v4, v3, s[12:13] offset:24
;     __device__ __forceinline__ void operator()(const f32x4 (&acc)[2][2][4][2], const Unit& u, int wr, int wc, int fr, int fq) const {
;     ...
;                     if (g == 1) { ksum[bj][0] += v0; ksum[bj][1] += v1; }
;                 }
;             }
;         if (g == 1) {
; #pragma unroll
;             for (int bj = 0; bj < 2; ++bj)
; #pragma unroll
;                 for (int n = 0; n < 2; ++n)
; #pragma unroll
;                     for (int j = 0; j < 4; ++j) { float t = ksum[bj][n][j]; t += __shfl_xor(t, 1); t += __shfl_xor(t, 2); t += __shfl_xor(t, 4); t += __shfl_xor(t, 8);
;                         if (fr == 0) unsafeAtomicAdd(kmf + (((size_t)(b * 16 + (u.pn & 7) * 2 + bj) * 16 + (u.pm & 15)) * 128 + wc * 32 + 8 * fq + 4 * n + j), t); }
.LBB0_858:
	s_or_b64 exec, exec, s[10:11]
	s_nop 1
	v_mov_b32_dpp v3, v2 quad_perm:[1,0,3,2] row_mask:0xf bank_mask:0xf
	s_waitcnt lgkmcnt(0)
	v_add_f32_e32 v2, v2, v3
	s_nop 1
	v_mov_b32_dpp v3, v2 quad_perm:[2,3,0,1] row_mask:0xf bank_mask:0xf
	s_waitcnt lgkmcnt(0)
	v_add_f32_e32 v2, v2, v3
	s_nop 1
	v_mov_b32_dpp v3, v2 row_half_mirror row_mask:0xf bank_mask:0xf
	s_nop 1
	v_mov_b32_dpp v3, v3 quad_perm:[3,2,1,0] row_mask:0xf bank_mask:0xf
	s_waitcnt lgkmcnt(0)
	v_add_f32_e32 v2, v2, v3
	s_nop 1
	v_mov_b32_dpp v3, v2 row_mirror row_mask:0xf bank_mask:0xf
	s_nop 1
	v_mov_b32_dpp v3, v3 row_half_mirror row_mask:0xf bank_mask:0xf
	s_and_saveexec_b64 s[10:11], s[4:5]
	s_cbranch_execz .LBB0_860
	s_lshl_b32 s12, s22, 1
	s_and_b32 s12, s12, 14
	s_or_b32 s12, s12, s3
	s_ashr_i32 s13, s12, 31
	s_lshl_b64 s[12:13], s[12:13], 13
	v_readlane_b32 s14, v253, 48
	s_add_u32 s12, s14, s12
	v_readlane_b32 s14, v253, 49
	s_addc_u32 s13, s14, s13
	s_lshl_b32 s14, s16, 9
	s_and_b32 s14, s14, 0x1e00
	s_add_u32 s12, s12, s14
	s_addc_u32 s13, s13, 0
	s_lshl_b32 s14, s28, 2
	s_add_u32 s12, s12, s14
	s_waitcnt lgkmcnt(0)
	v_add_f32_e32 v2, v2, v3
	s_addc_u32 s13, s13, 0
	global_atomic_add_f32 v4, v2, s[12:13] offset:28
.LBB0_860:
	s_or_b64 exec, exec, s[10:11]
	s_waitcnt lgkmcnt(0)
	v_pk_add_f32 v[2:3], v[32:33], 0 op_sel_hi:[1,0]
	s_nop 0
	v_pk_add_f32 v[2:3], v[2:3], v[134:135]
	s_nop 0
	v_pk_add_f32 v[2:3], v[2:3], v[118:119]
	s_nop 0
	v_pk_add_f32 v[2:3], v[2:3], v[102:103]
	s_nop 0
	v_pk_add_f32 v[2:3], v[2:3], v[86:87]
	s_nop 0
	v_pk_add_f32 v[2:3], v[2:3], v[70:71]
	s_nop 0
	v_pk_add_f32 v[2:3], v[2:3], v[54:55]
	s_nop 0
	v_pk_add_f32 v[2:3], v[2:3], v[38:39]
	s_nop 0
	v_cndmask_b32_e64 v2, 0, v2, s[8:9]
	s_nop 1
	v_mov_b32_dpp v9, v2 quad_perm:[1,0,3,2] row_mask:0xf bank_mask:0xf
	s_waitcnt lgkmcnt(0)
	v_add_f32_e32 v2, v2, v9
	s_nop 1
	v_mov_b32_dpp v9, v2 quad_perm:[2,3,0,1] row_mask:0xf bank_mask:0xf
	s_waitcnt lgkmcnt(0)
	v_add_f32_e32 v2, v2, v9
	s_nop 1
	v_mov_b32_dpp v9, v2 row_half_mirror row_mask:0xf bank_mask:0xf
	s_nop 1
	v_mov_b32_dpp v9, v9 quad_perm:[3,2,1,0] row_mask:0xf bank_mask:0xf
	s_waitcnt lgkmcnt(0)
	v_add_f32_e32 v2, v2, v9
	s_nop 1
	v_mov_b32_dpp v9, v2 row_mirror row_mask:0xf bank_mask:0xf
	s_nop 1
	v_mov_b32_dpp v9, v9 row_half_mirror row_mask:0xf bank_mask:0xf
	s_and_saveexec_b64 s[10:11], s[4:5]
	s_cbranch_execz .LBB0_862
	s_lshl_b32 s12, s22, 1
	s_and_b32 s12, s12, 14
	s_or_b32 s12, s3, s12
	s_or_b32 s12, s12, 1
	s_ashr_i32 s13, s12, 31
	s_lshl_b64 s[12:13], s[12:13], 13
	v_readlane_b32 s14, v253, 48
	s_add_u32 s12, s14, s12
	v_readlane_b32 s14, v253, 49
	s_addc_u32 s13, s14, s13
	s_lshl_b32 s14, s16, 9
	s_and_b32 s14, s14, 0x1e00
	s_add_u32 s12, s12, s14
	s_addc_u32 s13, s13, 0
	s_lshl_b32 s14, s28, 2
	s_add_u32 s12, s12, s14
	s_waitcnt lgkmcnt(0)
	v_add_f32_e32 v2, v2, v9
	s_addc_u32 s13, s13, 0
	global_atomic_add_f32 v4, v2, s[12:13]
.LBB0_862:
	s_or_b64 exec, exec, s[10:11]
	v_cndmask_b32_e64 v2, 0, v3, s[8:9]
	s_nop 1
	v_mov_b32_dpp v3, v2 quad_perm:[1,0,3,2] row_mask:0xf bank_mask:0xf
	s_waitcnt lgkmcnt(0)
	v_add_f32_e32 v9, v2, v3
	s_nop 1
	v_mov_b32_dpp v10, v9 quad_perm:[2,3,0,1] row_mask:0xf bank_mask:0xf
	v_pk_add_f32 v[2:3], v[28:29], 0 op_sel_hi:[1,0]
	s_waitcnt lgkmcnt(0)
	v_add_f32_e32 v9, v9, v10
	s_nop 1
	v_mov_b32_dpp v10, v9 row_half_mirror row_mask:0xf bank_mask:0xf
	s_nop 1
	v_mov_b32_dpp v10, v10 quad_perm:[3,2,1,0] row_mask:0xf bank_mask:0xf
	v_pk_add_f32 v[2:3], v[2:3], v[136:137]
	s_waitcnt lgkmcnt(0)
	v_add_f32_e32 v9, v9, v10
	v_pk_add_f32 v[2:3], v[2:3], v[120:121]
	s_nop 1
	v_mov_b32_dpp v10, v9 row_mirror row_mask:0xf bank_mask:0xf
	s_nop 1
	v_mov_b32_dpp v10, v10 row_half_mirror row_mask:0xf bank_mask:0xf
	v_pk_add_f32 v[2:3], v[2:3], v[104:105]
	s_nop 0
	v_pk_add_f32 v[2:3], v[2:3], v[88:89]
	s_nop 0
	v_pk_add_f32 v[2:3], v[2:3], v[72:73]
	s_nop 0
	v_pk_add_f32 v[2:3], v[2:3], v[56:57]
	s_nop 0
	v_pk_add_f32 v[12:13], v[2:3], v[40:41]
	s_nop 0
	v_cndmask_b32_e64 v2, 0, v13, s[8:9]
	v_cndmask_b32_e64 v3, 0, v12, s[8:9]
	s_and_saveexec_b64 s[10:11], s[4:5]
	s_cbranch_execz .LBB0_864
	s_lshl_b32 s12, s22, 1
	s_and_b32 s12, s12, 14
	s_or_b32 s12, s3, s12
	s_or_b32 s12, s12, 1
	s_ashr_i32 s13, s12, 31
	s_lshl_b64 s[12:13], s[12:13], 13
	v_readlane_b32 s14, v253, 48
	s_add_u32 s12, s14, s12
	v_readlane_b32 s14, v253, 49
	s_addc_u32 s13, s14, s13
	s_lshl_b32 s14, s16, 9
	s_and_b32 s14, s14, 0x1e00
	s_add_u32 s12, s12, s14
	s_addc_u32 s13, s13, 0
	s_lshl_b32 s14, s28, 2
	s_add_u32 s12, s12, s14
	s_waitcnt lgkmcnt(0)
	v_add_f32_e32 v9, v9, v10
	s_addc_u32 s13, s13, 0
	global_atomic_add_f32 v4, v9, s[12:13] offset:4
.LBB0_864:
	s_or_b64 exec, exec, s[10:11]
	s_nop 1
	v_mov_b32_dpp v9, v3 quad_perm:[1,0,3,2] row_mask:0xf bank_mask:0xf
	s_waitcnt lgkmcnt(0)
	v_add_f32_e32 v3, v3, v9
	s_nop 1
	v_mov_b32_dpp v9, v3 quad_perm:[2,3,0,1] row_mask:0xf bank_mask:0xf
	s_waitcnt lgkmcnt(0)
	v_add_f32_e32 v3, v3, v9
	s_nop 1
	v_mov_b32_dpp v9, v3 row_half_mirror row_mask:0xf bank_mask:0xf
	s_nop 1
	v_mov_b32_dpp v9, v9 quad_perm:[3,2,1,0] row_mask:0xf bank_mask:0xf
	s_waitcnt lgkmcnt(0)
	v_add_f32_e32 v3, v3, v9
	s_nop 1
	v_mov_b32_dpp v9, v3 row_mirror row_mask:0xf bank_mask:0xf
	s_nop 1
	v_mov_b32_dpp v9, v9 row_half_mirror row_mask:0xf bank_mask:0xf
	s_and_saveexec_b64 s[10:11], s[4:5]
	s_cbranch_execz .LBB0_866
	s_lshl_b32 s12, s22, 1
	s_and_b32 s12, s12, 14
	s_or_b32 s12, s3, s12
	s_or_b32 s12, s12, 1
	s_ashr_i32 s13, s12, 31
	s_lshl_b64 s[12:13], s[12:13], 13
	v_readlane_b32 s14, v253, 48
	s_add_u32 s12, s14, s12
	v_readlane_b32 s14, v253, 49
	s_addc_u32 s13, s14, s13
	s_lshl_b32 s14, s16, 9
	s_and_b32 s14, s14, 0x1e00
	s_add_u32 s12, s12, s14
	s_addc_u32 s13, s13, 0
	s_lshl_b32 s14, s28, 2
	s_add_u32 s12, s12, s14
	s_waitcnt lgkmcnt(0)
	v_add_f32_e32 v3, v3, v9
	s_addc_u32 s13, s13, 0
	global_atomic_add_f32 v4, v3, s[12:13] offset:8
;     __device__ __forceinline__ void operator()(const f32x4 (&acc)[2][2][4][2], const Unit& u, int wr, int wc, int fr, int fq) const {
;     ...
;                     if (g == 1) { ksum[bj][0] += v0; ksum[bj][1] += v1; }
;                 }
;             }
;         if (g == 1) {
; #pragma unroll
;             for (int bj = 0; bj < 2; ++bj)
; #pragma unroll
;                 for (int n = 0; n < 2; ++n)
; #pragma unroll
;                     for (int j = 0; j < 4; ++j) { float t = ksum[bj][n][j]; t += __shfl_xor(t, 1); t += __shfl_xor(t, 2); t += __shfl_xor(t, 4); t += __shfl_xor(t, 8);
;                         if (fr == 0) unsafeAtomicAdd(kmf + (((size_t)(b * 16 + (u.pn & 7) * 2 + bj) * 16 + (u.pm & 15)) * 128 + wc * 32 + 8 * fq + 4 * n + j), t); }
.LBB0_866:
	s_or_b64 exec, exec, s[10:11]
	s_nop 1
	v_mov_b32_dpp v3, v2 quad_perm:[1,0,3,2] row_mask:0xf bank_mask:0xf
	s_waitcnt lgkmcnt(0)
	v_add_f32_e32 v2, v2, v3
	s_nop 1
	v_mov_b32_dpp v3, v2 quad_perm:[2,3,0,1] row_mask:0xf bank_mask:0xf
	s_waitcnt lgkmcnt(0)
	v_add_f32_e32 v2, v2, v3
	s_nop 1
	v_mov_b32_dpp v3, v2 row_half_mirror row_mask:0xf bank_mask:0xf
	s_nop 1
	v_mov_b32_dpp v3, v3 quad_perm:[3,2,1,0] row_mask:0xf bank_mask:0xf
	s_waitcnt lgkmcnt(0)
	v_add_f32_e32 v2, v2, v3
	s_nop 1
	v_mov_b32_dpp v3, v2 row_mirror row_mask:0xf bank_mask:0xf
	s_nop 1
	v_mov_b32_dpp v3, v3 row_half_mirror row_mask:0xf bank_mask:0xf
	s_and_saveexec_b64 s[10:11], s[4:5]
	s_cbranch_execz .LBB0_868
	s_lshl_b32 s12, s22, 1
	s_and_b32 s12, s12, 14
	s_or_b32 s12, s3, s12
	s_or_b32 s12, s12, 1
	s_ashr_i32 s13, s12, 31
	s_lshl_b64 s[12:13], s[12:13], 13
	v_readlane_b32 s14, v253, 48
	s_add_u32 s12, s14, s12
	v_readlane_b32 s14, v253, 49
	s_addc_u32 s13, s14, s13
	s_lshl_b32 s14, s16, 9
	s_and_b32 s14, s14, 0x1e00
	s_add_u32 s12, s12, s14
	s_addc_u32 s13, s13, 0
	s_lshl_b32 s14, s28, 2
	s_add_u32 s12, s12, s14
	s_waitcnt lgkmcnt(0)
	v_add_f32_e32 v2, v2, v3
	s_addc_u32 s13, s13, 0
	global_atomic_add_f32 v4, v2, s[12:13] offset:12
.LBB0_868:
	s_or_b64 exec, exec, s[10:11]
	s_waitcnt lgkmcnt(0)
	v_pk_add_f32 v[2:3], v[24:25], 0 op_sel_hi:[1,0]
	s_nop 0
	v_pk_add_f32 v[2:3], v[2:3], v[130:131]
	s_nop 0
	v_pk_add_f32 v[2:3], v[2:3], v[114:115]
	s_nop 0
	v_pk_add_f32 v[2:3], v[2:3], v[98:99]
	s_nop 0
	v_pk_add_f32 v[2:3], v[2:3], v[82:83]
	s_nop 0
	v_pk_add_f32 v[2:3], v[2:3], v[66:67]
	s_nop 0
	v_pk_add_f32 v[2:3], v[2:3], v[50:51]
	s_nop 0
	v_pk_add_f32 v[2:3], v[2:3], v[34:35]
	s_nop 0
	v_cndmask_b32_e64 v2, 0, v2, s[8:9]
	s_nop 1
	v_mov_b32_dpp v9, v2 quad_perm:[1,0,3,2] row_mask:0xf bank_mask:0xf
	s_waitcnt lgkmcnt(0)
	v_add_f32_e32 v2, v2, v9
	s_nop 1
	v_mov_b32_dpp v9, v2 quad_perm:[2,3,0,1] row_mask:0xf bank_mask:0xf
	s_waitcnt lgkmcnt(0)
	v_add_f32_e32 v2, v2, v9
	s_nop 1
	v_mov_b32_dpp v9, v2 row_half_mirror row_mask:0xf bank_mask:0xf
	s_nop 1
	v_mov_b32_dpp v9, v9 quad_perm:[3,2,1,0] row_mask:0xf bank_mask:0xf
	s_waitcnt lgkmcnt(0)
	v_add_f32_e32 v2, v2, v9
	s_nop 1
	v_mov_b32_dpp v9, v2 row_mirror row_mask:0xf bank_mask:0xf
	s_nop 1
	v_mov_b32_dpp v9, v9 row_half_mirror row_mask:0xf bank_mask:0xf
	s_and_saveexec_b64 s[10:11], s[4:5]
	s_cbranch_execz .LBB0_870
	s_lshl_b32 s12, s22, 1
	s_and_b32 s12, s12, 14
	s_or_b32 s12, s3, s12
	s_or_b32 s12, s12, 1
	s_ashr_i32 s13, s12, 31
	s_lshl_b64 s[12:13], s[12:13], 13
	v_readlane_b32 s14, v253, 48
	s_add_u32 s12, s14, s12
	v_readlane_b32 s14, v253, 49
	s_addc_u32 s13, s14, s13
	s_lshl_b32 s14, s16, 9
	s_and_b32 s14, s14, 0x1e00
	s_add_u32 s12, s12, s14
	s_addc_u32 s13, s13, 0
	s_lshl_b32 s14, s28, 2
	s_add_u32 s12, s12, s14
	s_waitcnt lgkmcnt(0)
	v_add_f32_e32 v2, v2, v9
	s_addc_u32 s13, s13, 0
	global_atomic_add_f32 v4, v2, s[12:13] offset:16
;     __device__ __forceinline__ void operator()(const f32x4 (&acc)[2][2][4][2], const Unit& u, int wr, int wc, int fr, int fq) const {
;     ...
;                     if (g == 1) { ksum[bj][0] += v0; ksum[bj][1] += v1; }
;                 }
;             }
;         if (g == 1) {
; #pragma unroll
;             for (int bj = 0; bj < 2; ++bj)
; #pragma unroll
;                 for (int n = 0; n < 2; ++n)
; #pragma unroll
;                     for (int j = 0; j < 4; ++j) { float t = ksum[bj][n][j]; t += __shfl_xor(t, 1); t += __shfl_xor(t, 2); t += __shfl_xor(t, 4); t += __shfl_xor(t, 8);
;                         if (fr == 0) unsafeAtomicAdd(kmf + (((size_t)(b * 16 + (u.pn & 7) * 2 + bj) * 16 + (u.pm & 15)) * 128 + wc * 32 + 8 * fq + 4 * n + j), t); }
.LBB0_870:
	s_or_b64 exec, exec, s[10:11]
	v_cndmask_b32_e64 v2, 0, v3, s[8:9]
	s_nop 1
	v_mov_b32_dpp v3, v2 quad_perm:[1,0,3,2] row_mask:0xf bank_mask:0xf
	s_waitcnt lgkmcnt(0)
	v_add_f32_e32 v9, v2, v3
	s_nop 1
	v_mov_b32_dpp v10, v9 quad_perm:[2,3,0,1] row_mask:0xf bank_mask:0xf
	v_pk_add_f32 v[2:3], v[20:21], 0 op_sel_hi:[1,0]
	s_waitcnt lgkmcnt(0)
	v_add_f32_e32 v9, v9, v10
	s_nop 1
	v_mov_b32_dpp v10, v9 row_half_mirror row_mask:0xf bank_mask:0xf
	s_nop 1
	v_mov_b32_dpp v10, v10 quad_perm:[3,2,1,0] row_mask:0xf bank_mask:0xf
	v_pk_add_f32 v[2:3], v[2:3], v[132:133]
	s_waitcnt lgkmcnt(0)
	v_add_f32_e32 v9, v9, v10
	v_pk_add_f32 v[2:3], v[2:3], v[116:117]
	s_nop 1
	v_mov_b32_dpp v10, v9 row_mirror row_mask:0xf bank_mask:0xf
	s_nop 1
	v_mov_b32_dpp v10, v10 row_half_mirror row_mask:0xf bank_mask:0xf
	v_pk_add_f32 v[2:3], v[2:3], v[100:101]
	s_nop 0
	v_pk_add_f32 v[2:3], v[2:3], v[84:85]
	s_nop 0
	v_pk_add_f32 v[2:3], v[2:3], v[68:69]
	s_nop 0
	v_pk_add_f32 v[2:3], v[2:3], v[52:53]
	s_nop 0
	v_pk_add_f32 v[12:13], v[2:3], v[36:37]
	s_nop 0
	v_cndmask_b32_e64 v2, 0, v13, s[8:9]
	v_cndmask_b32_e64 v3, 0, v12, s[8:9]
	s_and_saveexec_b64 s[8:9], s[4:5]
	s_cbranch_execz .LBB0_872
	s_lshl_b32 s10, s22, 1
	s_and_b32 s10, s10, 14
	s_or_b32 s10, s3, s10
	s_or_b32 s10, s10, 1
	s_ashr_i32 s11, s10, 31
	s_lshl_b64 s[10:11], s[10:11], 13
	v_readlane_b32 s12, v253, 48
	s_add_u32 s10, s12, s10
	v_readlane_b32 s12, v253, 49
	s_addc_u32 s11, s12, s11
	s_lshl_b32 s12, s16, 9
	s_and_b32 s12, s12, 0x1e00
	s_add_u32 s10, s10, s12
	s_addc_u32 s11, s11, 0
	s_lshl_b32 s12, s28, 2
	s_add_u32 s10, s10, s12
	s_waitcnt lgkmcnt(0)
	v_add_f32_e32 v9, v9, v10
	s_addc_u32 s11, s11, 0
	global_atomic_add_f32 v4, v9, s[10:11] offset:20
.LBB0_872:
	s_or_b64 exec, exec, s[8:9]
	s_nop 1
	v_mov_b32_dpp v9, v3 quad_perm:[1,0,3,2] row_mask:0xf bank_mask:0xf
	s_waitcnt lgkmcnt(0)
	v_add_f32_e32 v3, v3, v9
	s_nop 1
	v_mov_b32_dpp v9, v3 quad_perm:[2,3,0,1] row_mask:0xf bank_mask:0xf
	s_waitcnt lgkmcnt(0)
	v_add_f32_e32 v3, v3, v9
	s_nop 1
	v_mov_b32_dpp v9, v3 row_half_mirror row_mask:0xf bank_mask:0xf
	s_nop 1
	v_mov_b32_dpp v9, v9 quad_perm:[3,2,1,0] row_mask:0xf bank_mask:0xf
	s_waitcnt lgkmcnt(0)
	v_add_f32_e32 v3, v3, v9
	s_nop 1
	v_mov_b32_dpp v9, v3 row_mirror row_mask:0xf bank_mask:0xf
	s_nop 1
	v_mov_b32_dpp v9, v9 row_half_mirror row_mask:0xf bank_mask:0xf
	s_and_saveexec_b64 s[8:9], s[4:5]
	s_cbranch_execz .LBB0_874
	s_lshl_b32 s10, s22, 1
	s_and_b32 s10, s10, 14
	s_or_b32 s10, s3, s10
	s_or_b32 s10, s10, 1
	s_ashr_i32 s11, s10, 31
	s_lshl_b64 s[10:11], s[10:11], 13
	v_readlane_b32 s12, v253, 48
	s_add_u32 s10, s12, s10
	v_readlane_b32 s12, v253, 49
	s_addc_u32 s11, s12, s11
	s_lshl_b32 s12, s16, 9
	s_and_b32 s12, s12, 0x1e00
	s_add_u32 s10, s10, s12
	s_addc_u32 s11, s11, 0
	s_lshl_b32 s12, s28, 2
	s_add_u32 s10, s10, s12
	s_waitcnt lgkmcnt(0)
	v_add_f32_e32 v3, v3, v9
	s_addc_u32 s11, s11, 0
	global_atomic_add_f32 v4, v3, s[10:11] offset:24
.LBB0_874:
	s_or_b64 exec, exec, s[8:9]
	s_nop 1
	v_mov_b32_dpp v3, v2 quad_perm:[1,0,3,2] row_mask:0xf bank_mask:0xf
	s_waitcnt lgkmcnt(0)
	v_add_f32_e32 v2, v2, v3
	s_nop 1
	v_mov_b32_dpp v3, v2 quad_perm:[2,3,0,1] row_mask:0xf bank_mask:0xf
	s_waitcnt lgkmcnt(0)
	v_add_f32_e32 v2, v2, v3
	s_nop 1
	v_mov_b32_dpp v3, v2 row_half_mirror row_mask:0xf bank_mask:0xf
	s_nop 1
	v_mov_b32_dpp v3, v3 quad_perm:[3,2,1,0] row_mask:0xf bank_mask:0xf
	s_waitcnt lgkmcnt(0)
	v_add_f32_e32 v2, v2, v3
	s_nop 1
	v_mov_b32_dpp v3, v2 row_mirror row_mask:0xf bank_mask:0xf
	s_nop 1
	v_mov_b32_dpp v3, v3 row_half_mirror row_mask:0xf bank_mask:0xf
	s_and_saveexec_b64 s[8:9], s[4:5]
	s_cbranch_execz .LBB0_876
	s_lshl_b32 s10, s22, 1
	s_and_b32 s10, s10, 14
	s_or_b32 s3, s3, s10
	s_or_b32 s10, s3, 1
	s_ashr_i32 s11, s10, 31
	s_lshl_b64 s[10:11], s[10:11], 13
	v_readlane_b32 s3, v253, 48
	s_add_u32 s3, s3, s10
	v_readlane_b32 s10, v253, 49
	s_addc_u32 s10, s10, s11
	s_lshl_b32 s11, s16, 9
	s_and_b32 s11, s11, 0x1e00
	s_add_u32 s3, s3, s11
	s_addc_u32 s11, s10, 0
	s_lshl_b32 s10, s28, 2
	s_add_u32 s10, s3, s10
	s_waitcnt lgkmcnt(0)
	v_add_f32_e32 v2, v2, v3
	s_addc_u32 s11, s11, 0
	global_atomic_add_f32 v4, v2, s[10:11] offset:28

; __device__ __forceinline__ float wave_sum(float v) {
; #pragma unroll
;     for (int o = 1; o < 64; o <<= 1) v += __shfl_xor(v, o);
;     return v;
; }
; __global__ void __launch_bounds__(NWAVES * 64, 2) mk_fwd(Args args) {
;     ...
;     if (IN(3)) {
;         float lam;
;         { const float s1 = wave_sum(lq1[lane] * lk1[lane] + lq1[lane + 64] * lk1[lane + 64]), s2 = wave_sum(lq2[lane] * lk2[lane] + lq2[lane + 64] * lk2[lane + 64]);
;           lam = __expf(s1) - __expf(s2) + 0.2f; lam = __uint_as_float(__builtin_amdgcn_readfirstlane(__float_as_uint(lam))); }
.LBB0_970:
	s_add_u32 s0, s78, 0x18c00000
	s_addc_u32 s1, s79, 0
	v_writelane_b32 v253, s0, 54
	s_nop 1
	v_writelane_b32 v253, s1, 55
	s_add_u32 s0, s78, 0x1b800000
	s_addc_u32 s1, s79, 0
	v_writelane_b32 v253, s0, 56
	s_nop 1
	v_writelane_b32 v253, s1, 57
	s_add_u32 s0, s78, 0x8800000
	s_addc_u32 s1, s79, 0
	v_writelane_b32 v253, s0, 58
	s_nop 1
	v_writelane_b32 v253, s1, 59
	s_add_u32 s0, s78, 0x1ac00000
	s_addc_u32 s1, s79, 0
	v_writelane_b32 v253, s0, 60
	s_nop 1
	v_writelane_b32 v253, s1, 61
	s_add_u32 s0, s78, 0x400000
	s_addc_u32 s1, s79, 0
	v_writelane_b32 v253, s0, 62
	s_cmp_lt_i32 s80, 4
	s_nop 0
	v_writelane_b32 v253, s1, 63
	s_cselect_b64 s[0:1], -1, 0
	s_cmp_gt_i32 s81, 3
	s_cselect_b64 s[2:3], -1, 0
	s_and_b64 s[0:1], s[0:1], s[2:3]
	s_andn2_b64 vcc, exec, s[0:1]
	s_cbranch_vccnz .LBB0_1654
	v_readlane_b32 s8, v253, 30
	v_lshlrev_b32_e32 v1, 2, v216
	v_readlane_b32 s18, v253, 40
	v_readlane_b32 s19, v253, 41
	v_readlane_b32 s20, v253, 42
	v_readlane_b32 s21, v253, 43
	s_nop 2
	global_load_dword v2, v1, s[18:19]
	s_waitcnt lgkmcnt(0)
	global_load_dword v3, v1, s[20:21]
	global_load_dword v4, v1, s[18:19] offset:256
	global_load_dword v5, v1, s[20:21] offset:256
	v_readlane_b32 s9, v253, 31
	v_readlane_b32 s10, v253, 32
	v_readlane_b32 s11, v253, 33
	v_readlane_b32 s12, v253, 34
	v_readlane_b32 s13, v253, 35
	v_readlane_b32 s14, v253, 36
	v_readlane_b32 s15, v253, 37
	v_readlane_b32 s16, v253, 38
	v_readlane_b32 s17, v253, 39
	v_readlane_b32 s4, v253, 10
	v_readlane_b32 s22, v253, 44
	v_readlane_b32 s23, v253, 45
	v_readlane_b32 s5, v253, 11
	s_ashr_i32 s83, s82, 31
	v_writelane_b32 v252, s80, 0
	s_mov_b32 s87, 0
	v_readlane_b32 s6, v253, 12
	v_writelane_b32 v252, s81, 1
	v_readlane_b32 s7, v253, 13
	v_readlane_b32 s10, v253, 16
	v_readlane_b32 s11, v253, 17
	s_movk_i32 s52, 0x104
	s_mov_b32 s94, 0x43000000
	s_mov_b32 s95, 0xc3e00000
	s_mov_b32 s92, 0x42800000
	s_mov_b32 s54, 0x3b800000
	s_mov_b32 s96, 0x3a0293ee
	s_mov_b32 s53, 0x800000
	v_mov_b32_e32 v199, 0x43e00000
	v_mov_b32_e32 v210, 0xff800000
	v_mov_b32_e32 v211, 0xf149f2ca
	v_mov_b32_e32 v198, 0x3727c5ac
	s_mov_b32 s28, 0
	s_mov_b32 s30, 0
	s_mov_b32 s29, 0
	s_mov_b32 s33, 0
	v_readlane_b32 s8, v253, 14
	v_readlane_b32 s9, v253, 15
	v_readlane_b32 s12, v253, 18
	v_readlane_b32 s13, v253, 19
	v_readlane_b32 s14, v253, 20
	v_readlane_b32 s15, v253, 21
	v_readlane_b32 s16, v253, 22
	v_readlane_b32 s17, v253, 23
	v_readlane_b32 s18, v253, 24
	v_readlane_b32 s19, v253, 25
	s_waitcnt vmcnt(0)
	v_mul_f32_e32 v4, v4, v5
	v_fmac_f32_e32 v4, v2, v3
	v_mbcnt_lo_u32_b32 v2, -1, 0
	v_mbcnt_hi_u32_b32 v2, -1, v2
	v_and_b32_e32 v3, 64, v2
	v_add_u32_e32 v3, 64, v3
	v_xor_b32_e32 v5, 1, v2
	v_cmp_lt_i32_e32 vcc, v5, v3
	s_nop 1
	v_cndmask_b32_e32 v5, v2, v5, vcc
	v_lshlrev_b32_e32 v5, 2, v5
	s_nop 1
	v_mov_b32_dpp v6, v4 quad_perm:[1,0,3,2] row_mask:0xf bank_mask:0xf
	s_waitcnt lgkmcnt(0)
	v_add_f32_e32 v4, v4, v6
	v_xor_b32_e32 v6, 2, v2
	v_cmp_lt_i32_e32 vcc, v6, v3
	s_nop 1
	v_cndmask_b32_e32 v6, v2, v6, vcc
	v_lshlrev_b32_e32 v6, 2, v6
	s_nop 1
	v_mov_b32_dpp v7, v4 quad_perm:[2,3,0,1] row_mask:0xf bank_mask:0xf
	s_waitcnt lgkmcnt(0)
	v_add_f32_e32 v4, v4, v7
	v_xor_b32_e32 v7, 4, v2
	v_cmp_lt_i32_e32 vcc, v7, v3
	s_nop 1
	v_cndmask_b32_e32 v7, v2, v7, vcc
	v_lshlrev_b32_e32 v7, 2, v7
	s_nop 1
	v_mov_b32_dpp v8, v4 row_half_mirror row_mask:0xf bank_mask:0xf
	s_nop 1
	v_mov_b32_dpp v8, v8 quad_perm:[3,2,1,0] row_mask:0xf bank_mask:0xf
	s_waitcnt lgkmcnt(0)
	v_add_f32_e32 v4, v4, v8
	v_xor_b32_e32 v8, 8, v2
	v_cmp_lt_i32_e32 vcc, v8, v3
	s_nop 1
	v_cndmask_b32_e32 v8, v2, v8, vcc
	v_lshlrev_b32_e32 v8, 2, v8
	s_nop 1
	v_mov_b32_dpp v9, v4 row_mirror row_mask:0xf bank_mask:0xf
	s_nop 1
	v_mov_b32_dpp v9, v9 row_half_mirror row_mask:0xf bank_mask:0xf
	s_waitcnt lgkmcnt(0)
	v_add_f32_e32 v4, v4, v9
	v_xor_b32_e32 v9, 16, v2
	v_cmp_lt_i32_e32 vcc, v9, v3
	s_nop 1
	v_cndmask_b32_e32 v9, v2, v9, vcc
	v_lshlrev_b32_e32 v9, 2, v9
	v_mov_b32_e32 v10, v4
	s_nop 1
	v_permlane16_swap_b32_e32 v4, v10
	s_waitcnt lgkmcnt(0)
; __global__ void __launch_bounds__(NWAVES * 64, 2) mk_fwd(Args args) {
;     ...
;         float lam;
;         { const float s1 = wave_sum(lq1[lane] * lk1[lane] + lq1[lane + 64] * lk1[lane + 64]), s2 = wave_sum(lq2[lane] * lk2[lane] + lq2[lane + 64] * lk2[lane + 64]);
;           lam = __expf(s1) - __expf(s2) + 0.2f; lam = __uint_as_float(__builtin_amdgcn_readfirstlane(__float_as_uint(lam))); }
;         att::Seam S;
;         float* const scrw = SCR + ((size_t)bx * NWAVES + wave) * 8192;
;         float* const ssqw = (float*)((char*)lds + RING_OFF + att::LDS_SSQ) + wave * 32;
;         constexpr size_t GRP = (size_t)64 * 4096 * 128;
	v_add_f32_e32 v4, v4, v10
	v_xor_b32_e32 v10, 32, v2
	v_cmp_lt_i32_e32 vcc, v10, v3
	s_nop 1
	v_cndmask_b32_e32 v2, v2, v10, vcc
	v_lshlrev_b32_e32 v2, 2, v2
	ds_bpermute_b32 v3, v2, v4
	s_waitcnt lgkmcnt(0)
	v_add_f32_e32 v3, v4, v3
	global_load_dword v4, v1, s[22:23]
	global_load_dword v10, v1, s[4:5]
	global_load_dword v11, v1, s[22:23] offset:256
	s_nop 0
	global_load_dword v1, v1, s[4:5] offset:256
	s_waitcnt vmcnt(0)
	v_mul_f32_e32 v1, v11, v1
	v_fmac_f32_e32 v1, v4, v10
	s_nop 1
	v_mov_b32_dpp v4, v1 quad_perm:[1,0,3,2] row_mask:0xf bank_mask:0xf
	s_waitcnt lgkmcnt(0)
	v_add_f32_e32 v1, v1, v4
	s_nop 1
	v_mov_b32_dpp v4, v1 quad_perm:[2,3,0,1] row_mask:0xf bank_mask:0xf
	s_waitcnt lgkmcnt(0)
	v_add_f32_e32 v1, v1, v4
	s_nop 1
	v_mov_b32_dpp v4, v1 row_half_mirror row_mask:0xf bank_mask:0xf
	s_nop 1
	v_mov_b32_dpp v4, v4 quad_perm:[3,2,1,0] row_mask:0xf bank_mask:0xf
	s_waitcnt lgkmcnt(0)
	v_add_f32_e32 v1, v1, v4
	s_nop 1
	v_mov_b32_dpp v4, v1 row_mirror row_mask:0xf bank_mask:0xf
	s_nop 1
	v_mov_b32_dpp v4, v4 row_half_mirror row_mask:0xf bank_mask:0xf
	s_waitcnt lgkmcnt(0)
	v_add_f32_e32 v1, v1, v4
	v_mov_b32_e32 v4, v1
	s_nop 1
	v_permlane16_swap_b32_e32 v1, v4
	s_waitcnt lgkmcnt(0)
	v_add_f32_e32 v1, v1, v4
	v_mov_b32_e32 v2, v1
	s_nop 1
	v_permlane32_swap_b32_e32 v1, v2
	s_waitcnt lgkmcnt(0)
	v_add_f32_e32 v1, v1, v2
	v_mul_f32_e32 v2, 0x3fb8aa3b, v3
	v_mul_f32_e32 v1, 0x3fb8aa3b, v1
	v_exp_f32_e32 v2, v2
	v_exp_f32_e32 v1, v1
	v_mov_b32_e32 v3, 0
	v_sub_f32_e32 v1, v2, v1
	s_nop 0
	v_readfirstlane_b32 s0, v1
	v_mov_b32_e32 v1, 0x3e4ccccd
	s_nop 0
	v_add_f32_e32 v2, s0, v1
	s_mov_b32 s0, s82
	v_writelane_b32 v252, s0, 2
	v_mov_b32_e32 v1, 0x40a00000
	v_xor_b32_e32 v212, 0x80000000, v2
	v_writelane_b32 v252, s1, 3
	s_lshl_b64 s[0:1], s[82:83], 18
	s_add_u32 s2, s78, s0
	s_addc_u32 s3, s79, s1
	s_lshl_b64 s[0:1], s[86:87], 15
	s_add_u32 s0, s2, s0
	s_addc_u32 s1, s3, s1
	s_add_u32 s0, s0, 0x37c00000
	s_addc_u32 s1, s1, 0
	v_writelane_b32 v252, s0, 4
	s_nop 1
	v_writelane_b32 v252, s1, 5
	s_mul_i32 s0, s86, 0x4100
	s_add_i32 s82, s0, 0
	v_readlane_b32 s0, v253, 0
	v_readlane_b32 s1, v253, 1
	s_cmp_lg_u64 s[0:1], 0
	s_cselect_b64 s[68:69], -1, 0
	s_add_u32 s0, s78, 0x1ae00000
	s_addc_u32 s1, s79, 0
	v_readlane_b32 s2, v253, 2
	v_readlane_b32 s3, v253, 3
	v_writelane_b32 v252, s0, 6
	v_cmp_eq_u32_e64 s[2:3], 0, v0
	s_cmp_lg_u64 s[10:11], 0
	v_writelane_b32 v252, s1, 7
	v_writelane_b32 v252, s2, 8
	s_cselect_b64 s[0:1], -1, 0
	v_readlane_b32 s4, v253, 4
	v_writelane_b32 v252, s3, 9
	s_add_u32 s2, s78, 0x1fc00000
	v_writelane_b32 v252, s2, 10
	s_addc_u32 s2, s79, 0
	v_writelane_b32 v252, s2, 11
	s_add_u32 s2, s78, 0x23c00000
	v_writelane_b32 v252, s2, 12
	s_addc_u32 s2, s79, 0
	v_writelane_b32 v252, s2, 13
	s_add_u32 s2, s78, 0x27c00000
	v_writelane_b32 v252, s2, 14
	s_addc_u32 s2, s79, 0
	v_writelane_b32 v252, s2, 15
	s_add_u32 s2, s78, 0x2bc00000
	v_writelane_b32 v252, s2, 16
	s_addc_u32 s2, s79, 0
	v_writelane_b32 v252, s2, 17
	s_add_u32 s2, s78, 0x2fc00000
	v_writelane_b32 v252, s2, 18
	v_writelane_b32 v252, s76, 19
	s_addc_u32 s2, s79, 0
	s_lshl_b32 s83, s75, 9
	v_writelane_b32 v252, s77, 20
	v_writelane_b32 v252, s78, 21
	v_writelane_b32 v252, s79, 22
	v_writelane_b32 v252, s2, 23
	s_add_i32 s2, s90, 0xffffa800
	v_writelane_b32 v252, s2, 24
	v_writelane_b32 v252, s75, 25
	s_add_i32 s2, s90, 0xffffe800
	v_writelane_b32 v252, s2, 26
	s_add_i32 s2, s90, 0xffffea00
	v_writelane_b32 v252, s2, 27
	s_add_i32 s2, s90, 0xffffee00
	v_writelane_b32 v252, s2, 28
	s_add_i32 s2, s90, 0xfffff000
	s_add_u32 s76, s10, 32
	v_writelane_b32 v252, s2, 29
	s_addc_u32 s77, s11, 0
	s_add_i32 s4, 0, 0x21180
	v_writelane_b32 v252, s4, 30
	s_add_i32 s4, 0, 0x11000
	v_readlane_b32 s5, v253, 5
	v_writelane_b32 v252, s4, 31
	s_mov_b32 s4, s90
	v_writelane_b32 v252, s4, 32
	s_mov_b64 s[74:75], 0x40000
	s_mov_b64 s[2:3], 0x10000
	v_writelane_b32 v252, s5, 33
	v_writelane_b32 v252, s88, 34
	v_readlane_b32 s6, v253, 6
	v_readlane_b32 s7, v253, 7
	v_writelane_b32 v252, s89, 35
	v_writelane_b32 v252, s76, 36
	s_nop 1
	v_writelane_b32 v252, s77, 37
	s_branch .LBB0_975

; __device__ __forceinline__ unsigned cvt_pk_bf16(float lo, float hi) { unsigned r; asm volatile("v_cvt_pk_bf16_f32 %0, %1, %2" : "=v"(r) : "v"(lo), "v"(hi)); return r; }
;     __device__ __forceinline__ void operator()(const f32x4 (&acc)[2][2][4][2], const Unit& u, int wr, int wc, int fr, int fq) const {
;     ...
;                     const f32x4 v0 = a0 + acc[ai][bj][m][0] * sc, v1 = a1 + acc[ai][bj][m][1] * sc;
;                     q += ((v0[0] * v0[0] + v0[1] * v0[1]) + (v0[2] * v0[2] + v0[3] * v0[3])) + ((v1[0] * v1[0] + v1[1] * v1[1]) + (v1[2] * v1[2] + v1[3] * v1[3]));
;                     u32x4 wo; wo.x = cvt_pk_bf16(v0[0], v0[1]); wo.y = cvt_pk_bf16(v0[2], v0[3]); wo.z = cvt_pk_bf16(v1[0], v1[1]); wo.w = cvt_pk_bf16(v1[2], v1[3]);
;                     *(u32x4*)(xb + o2) = wo;
;                     if (x8) { u32x2 w8; w8.x = pk4_fp8(v0[0], v0[1], v0[2], v0[3]); w8.y = pk4_fp8(v1[0], v1[1], v1[2], v1[3]); *(u32x2*)(x8 + o2) = w8; } }
;                 q += __shfl_xor(q, 16); q += __shfl_xor(q, 32);
;                 if (fq == 0) unsafeAtomicAdd(ss + row, q);
.LBB0_1682:
	v_mul_f32_e32 v148, v159, v159
	v_mul_f32_e32 v149, v161, v161
	v_fmac_f32_e32 v148, v158, v158
	v_fmac_f32_e32 v149, v160, v160
	v_add_f32_e32 v148, v148, v149
	v_mul_f32_e32 v149, v155, v155
	v_mul_f32_e32 v152, v157, v157
	v_fmac_f32_e32 v149, v154, v154
	v_fmac_f32_e32 v152, v156, v156
	v_add_f32_e32 v149, v149, v152
	v_add_f32_e32 v148, v148, v149
	v_mul_f32_e32 v149, v151, v151
	v_mul_f32_e32 v27, v27, v27
	v_fmac_f32_e32 v149, v150, v150
	v_fmac_f32_e32 v27, v26, v26
	v_add_f32_e32 v26, v149, v27
	v_mul_f32_e32 v27, v147, v147
	v_mul_f32_e32 v29, v29, v29
	v_fmac_f32_e32 v27, v146, v146
	v_fmac_f32_e32 v29, v28, v28
	v_add_f32_e32 v27, v27, v29
	v_and_b32_e32 v28, 64, v199
	v_add_f32_e32 v26, v26, v27
	v_xor_b32_e32 v27, 16, v199
	v_add_u32_e32 v28, 64, v28
	v_cmp_lt_i32_e32 vcc, v27, v28
	v_add_f32_e32 v26, v148, v26
	s_nop 0
	v_cndmask_b32_e32 v27, v199, v27, vcc
	v_lshlrev_b32_e32 v146, 2, v27
	v_mov_b32_e32 v27, v26
	s_nop 1
	v_permlane16_swap_b32_e32 v26, v27
	s_waitcnt lgkmcnt(0)
	v_add_f32_e32 v26, v26, v27
	v_xor_b32_e32 v27, 32, v199
	v_cmp_lt_i32_e32 vcc, v27, v28
	s_nop 1
	v_cndmask_b32_e32 v27, v199, v27, vcc
	v_lshlrev_b32_e32 v147, 2, v27
	v_mov_b32_e32 v27, v26
	s_nop 1
	v_permlane32_swap_b32_e32 v26, v27
	s_and_saveexec_b64 s[28:29], s[0:1]
	s_cbranch_execz .LBB0_1684
	v_lshl_add_u64 v[28:29], v[178:179], 2, s[2:3]
	s_waitcnt lgkmcnt(0)
	v_add_f32_e32 v26, v26, v27
	global_atomic_add_f32 v[28:29], v26, off

; __device__ __forceinline__ unsigned cvt_pk_bf16(float lo, float hi) { unsigned r; asm volatile("v_cvt_pk_bf16_f32 %0, %1, %2" : "=v"(r) : "v"(lo), "v"(hi)); return r; }
;     __device__ __forceinline__ void operator()(const f32x4 (&acc)[2][2][4][2], const Unit& u, int wr, int wc, int fr, int fq) const {
;     ...
;                     const f32x4 v0 = a0 + acc[ai][bj][m][0] * sc, v1 = a1 + acc[ai][bj][m][1] * sc;
;                     q += ((v0[0] * v0[0] + v0[1] * v0[1]) + (v0[2] * v0[2] + v0[3] * v0[3])) + ((v1[0] * v1[0] + v1[1] * v1[1]) + (v1[2] * v1[2] + v1[3] * v1[3]));
;                     u32x4 wo; wo.x = cvt_pk_bf16(v0[0], v0[1]); wo.y = cvt_pk_bf16(v0[2], v0[3]); wo.z = cvt_pk_bf16(v1[0], v1[1]); wo.w = cvt_pk_bf16(v1[2], v1[3]);
;                     *(u32x4*)(xb + o2) = wo;
;                     if (x8) { u32x2 w8; w8.x = pk4_fp8(v0[0], v0[1], v0[2], v0[3]); w8.y = pk4_fp8(v1[0], v1[1], v1[2], v1[3]); *(u32x2*)(x8 + o2) = w8; } }
;                 q += __shfl_xor(q, 16); q += __shfl_xor(q, 32);
;                 if (fq == 0) unsafeAtomicAdd(ss + row, q);
.LBB0_1688:
	v_mul_f32_e32 v26, v29, v29
	v_mul_f32_e32 v23, v23, v23
	v_fmac_f32_e32 v26, v28, v28
	v_fmac_f32_e32 v23, v22, v22
	v_add_f32_e32 v22, v26, v23
	v_mul_f32_e32 v23, v139, v139
	v_mul_f32_e32 v25, v25, v25
	v_fmac_f32_e32 v23, v138, v138
	v_fmac_f32_e32 v25, v24, v24
	v_add_f32_e32 v23, v23, v25
	v_add_f32_e32 v22, v22, v23
	v_mul_f32_e32 v23, v135, v135
	v_mul_f32_e32 v19, v19, v19
	v_fmac_f32_e32 v23, v134, v134
	v_fmac_f32_e32 v19, v18, v18
	v_add_f32_e32 v18, v23, v19
	v_mul_f32_e32 v19, v131, v131
	v_mul_f32_e32 v21, v21, v21
	v_fmac_f32_e32 v19, v130, v130
	v_fmac_f32_e32 v21, v20, v20
	v_add_f32_e32 v19, v19, v21
	v_add_f32_e32 v18, v18, v19
	v_add_f32_e32 v18, v22, v18
	v_mov_b32_e32 v19, v18
	s_nop 1
	v_permlane16_swap_b32_e32 v18, v19
	s_waitcnt lgkmcnt(0)
	v_add_f32_e32 v18, v18, v19
	v_mov_b32_e32 v19, v18
	s_nop 1
	v_permlane32_swap_b32_e32 v18, v19
	s_and_saveexec_b64 s[28:29], s[0:1]
	s_cbranch_execz .LBB0_1690
	v_lshl_add_u64 v[20:21], v[188:189], 2, s[2:3]
	s_waitcnt lgkmcnt(0)
	v_add_f32_e32 v18, v18, v19
	global_atomic_add_f32 v[20:21], v18, off

; __device__ __forceinline__ unsigned cvt_pk_bf16(float lo, float hi) { unsigned r; asm volatile("v_cvt_pk_bf16_f32 %0, %1, %2" : "=v"(r) : "v"(lo), "v"(hi)); return r; }
;     __device__ __forceinline__ void operator()(const f32x4 (&acc)[2][2][4][2], const Unit& u, int wr, int wc, int fr, int fq) const {
;     ...
;                     const f32x4 v0 = a0 + acc[ai][bj][m][0] * sc, v1 = a1 + acc[ai][bj][m][1] * sc;
;                     q += ((v0[0] * v0[0] + v0[1] * v0[1]) + (v0[2] * v0[2] + v0[3] * v0[3])) + ((v1[0] * v1[0] + v1[1] * v1[1]) + (v1[2] * v1[2] + v1[3] * v1[3]));
;                     u32x4 wo; wo.x = cvt_pk_bf16(v0[0], v0[1]); wo.y = cvt_pk_bf16(v0[2], v0[3]); wo.z = cvt_pk_bf16(v1[0], v1[1]); wo.w = cvt_pk_bf16(v1[2], v1[3]);
;                     *(u32x4*)(xb + o2) = wo;
;                     if (x8) { u32x2 w8; w8.x = pk4_fp8(v0[0], v0[1], v0[2], v0[3]); w8.y = pk4_fp8(v1[0], v1[1], v1[2], v1[3]); *(u32x2*)(x8 + o2) = w8; } }
;                 q += __shfl_xor(q, 16); q += __shfl_xor(q, 32);
;                 if (fq == 0) unsafeAtomicAdd(ss + row, q);
.LBB0_1694:
	v_mul_f32_e32 v18, v21, v21
	v_mul_f32_e32 v15, v15, v15
	v_fmac_f32_e32 v18, v20, v20
	v_fmac_f32_e32 v15, v14, v14
	v_add_f32_e32 v14, v18, v15
	v_mul_f32_e32 v15, v23, v23
	v_mul_f32_e32 v17, v17, v17
	v_fmac_f32_e32 v15, v22, v22
	v_fmac_f32_e32 v17, v16, v16
	v_add_f32_e32 v15, v15, v17
	v_add_f32_e32 v14, v14, v15
	v_mul_f32_e32 v15, v25, v25
	v_mul_f32_e32 v11, v11, v11
	v_fmac_f32_e32 v15, v24, v24
	v_fmac_f32_e32 v11, v10, v10
	v_add_f32_e32 v10, v15, v11
	v_mul_f32_e32 v11, v27, v27
	v_mul_f32_e32 v13, v13, v13
	v_fmac_f32_e32 v11, v26, v26
	v_fmac_f32_e32 v13, v12, v12
	v_add_f32_e32 v11, v11, v13
	v_add_f32_e32 v10, v10, v11
	v_add_f32_e32 v10, v14, v10
	v_mov_b32_e32 v11, v10
	s_nop 1
	v_permlane16_swap_b32_e32 v10, v11
	s_waitcnt lgkmcnt(0)
	v_add_f32_e32 v10, v10, v11
	v_mov_b32_e32 v11, v10
	s_nop 1
	v_permlane32_swap_b32_e32 v10, v11
	s_and_saveexec_b64 s[28:29], s[0:1]
	s_cbranch_execz .LBB0_1696
	v_lshl_add_u64 v[12:13], v[184:185], 2, s[2:3]
	s_waitcnt lgkmcnt(0)
	v_add_f32_e32 v10, v10, v11
	global_atomic_add_f32 v[12:13], v10, off

; __device__ __forceinline__ unsigned cvt_pk_bf16(float lo, float hi) { unsigned r; asm volatile("v_cvt_pk_bf16_f32 %0, %1, %2" : "=v"(r) : "v"(lo), "v"(hi)); return r; }
;     __device__ __forceinline__ void operator()(const f32x4 (&acc)[2][2][4][2], const Unit& u, int wr, int wc, int fr, int fq) const {
;     ...
;                     const f32x4 v0 = a0 + acc[ai][bj][m][0] * sc, v1 = a1 + acc[ai][bj][m][1] * sc;
;                     q += ((v0[0] * v0[0] + v0[1] * v0[1]) + (v0[2] * v0[2] + v0[3] * v0[3])) + ((v1[0] * v1[0] + v1[1] * v1[1]) + (v1[2] * v1[2] + v1[3] * v1[3]));
;                     u32x4 wo; wo.x = cvt_pk_bf16(v0[0], v0[1]); wo.y = cvt_pk_bf16(v0[2], v0[3]); wo.z = cvt_pk_bf16(v1[0], v1[1]); wo.w = cvt_pk_bf16(v1[2], v1[3]);
;                     *(u32x4*)(xb + o2) = wo;
;                     if (x8) { u32x2 w8; w8.x = pk4_fp8(v0[0], v0[1], v0[2], v0[3]); w8.y = pk4_fp8(v1[0], v1[1], v1[2], v1[3]); *(u32x2*)(x8 + o2) = w8; } }
;                 q += __shfl_xor(q, 16); q += __shfl_xor(q, 32);
;                 if (fq == 0) unsafeAtomicAdd(ss + row, q);
.LBB0_1700:
	v_mul_f32_e32 v10, v13, v13
	v_mul_f32_e32 v7, v7, v7
	v_fmac_f32_e32 v10, v12, v12
	v_fmac_f32_e32 v7, v6, v6
	v_add_f32_e32 v6, v10, v7
	v_mul_f32_e32 v7, v15, v15
	v_mul_f32_e32 v9, v9, v9
	v_fmac_f32_e32 v7, v14, v14
	v_fmac_f32_e32 v9, v8, v8
	v_add_f32_e32 v7, v7, v9
	v_add_f32_e32 v6, v6, v7
	v_mul_f32_e32 v7, v17, v17
	v_mul_f32_e32 v3, v3, v3
	v_fmac_f32_e32 v7, v16, v16
	v_fmac_f32_e32 v3, v2, v2
	v_add_f32_e32 v2, v7, v3
	v_mul_f32_e32 v3, v19, v19
	v_mul_f32_e32 v5, v5, v5
	v_fmac_f32_e32 v3, v18, v18
	v_fmac_f32_e32 v5, v4, v4
	v_add_f32_e32 v3, v3, v5
	v_add_f32_e32 v2, v2, v3
	v_add_f32_e32 v2, v6, v2
	v_mov_b32_e32 v3, v2
	s_nop 1
	v_permlane16_swap_b32_e32 v2, v3
	s_waitcnt lgkmcnt(0)
	v_add_f32_e32 v2, v2, v3
	v_mov_b32_e32 v3, v2
	s_nop 1
	v_permlane32_swap_b32_e32 v2, v3
	s_and_saveexec_b64 s[28:29], s[0:1]
	s_cbranch_execz .LBB0_1702
	v_lshl_add_u64 v[4:5], v[180:181], 2, s[2:3]
	s_waitcnt lgkmcnt(0)
	v_add_f32_e32 v2, v2, v3
	global_atomic_add_f32 v[4:5], v2, off

; __device__ __forceinline__ unsigned cvt_pk_bf16(float lo, float hi) { unsigned r; asm volatile("v_cvt_pk_bf16_f32 %0, %1, %2" : "=v"(r) : "v"(lo), "v"(hi)); return r; }
;     __device__ __forceinline__ void operator()(const f32x4 (&acc)[2][2][4][2], const Unit& u, int wr, int wc, int fr, int fq) const {
;     ...
;                     const f32x4 v0 = a0 + acc[ai][bj][m][0] * sc, v1 = a1 + acc[ai][bj][m][1] * sc;
;                     q += ((v0[0] * v0[0] + v0[1] * v0[1]) + (v0[2] * v0[2] + v0[3] * v0[3])) + ((v1[0] * v1[0] + v1[1] * v1[1]) + (v1[2] * v1[2] + v1[3] * v1[3]));
;                     u32x4 wo; wo.x = cvt_pk_bf16(v0[0], v0[1]); wo.y = cvt_pk_bf16(v0[2], v0[3]); wo.z = cvt_pk_bf16(v1[0], v1[1]); wo.w = cvt_pk_bf16(v1[2], v1[3]);
;                     *(u32x4*)(xb + o2) = wo;
;                     if (x8) { u32x2 w8; w8.x = pk4_fp8(v0[0], v0[1], v0[2], v0[3]); w8.y = pk4_fp8(v1[0], v1[1], v1[2], v1[3]); *(u32x2*)(x8 + o2) = w8; } }
;                 q += __shfl_xor(q, 16); q += __shfl_xor(q, 32);
;                 if (fq == 0) unsafeAtomicAdd(ss + row, q);
.LBB0_1706:
	v_mul_f32_e32 v84, v95, v95
	v_mul_f32_e32 v85, v97, v97
	v_fmac_f32_e32 v84, v94, v94
	v_fmac_f32_e32 v85, v96, v96
	v_add_f32_e32 v84, v84, v85
	v_mul_f32_e32 v85, v91, v91
	v_mul_f32_e32 v88, v93, v93
	v_fmac_f32_e32 v85, v90, v90
	v_fmac_f32_e32 v88, v92, v92
	v_add_f32_e32 v85, v85, v88
	v_add_f32_e32 v84, v84, v85
	v_mul_f32_e32 v85, v87, v87
	v_mul_f32_e32 v27, v27, v27
	v_fmac_f32_e32 v85, v86, v86
	v_fmac_f32_e32 v27, v26, v26
	v_add_f32_e32 v26, v85, v27
	v_mul_f32_e32 v27, v83, v83
	v_mul_f32_e32 v29, v29, v29
	v_fmac_f32_e32 v27, v82, v82
	v_fmac_f32_e32 v29, v28, v28
	v_add_f32_e32 v27, v27, v29
	v_add_f32_e32 v26, v26, v27
	v_add_f32_e32 v26, v84, v26
	v_mov_b32_e32 v27, v26
	s_nop 1
	v_permlane16_swap_b32_e32 v26, v27
	s_waitcnt lgkmcnt(0)
	v_add_f32_e32 v26, v26, v27
	v_mov_b32_e32 v27, v26
	s_nop 1
	v_permlane32_swap_b32_e32 v26, v27
	s_and_saveexec_b64 s[28:29], s[0:1]
	s_cbranch_execz .LBB0_1708
	v_lshl_add_u64 v[28:29], v[108:109], 2, s[2:3]
	s_waitcnt lgkmcnt(0)
	v_add_f32_e32 v26, v26, v27
	global_atomic_add_f32 v[28:29], v26, off

; __device__ __forceinline__ unsigned cvt_pk_bf16(float lo, float hi) { unsigned r; asm volatile("v_cvt_pk_bf16_f32 %0, %1, %2" : "=v"(r) : "v"(lo), "v"(hi)); return r; }
;     __device__ __forceinline__ void operator()(const f32x4 (&acc)[2][2][4][2], const Unit& u, int wr, int wc, int fr, int fq) const {
;     ...
;                     const f32x4 v0 = a0 + acc[ai][bj][m][0] * sc, v1 = a1 + acc[ai][bj][m][1] * sc;
;                     q += ((v0[0] * v0[0] + v0[1] * v0[1]) + (v0[2] * v0[2] + v0[3] * v0[3])) + ((v1[0] * v1[0] + v1[1] * v1[1]) + (v1[2] * v1[2] + v1[3] * v1[3]));
;                     u32x4 wo; wo.x = cvt_pk_bf16(v0[0], v0[1]); wo.y = cvt_pk_bf16(v0[2], v0[3]); wo.z = cvt_pk_bf16(v1[0], v1[1]); wo.w = cvt_pk_bf16(v1[2], v1[3]);
;                     *(u32x4*)(xb + o2) = wo;
;                     if (x8) { u32x2 w8; w8.x = pk4_fp8(v0[0], v0[1], v0[2], v0[3]); w8.y = pk4_fp8(v1[0], v1[1], v1[2], v1[3]); *(u32x2*)(x8 + o2) = w8; } }
;                 q += __shfl_xor(q, 16); q += __shfl_xor(q, 32);
;                 if (fq == 0) unsafeAtomicAdd(ss + row, q);
.LBB0_1712:
	v_mul_f32_e32 v26, v29, v29
	v_mul_f32_e32 v23, v23, v23
	v_fmac_f32_e32 v26, v28, v28
	v_fmac_f32_e32 v23, v22, v22
	v_add_f32_e32 v22, v26, v23
	v_mul_f32_e32 v23, v75, v75
	v_mul_f32_e32 v25, v25, v25
	v_fmac_f32_e32 v23, v74, v74
	v_fmac_f32_e32 v25, v24, v24
	v_add_f32_e32 v23, v23, v25
	v_add_f32_e32 v22, v22, v23
	v_mul_f32_e32 v23, v71, v71
	v_mul_f32_e32 v19, v19, v19
	v_fmac_f32_e32 v23, v70, v70
	v_fmac_f32_e32 v19, v18, v18
	v_add_f32_e32 v18, v23, v19
	v_mul_f32_e32 v19, v67, v67
	v_mul_f32_e32 v21, v21, v21
	v_fmac_f32_e32 v19, v66, v66
	v_fmac_f32_e32 v21, v20, v20
	v_add_f32_e32 v19, v19, v21
	v_add_f32_e32 v18, v18, v19
	v_add_f32_e32 v18, v22, v18
	v_mov_b32_e32 v19, v18
	s_nop 1
	v_permlane16_swap_b32_e32 v18, v19
	s_waitcnt lgkmcnt(0)
	v_add_f32_e32 v18, v18, v19
	v_mov_b32_e32 v19, v18
	s_nop 1
	v_permlane32_swap_b32_e32 v18, v19
	s_and_saveexec_b64 s[28:29], s[0:1]
	s_cbranch_execz .LBB0_1714
	v_lshl_add_u64 v[20:21], v[104:105], 2, s[2:3]
	s_waitcnt lgkmcnt(0)
	v_add_f32_e32 v18, v18, v19
	global_atomic_add_f32 v[20:21], v18, off

; __device__ __forceinline__ unsigned cvt_pk_bf16(float lo, float hi) { unsigned r; asm volatile("v_cvt_pk_bf16_f32 %0, %1, %2" : "=v"(r) : "v"(lo), "v"(hi)); return r; }
;     __device__ __forceinline__ void operator()(const f32x4 (&acc)[2][2][4][2], const Unit& u, int wr, int wc, int fr, int fq) const {
;     ...
;                     const f32x4 v0 = a0 + acc[ai][bj][m][0] * sc, v1 = a1 + acc[ai][bj][m][1] * sc;
;                     q += ((v0[0] * v0[0] + v0[1] * v0[1]) + (v0[2] * v0[2] + v0[3] * v0[3])) + ((v1[0] * v1[0] + v1[1] * v1[1]) + (v1[2] * v1[2] + v1[3] * v1[3]));
;                     u32x4 wo; wo.x = cvt_pk_bf16(v0[0], v0[1]); wo.y = cvt_pk_bf16(v0[2], v0[3]); wo.z = cvt_pk_bf16(v1[0], v1[1]); wo.w = cvt_pk_bf16(v1[2], v1[3]);
;                     *(u32x4*)(xb + o2) = wo;
;                     if (x8) { u32x2 w8; w8.x = pk4_fp8(v0[0], v0[1], v0[2], v0[3]); w8.y = pk4_fp8(v1[0], v1[1], v1[2], v1[3]); *(u32x2*)(x8 + o2) = w8; } }
;                 q += __shfl_xor(q, 16); q += __shfl_xor(q, 32);
;                 if (fq == 0) unsafeAtomicAdd(ss + row, q);
.LBB0_1718:
	v_mul_f32_e32 v18, v21, v21
	v_mul_f32_e32 v15, v15, v15
	v_fmac_f32_e32 v18, v20, v20
	v_fmac_f32_e32 v15, v14, v14
	v_add_f32_e32 v14, v18, v15
	v_mul_f32_e32 v15, v23, v23
	v_mul_f32_e32 v17, v17, v17
	v_fmac_f32_e32 v15, v22, v22
	v_fmac_f32_e32 v17, v16, v16
	v_add_f32_e32 v15, v15, v17
	v_add_f32_e32 v14, v14, v15
	v_mul_f32_e32 v15, v25, v25
	v_mul_f32_e32 v11, v11, v11
	v_fmac_f32_e32 v15, v24, v24
	v_fmac_f32_e32 v11, v10, v10
	v_add_f32_e32 v10, v15, v11
	v_mul_f32_e32 v11, v27, v27
	v_mul_f32_e32 v13, v13, v13
	v_fmac_f32_e32 v11, v26, v26
	v_fmac_f32_e32 v13, v12, v12
	v_add_f32_e32 v11, v11, v13
	v_add_f32_e32 v10, v10, v11
	v_add_f32_e32 v10, v14, v10
	v_mov_b32_e32 v11, v10
	s_nop 1
	v_permlane16_swap_b32_e32 v10, v11
	s_waitcnt lgkmcnt(0)
	v_add_f32_e32 v10, v10, v11
	v_mov_b32_e32 v11, v10
	s_nop 1
	v_permlane32_swap_b32_e32 v10, v11
	s_and_saveexec_b64 s[28:29], s[0:1]
	s_cbranch_execz .LBB0_1720
	v_lshl_add_u64 v[12:13], v[100:101], 2, s[2:3]
	s_waitcnt lgkmcnt(0)
	v_add_f32_e32 v10, v10, v11
	global_atomic_add_f32 v[12:13], v10, off

; __device__ __forceinline__ unsigned cvt_pk_bf16(float lo, float hi) { unsigned r; asm volatile("v_cvt_pk_bf16_f32 %0, %1, %2" : "=v"(r) : "v"(lo), "v"(hi)); return r; }
;     __device__ __forceinline__ void operator()(const f32x4 (&acc)[2][2][4][2], const Unit& u, int wr, int wc, int fr, int fq) const {
;     ...
;                     const f32x4 v0 = a0 + acc[ai][bj][m][0] * sc, v1 = a1 + acc[ai][bj][m][1] * sc;
;                     q += ((v0[0] * v0[0] + v0[1] * v0[1]) + (v0[2] * v0[2] + v0[3] * v0[3])) + ((v1[0] * v1[0] + v1[1] * v1[1]) + (v1[2] * v1[2] + v1[3] * v1[3]));
;                     u32x4 wo; wo.x = cvt_pk_bf16(v0[0], v0[1]); wo.y = cvt_pk_bf16(v0[2], v0[3]); wo.z = cvt_pk_bf16(v1[0], v1[1]); wo.w = cvt_pk_bf16(v1[2], v1[3]);
;                     *(u32x4*)(xb + o2) = wo;
;                     if (x8) { u32x2 w8; w8.x = pk4_fp8(v0[0], v0[1], v0[2], v0[3]); w8.y = pk4_fp8(v1[0], v1[1], v1[2], v1[3]); *(u32x2*)(x8 + o2) = w8; } }
;                 q += __shfl_xor(q, 16); q += __shfl_xor(q, 32);
;                 if (fq == 0) unsafeAtomicAdd(ss + row, q);
.LBB0_1724:
	v_mul_f32_e32 v10, v13, v13
	v_mul_f32_e32 v7, v7, v7
	v_fmac_f32_e32 v10, v12, v12
	v_fmac_f32_e32 v7, v6, v6
	v_add_f32_e32 v6, v10, v7
	v_mul_f32_e32 v7, v15, v15
	v_mul_f32_e32 v9, v9, v9
	v_fmac_f32_e32 v7, v14, v14
	v_fmac_f32_e32 v9, v8, v8
	v_add_f32_e32 v7, v7, v9
	v_add_f32_e32 v6, v6, v7
	v_mul_f32_e32 v7, v17, v17
	v_mul_f32_e32 v3, v3, v3
	v_fmac_f32_e32 v7, v16, v16
	v_fmac_f32_e32 v3, v2, v2
	v_add_f32_e32 v2, v7, v3
	v_mul_f32_e32 v3, v19, v19
	v_mul_f32_e32 v5, v5, v5
	v_fmac_f32_e32 v3, v18, v18
	v_fmac_f32_e32 v5, v4, v4
	v_add_f32_e32 v3, v3, v5
	v_add_f32_e32 v2, v2, v3
	v_add_f32_e32 v2, v6, v2
	v_mov_b32_e32 v3, v2
	s_nop 1
	v_permlane16_swap_b32_e32 v2, v3
	s_waitcnt lgkmcnt(0)
	v_add_f32_e32 v2, v2, v3
	v_mov_b32_e32 v3, v2
	s_nop 1
	v_permlane32_swap_b32_e32 v2, v3
	s_and_saveexec_b64 s[6:7], s[0:1]
	s_cbranch_execz .LBB0_1726
	v_lshl_add_u64 v[4:5], v[98:99], 2, s[2:3]
	s_waitcnt lgkmcnt(0)
	v_add_f32_e32 v2, v2, v3
	global_atomic_add_f32 v[4:5], v2, off

; __device__ __forceinline__ unsigned cvt_pk_bf16(float lo, float hi) { unsigned r; asm volatile("v_cvt_pk_bf16_f32 %0, %1, %2" : "=v"(r) : "v"(lo), "v"(hi)); return r; }
;     __device__ __forceinline__ void operator()(const f32x4 (&acc)[2][2][4][2], const Unit& u, int wr, int wc, int fr, int fq) const {
;     ...
;                     const f32x4 v0 = a0 + acc[ai][bj][m][0] * sc, v1 = a1 + acc[ai][bj][m][1] * sc;
;                     q += ((v0[0] * v0[0] + v0[1] * v0[1]) + (v0[2] * v0[2] + v0[3] * v0[3])) + ((v1[0] * v1[0] + v1[1] * v1[1]) + (v1[2] * v1[2] + v1[3] * v1[3]));
;                     u32x4 wo; wo.x = cvt_pk_bf16(v0[0], v0[1]); wo.y = cvt_pk_bf16(v0[2], v0[3]); wo.z = cvt_pk_bf16(v1[0], v1[1]); wo.w = cvt_pk_bf16(v1[2], v1[3]);
;                     *(u32x4*)(xb + o2) = wo;
;                     if (x8) { u32x2 w8; w8.x = pk4_fp8(v0[0], v0[1], v0[2], v0[3]); w8.y = pk4_fp8(v1[0], v1[1], v1[2], v1[3]); *(u32x2*)(x8 + o2) = w8; } }
;                 q += __shfl_xor(q, 16); q += __shfl_xor(q, 32);
;                 if (fq == 0) unsafeAtomicAdd(ss + row, q);
.LBB0_2166:
	v_mul_f32_e32 v148, v159, v159
	v_mul_f32_e32 v149, v161, v161
	v_fmac_f32_e32 v148, v158, v158
	v_fmac_f32_e32 v149, v160, v160
	v_add_f32_e32 v148, v148, v149
	v_mul_f32_e32 v149, v155, v155
	v_mul_f32_e32 v152, v157, v157
	v_fmac_f32_e32 v149, v154, v154
	v_fmac_f32_e32 v152, v156, v156
	v_add_f32_e32 v149, v149, v152
	v_add_f32_e32 v148, v148, v149
	v_mul_f32_e32 v149, v151, v151
	v_mul_f32_e32 v27, v27, v27
	v_fmac_f32_e32 v149, v150, v150
	v_fmac_f32_e32 v27, v26, v26
	v_add_f32_e32 v26, v149, v27
	v_mul_f32_e32 v27, v147, v147
	v_mul_f32_e32 v29, v29, v29
	v_fmac_f32_e32 v27, v146, v146
	v_fmac_f32_e32 v29, v28, v28
	v_add_f32_e32 v27, v27, v29
	v_and_b32_e32 v28, 64, v195
	v_add_f32_e32 v26, v26, v27
	v_xor_b32_e32 v27, 16, v195
	v_add_u32_e32 v28, 64, v28
	v_cmp_lt_i32_e32 vcc, v27, v28
	v_add_f32_e32 v26, v148, v26
	s_nop 0
	v_cndmask_b32_e32 v27, v195, v27, vcc
	v_lshlrev_b32_e32 v146, 2, v27
	v_mov_b32_e32 v27, v26
	s_nop 1
	v_permlane16_swap_b32_e32 v26, v27
	s_waitcnt lgkmcnt(0)
	v_add_f32_e32 v26, v26, v27
	v_xor_b32_e32 v27, 32, v195
	v_cmp_lt_i32_e32 vcc, v27, v28
	s_nop 1
	v_cndmask_b32_e32 v27, v195, v27, vcc
	v_lshlrev_b32_e32 v147, 2, v27
	v_mov_b32_e32 v27, v26
	s_nop 1
	v_permlane32_swap_b32_e32 v26, v27
	s_and_saveexec_b64 s[30:31], s[0:1]
	s_cbranch_execz .LBB0_2168
	v_lshl_add_u64 v[28:29], v[32:33], 2, s[2:3]
	s_waitcnt lgkmcnt(0)
	v_add_f32_e32 v26, v26, v27
	global_atomic_add_f32 v[28:29], v26, off

; __device__ __forceinline__ unsigned cvt_pk_bf16(float lo, float hi) { unsigned r; asm volatile("v_cvt_pk_bf16_f32 %0, %1, %2" : "=v"(r) : "v"(lo), "v"(hi)); return r; }
;     __device__ __forceinline__ void operator()(const f32x4 (&acc)[2][2][4][2], const Unit& u, int wr, int wc, int fr, int fq) const {
;     ...
;                     const f32x4 v0 = a0 + acc[ai][bj][m][0] * sc, v1 = a1 + acc[ai][bj][m][1] * sc;
;                     q += ((v0[0] * v0[0] + v0[1] * v0[1]) + (v0[2] * v0[2] + v0[3] * v0[3])) + ((v1[0] * v1[0] + v1[1] * v1[1]) + (v1[2] * v1[2] + v1[3] * v1[3]));
;                     u32x4 wo; wo.x = cvt_pk_bf16(v0[0], v0[1]); wo.y = cvt_pk_bf16(v0[2], v0[3]); wo.z = cvt_pk_bf16(v1[0], v1[1]); wo.w = cvt_pk_bf16(v1[2], v1[3]);
;                     *(u32x4*)(xb + o2) = wo;
;                     if (x8) { u32x2 w8; w8.x = pk4_fp8(v0[0], v0[1], v0[2], v0[3]); w8.y = pk4_fp8(v1[0], v1[1], v1[2], v1[3]); *(u32x2*)(x8 + o2) = w8; } }
;                 q += __shfl_xor(q, 16); q += __shfl_xor(q, 32);
;                 if (fq == 0) unsafeAtomicAdd(ss + row, q);
.LBB0_2172:
	v_mul_f32_e32 v26, v29, v29
	v_mul_f32_e32 v23, v23, v23
	v_fmac_f32_e32 v26, v28, v28
	v_fmac_f32_e32 v23, v22, v22
	v_add_f32_e32 v22, v26, v23
	v_mul_f32_e32 v23, v139, v139
	v_mul_f32_e32 v25, v25, v25
	v_fmac_f32_e32 v23, v138, v138
	v_fmac_f32_e32 v25, v24, v24
	v_add_f32_e32 v23, v23, v25
	v_add_f32_e32 v22, v22, v23
	v_mul_f32_e32 v23, v135, v135
	v_mul_f32_e32 v19, v19, v19
	v_fmac_f32_e32 v23, v134, v134
	v_fmac_f32_e32 v19, v18, v18
	v_add_f32_e32 v18, v23, v19
	v_mul_f32_e32 v19, v131, v131
	v_mul_f32_e32 v21, v21, v21
	v_fmac_f32_e32 v19, v130, v130
	v_fmac_f32_e32 v21, v20, v20
	v_add_f32_e32 v19, v19, v21
	v_add_f32_e32 v18, v18, v19
	v_add_f32_e32 v18, v22, v18
	v_mov_b32_e32 v19, v18
	s_nop 1
	v_permlane16_swap_b32_e32 v18, v19
	s_waitcnt lgkmcnt(0)
	v_add_f32_e32 v18, v18, v19
	v_mov_b32_e32 v19, v18
	s_nop 1
	v_permlane32_swap_b32_e32 v18, v19
	s_and_saveexec_b64 s[30:31], s[0:1]
	s_cbranch_execz .LBB0_2174
	v_lshl_add_u64 v[20:21], v[184:185], 2, s[2:3]
	s_waitcnt lgkmcnt(0)
	v_add_f32_e32 v18, v18, v19
	global_atomic_add_f32 v[20:21], v18, off

; __device__ __forceinline__ unsigned cvt_pk_bf16(float lo, float hi) { unsigned r; asm volatile("v_cvt_pk_bf16_f32 %0, %1, %2" : "=v"(r) : "v"(lo), "v"(hi)); return r; }
;     __device__ __forceinline__ void operator()(const f32x4 (&acc)[2][2][4][2], const Unit& u, int wr, int wc, int fr, int fq) const {
;     ...
;                     const f32x4 v0 = a0 + acc[ai][bj][m][0] * sc, v1 = a1 + acc[ai][bj][m][1] * sc;
;                     q += ((v0[0] * v0[0] + v0[1] * v0[1]) + (v0[2] * v0[2] + v0[3] * v0[3])) + ((v1[0] * v1[0] + v1[1] * v1[1]) + (v1[2] * v1[2] + v1[3] * v1[3]));
;                     u32x4 wo; wo.x = cvt_pk_bf16(v0[0], v0[1]); wo.y = cvt_pk_bf16(v0[2], v0[3]); wo.z = cvt_pk_bf16(v1[0], v1[1]); wo.w = cvt_pk_bf16(v1[2], v1[3]);
;                     *(u32x4*)(xb + o2) = wo;
;                     if (x8) { u32x2 w8; w8.x = pk4_fp8(v0[0], v0[1], v0[2], v0[3]); w8.y = pk4_fp8(v1[0], v1[1], v1[2], v1[3]); *(u32x2*)(x8 + o2) = w8; } }
;                 q += __shfl_xor(q, 16); q += __shfl_xor(q, 32);
;                 if (fq == 0) unsafeAtomicAdd(ss + row, q);
.LBB0_2178:
	v_mul_f32_e32 v18, v21, v21
	v_mul_f32_e32 v15, v15, v15
	v_fmac_f32_e32 v18, v20, v20
	v_fmac_f32_e32 v15, v14, v14
	v_add_f32_e32 v14, v18, v15
	v_mul_f32_e32 v15, v23, v23
	v_mul_f32_e32 v17, v17, v17
	v_fmac_f32_e32 v15, v22, v22
	v_fmac_f32_e32 v17, v16, v16
	v_add_f32_e32 v15, v15, v17
	v_add_f32_e32 v14, v14, v15
	v_mul_f32_e32 v15, v25, v25
	v_mul_f32_e32 v11, v11, v11
	v_fmac_f32_e32 v15, v24, v24
	v_fmac_f32_e32 v11, v10, v10
	v_add_f32_e32 v10, v15, v11
	v_mul_f32_e32 v11, v27, v27
	v_mul_f32_e32 v13, v13, v13
	v_fmac_f32_e32 v11, v26, v26
	v_fmac_f32_e32 v13, v12, v12
	v_add_f32_e32 v11, v11, v13
	v_add_f32_e32 v10, v10, v11
	v_add_f32_e32 v10, v14, v10
	v_mov_b32_e32 v11, v10
	s_nop 1
	v_permlane16_swap_b32_e32 v10, v11
	s_waitcnt lgkmcnt(0)
	v_add_f32_e32 v10, v10, v11
	v_mov_b32_e32 v11, v10
	s_nop 1
	v_permlane32_swap_b32_e32 v10, v11
	s_and_saveexec_b64 s[30:31], s[0:1]
	s_cbranch_execz .LBB0_2180
	v_lshl_add_u64 v[12:13], v[180:181], 2, s[2:3]
	s_waitcnt lgkmcnt(0)
	v_add_f32_e32 v10, v10, v11
	global_atomic_add_f32 v[12:13], v10, off

; __device__ __forceinline__ unsigned cvt_pk_bf16(float lo, float hi) { unsigned r; asm volatile("v_cvt_pk_bf16_f32 %0, %1, %2" : "=v"(r) : "v"(lo), "v"(hi)); return r; }
;     __device__ __forceinline__ void operator()(const f32x4 (&acc)[2][2][4][2], const Unit& u, int wr, int wc, int fr, int fq) const {
;     ...
;                     const f32x4 v0 = a0 + acc[ai][bj][m][0] * sc, v1 = a1 + acc[ai][bj][m][1] * sc;
;                     q += ((v0[0] * v0[0] + v0[1] * v0[1]) + (v0[2] * v0[2] + v0[3] * v0[3])) + ((v1[0] * v1[0] + v1[1] * v1[1]) + (v1[2] * v1[2] + v1[3] * v1[3]));
;                     u32x4 wo; wo.x = cvt_pk_bf16(v0[0], v0[1]); wo.y = cvt_pk_bf16(v0[2], v0[3]); wo.z = cvt_pk_bf16(v1[0], v1[1]); wo.w = cvt_pk_bf16(v1[2], v1[3]);
;                     *(u32x4*)(xb + o2) = wo;
;                     if (x8) { u32x2 w8; w8.x = pk4_fp8(v0[0], v0[1], v0[2], v0[3]); w8.y = pk4_fp8(v1[0], v1[1], v1[2], v1[3]); *(u32x2*)(x8 + o2) = w8; } }
;                 q += __shfl_xor(q, 16); q += __shfl_xor(q, 32);
;                 if (fq == 0) unsafeAtomicAdd(ss + row, q);
.LBB0_2184:
	v_mul_f32_e32 v10, v13, v13
	v_mul_f32_e32 v7, v7, v7
	v_fmac_f32_e32 v10, v12, v12
	v_fmac_f32_e32 v7, v6, v6
	v_add_f32_e32 v6, v10, v7
	v_mul_f32_e32 v7, v15, v15
	v_mul_f32_e32 v9, v9, v9
	v_fmac_f32_e32 v7, v14, v14
	v_fmac_f32_e32 v9, v8, v8
	v_add_f32_e32 v7, v7, v9
	v_add_f32_e32 v6, v6, v7
	v_mul_f32_e32 v7, v17, v17
	v_mul_f32_e32 v3, v3, v3
	v_fmac_f32_e32 v7, v16, v16
	v_fmac_f32_e32 v3, v2, v2
	v_add_f32_e32 v2, v7, v3
	v_mul_f32_e32 v3, v19, v19
	v_mul_f32_e32 v5, v5, v5
	v_fmac_f32_e32 v3, v18, v18
	v_fmac_f32_e32 v5, v4, v4
	v_add_f32_e32 v3, v3, v5
	v_add_f32_e32 v2, v2, v3
	v_add_f32_e32 v2, v6, v2
	v_mov_b32_e32 v3, v2
	s_nop 1
	v_permlane16_swap_b32_e32 v2, v3
	s_waitcnt lgkmcnt(0)
	v_add_f32_e32 v2, v2, v3
	v_mov_b32_e32 v3, v2
	s_nop 1
	v_permlane32_swap_b32_e32 v2, v3
	s_and_saveexec_b64 s[30:31], s[0:1]
	s_cbranch_execz .LBB0_2186
	v_lshl_add_u64 v[4:5], v[176:177], 2, s[2:3]
	s_waitcnt lgkmcnt(0)
	v_add_f32_e32 v2, v2, v3
	global_atomic_add_f32 v[4:5], v2, off

; __device__ __forceinline__ unsigned cvt_pk_bf16(float lo, float hi) { unsigned r; asm volatile("v_cvt_pk_bf16_f32 %0, %1, %2" : "=v"(r) : "v"(lo), "v"(hi)); return r; }
;     __device__ __forceinline__ void operator()(const f32x4 (&acc)[2][2][4][2], const Unit& u, int wr, int wc, int fr, int fq) const {
;     ...
;                     const f32x4 v0 = a0 + acc[ai][bj][m][0] * sc, v1 = a1 + acc[ai][bj][m][1] * sc;
;                     q += ((v0[0] * v0[0] + v0[1] * v0[1]) + (v0[2] * v0[2] + v0[3] * v0[3])) + ((v1[0] * v1[0] + v1[1] * v1[1]) + (v1[2] * v1[2] + v1[3] * v1[3]));
;                     u32x4 wo; wo.x = cvt_pk_bf16(v0[0], v0[1]); wo.y = cvt_pk_bf16(v0[2], v0[3]); wo.z = cvt_pk_bf16(v1[0], v1[1]); wo.w = cvt_pk_bf16(v1[2], v1[3]);
;                     *(u32x4*)(xb + o2) = wo;
;                     if (x8) { u32x2 w8; w8.x = pk4_fp8(v0[0], v0[1], v0[2], v0[3]); w8.y = pk4_fp8(v1[0], v1[1], v1[2], v1[3]); *(u32x2*)(x8 + o2) = w8; } }
;                 q += __shfl_xor(q, 16); q += __shfl_xor(q, 32);
;                 if (fq == 0) unsafeAtomicAdd(ss + row, q);
.LBB0_2190:
	v_mul_f32_e32 v84, v95, v95
	v_mul_f32_e32 v85, v97, v97
	v_fmac_f32_e32 v84, v94, v94
	v_fmac_f32_e32 v85, v96, v96
	v_add_f32_e32 v84, v84, v85
	v_mul_f32_e32 v85, v91, v91
	v_mul_f32_e32 v88, v93, v93
	v_fmac_f32_e32 v85, v90, v90
	v_fmac_f32_e32 v88, v92, v92
	v_add_f32_e32 v85, v85, v88
	v_add_f32_e32 v84, v84, v85
	v_mul_f32_e32 v85, v87, v87
	v_mul_f32_e32 v27, v27, v27
	v_fmac_f32_e32 v85, v86, v86
	v_fmac_f32_e32 v27, v26, v26
	v_add_f32_e32 v26, v85, v27
	v_mul_f32_e32 v27, v83, v83
	v_mul_f32_e32 v29, v29, v29
	v_fmac_f32_e32 v27, v82, v82
	v_fmac_f32_e32 v29, v28, v28
	v_add_f32_e32 v27, v27, v29
	v_add_f32_e32 v26, v26, v27
	v_add_f32_e32 v26, v84, v26
	v_mov_b32_e32 v27, v26
	s_nop 1
	v_permlane16_swap_b32_e32 v26, v27
	s_waitcnt lgkmcnt(0)
	v_add_f32_e32 v26, v26, v27
	v_mov_b32_e32 v27, v26
	s_nop 1
	v_permlane32_swap_b32_e32 v26, v27
	s_and_saveexec_b64 s[30:31], s[0:1]
	s_cbranch_execz .LBB0_2192
	v_lshl_add_u64 v[28:29], v[108:109], 2, s[2:3]
	s_waitcnt lgkmcnt(0)
	v_add_f32_e32 v26, v26, v27
	global_atomic_add_f32 v[28:29], v26, off

; __device__ __forceinline__ unsigned cvt_pk_bf16(float lo, float hi) { unsigned r; asm volatile("v_cvt_pk_bf16_f32 %0, %1, %2" : "=v"(r) : "v"(lo), "v"(hi)); return r; }
;     __device__ __forceinline__ void operator()(const f32x4 (&acc)[2][2][4][2], const Unit& u, int wr, int wc, int fr, int fq) const {
;     ...
;                     const f32x4 v0 = a0 + acc[ai][bj][m][0] * sc, v1 = a1 + acc[ai][bj][m][1] * sc;
;                     q += ((v0[0] * v0[0] + v0[1] * v0[1]) + (v0[2] * v0[2] + v0[3] * v0[3])) + ((v1[0] * v1[0] + v1[1] * v1[1]) + (v1[2] * v1[2] + v1[3] * v1[3]));
;                     u32x4 wo; wo.x = cvt_pk_bf16(v0[0], v0[1]); wo.y = cvt_pk_bf16(v0[2], v0[3]); wo.z = cvt_pk_bf16(v1[0], v1[1]); wo.w = cvt_pk_bf16(v1[2], v1[3]);
;                     *(u32x4*)(xb + o2) = wo;
;                     if (x8) { u32x2 w8; w8.x = pk4_fp8(v0[0], v0[1], v0[2], v0[3]); w8.y = pk4_fp8(v1[0], v1[1], v1[2], v1[3]); *(u32x2*)(x8 + o2) = w8; } }
;                 q += __shfl_xor(q, 16); q += __shfl_xor(q, 32);
;                 if (fq == 0) unsafeAtomicAdd(ss + row, q);
.LBB0_2196:
	v_mul_f32_e32 v26, v29, v29
	v_mul_f32_e32 v23, v23, v23
	v_fmac_f32_e32 v26, v28, v28
	v_fmac_f32_e32 v23, v22, v22
	v_add_f32_e32 v22, v26, v23
	v_mul_f32_e32 v23, v75, v75
	v_mul_f32_e32 v25, v25, v25
	v_fmac_f32_e32 v23, v74, v74
	v_fmac_f32_e32 v25, v24, v24
	v_add_f32_e32 v23, v23, v25
	v_add_f32_e32 v22, v22, v23
	v_mul_f32_e32 v23, v71, v71
	v_mul_f32_e32 v19, v19, v19
	v_fmac_f32_e32 v23, v70, v70
	v_fmac_f32_e32 v19, v18, v18
	v_add_f32_e32 v18, v23, v19
	v_mul_f32_e32 v19, v67, v67
	v_mul_f32_e32 v21, v21, v21
	v_fmac_f32_e32 v19, v66, v66
	v_fmac_f32_e32 v21, v20, v20
	v_add_f32_e32 v19, v19, v21
	v_add_f32_e32 v18, v18, v19
	v_add_f32_e32 v18, v22, v18
	v_mov_b32_e32 v19, v18
	s_nop 1
	v_permlane16_swap_b32_e32 v18, v19
	s_waitcnt lgkmcnt(0)
	v_add_f32_e32 v18, v18, v19
	v_mov_b32_e32 v19, v18
	s_nop 1
	v_permlane32_swap_b32_e32 v18, v19
	s_and_saveexec_b64 s[30:31], s[0:1]
	s_cbranch_execz .LBB0_2198
	v_lshl_add_u64 v[20:21], v[104:105], 2, s[2:3]
	s_waitcnt lgkmcnt(0)
	v_add_f32_e32 v18, v18, v19
	global_atomic_add_f32 v[20:21], v18, off

; __device__ __forceinline__ unsigned cvt_pk_bf16(float lo, float hi) { unsigned r; asm volatile("v_cvt_pk_bf16_f32 %0, %1, %2" : "=v"(r) : "v"(lo), "v"(hi)); return r; }
;     __device__ __forceinline__ void operator()(const f32x4 (&acc)[2][2][4][2], const Unit& u, int wr, int wc, int fr, int fq) const {
;     ...
;                     const f32x4 v0 = a0 + acc[ai][bj][m][0] * sc, v1 = a1 + acc[ai][bj][m][1] * sc;
;                     q += ((v0[0] * v0[0] + v0[1] * v0[1]) + (v0[2] * v0[2] + v0[3] * v0[3])) + ((v1[0] * v1[0] + v1[1] * v1[1]) + (v1[2] * v1[2] + v1[3] * v1[3]));
;                     u32x4 wo; wo.x = cvt_pk_bf16(v0[0], v0[1]); wo.y = cvt_pk_bf16(v0[2], v0[3]); wo.z = cvt_pk_bf16(v1[0], v1[1]); wo.w = cvt_pk_bf16(v1[2], v1[3]);
;                     *(u32x4*)(xb + o2) = wo;
;                     if (x8) { u32x2 w8; w8.x = pk4_fp8(v0[0], v0[1], v0[2], v0[3]); w8.y = pk4_fp8(v1[0], v1[1], v1[2], v1[3]); *(u32x2*)(x8 + o2) = w8; } }
;                 q += __shfl_xor(q, 16); q += __shfl_xor(q, 32);
;                 if (fq == 0) unsafeAtomicAdd(ss + row, q);
.LBB0_2202:
	v_mul_f32_e32 v18, v21, v21
	v_mul_f32_e32 v15, v15, v15
	v_fmac_f32_e32 v18, v20, v20
	v_fmac_f32_e32 v15, v14, v14
	v_add_f32_e32 v14, v18, v15
	v_mul_f32_e32 v15, v23, v23
	v_mul_f32_e32 v17, v17, v17
	v_fmac_f32_e32 v15, v22, v22
	v_fmac_f32_e32 v17, v16, v16
	v_add_f32_e32 v15, v15, v17
	v_add_f32_e32 v14, v14, v15
	v_mul_f32_e32 v15, v25, v25
	v_mul_f32_e32 v11, v11, v11
	v_fmac_f32_e32 v15, v24, v24
	v_fmac_f32_e32 v11, v10, v10
	v_add_f32_e32 v10, v15, v11
	v_mul_f32_e32 v11, v27, v27
	v_mul_f32_e32 v13, v13, v13
	v_fmac_f32_e32 v11, v26, v26
	v_fmac_f32_e32 v13, v12, v12
	v_add_f32_e32 v11, v11, v13
	v_add_f32_e32 v10, v10, v11
	v_add_f32_e32 v10, v14, v10
	v_mov_b32_e32 v11, v10
	s_nop 1
	v_permlane16_swap_b32_e32 v10, v11
	s_waitcnt lgkmcnt(0)
	v_add_f32_e32 v10, v10, v11
	v_mov_b32_e32 v11, v10
	s_nop 1
	v_permlane32_swap_b32_e32 v10, v11
	s_and_saveexec_b64 s[30:31], s[0:1]
	s_cbranch_execz .LBB0_2204
	v_lshl_add_u64 v[12:13], v[100:101], 2, s[2:3]
	s_waitcnt lgkmcnt(0)
	v_add_f32_e32 v10, v10, v11
	global_atomic_add_f32 v[12:13], v10, off

; __device__ __forceinline__ unsigned cvt_pk_bf16(float lo, float hi) { unsigned r; asm volatile("v_cvt_pk_bf16_f32 %0, %1, %2" : "=v"(r) : "v"(lo), "v"(hi)); return r; }
;     __device__ __forceinline__ void operator()(const f32x4 (&acc)[2][2][4][2], const Unit& u, int wr, int wc, int fr, int fq) const {
;     ...
;                     const f32x4 v0 = a0 + acc[ai][bj][m][0] * sc, v1 = a1 + acc[ai][bj][m][1] * sc;
;                     q += ((v0[0] * v0[0] + v0[1] * v0[1]) + (v0[2] * v0[2] + v0[3] * v0[3])) + ((v1[0] * v1[0] + v1[1] * v1[1]) + (v1[2] * v1[2] + v1[3] * v1[3]));
;                     u32x4 wo; wo.x = cvt_pk_bf16(v0[0], v0[1]); wo.y = cvt_pk_bf16(v0[2], v0[3]); wo.z = cvt_pk_bf16(v1[0], v1[1]); wo.w = cvt_pk_bf16(v1[2], v1[3]);
;                     *(u32x4*)(xb + o2) = wo;
;                     if (x8) { u32x2 w8; w8.x = pk4_fp8(v0[0], v0[1], v0[2], v0[3]); w8.y = pk4_fp8(v1[0], v1[1], v1[2], v1[3]); *(u32x2*)(x8 + o2) = w8; } }
;                 q += __shfl_xor(q, 16); q += __shfl_xor(q, 32);
;                 if (fq == 0) unsafeAtomicAdd(ss + row, q);
.LBB0_2208:
	v_mul_f32_e32 v10, v13, v13
	v_mul_f32_e32 v7, v7, v7
	v_fmac_f32_e32 v10, v12, v12
	v_fmac_f32_e32 v7, v6, v6
	v_add_f32_e32 v6, v10, v7
	v_mul_f32_e32 v7, v15, v15
	v_mul_f32_e32 v9, v9, v9
	v_fmac_f32_e32 v7, v14, v14
	v_fmac_f32_e32 v9, v8, v8
	v_add_f32_e32 v7, v7, v9
	v_add_f32_e32 v6, v6, v7
	v_mul_f32_e32 v7, v17, v17
	v_mul_f32_e32 v3, v3, v3
	v_fmac_f32_e32 v7, v16, v16
	v_fmac_f32_e32 v3, v2, v2
	v_add_f32_e32 v2, v7, v3
	v_mul_f32_e32 v3, v19, v19
	v_mul_f32_e32 v5, v5, v5
	v_fmac_f32_e32 v3, v18, v18
	v_fmac_f32_e32 v5, v4, v4
	v_add_f32_e32 v3, v3, v5
	v_add_f32_e32 v2, v2, v3
	v_add_f32_e32 v2, v6, v2
	v_mov_b32_e32 v3, v2
	s_nop 1
	v_permlane16_swap_b32_e32 v2, v3
	s_waitcnt lgkmcnt(0)
	v_add_f32_e32 v2, v2, v3
	v_mov_b32_e32 v3, v2
	s_nop 1
	v_permlane32_swap_b32_e32 v2, v3
	s_and_saveexec_b64 s[6:7], s[0:1]
	s_cbranch_execz .LBB0_2210
	v_lshl_add_u64 v[4:5], v[32:33], 2, s[2:3]
	s_waitcnt lgkmcnt(0)
	v_add_f32_e32 v2, v2, v3
	global_atomic_add_f32 v[4:5], v2, off

; __device__ __forceinline__ unsigned cvt_pk_bf16(float lo, float hi) { unsigned r; asm volatile("v_cvt_pk_bf16_f32 %0, %1, %2" : "=v"(r) : "v"(lo), "v"(hi)); return r; }
;     __device__ __forceinline__ void operator()(const f32x4 (&acc)[2][2][4][2], const Unit& u, int wr, int wc, int fr, int fq) const {
;     ...
;                 for (int bj = 0; bj < 2; ++bj) { const size_t o2 = (size_t)(row0 + ai * HALF + m * 16) * DM + col0 + bj * HALF;
;                     if constexpr (XF32) { a[m][bj][0] = *(const f32x4*)((const float*)xin + o2); a[m][bj][1] = *(const f32x4*)((const float*)xin + o2 + 4); }
;                     else { const u32x4 w = *(const u32x4*)((const bf16_t*)xin + o2); a[m][bj][0] = __builtin_bit_cast(f32x4, w); } }
; #pragma unroll
;             for (int m = 0; m < 4; ++m) {
;                 const int row = row0 + ai * HALF + m * 16; const size_t off = (size_t)row * DM + col0; float q = 0.f;
; #pragma unroll
;                 for (int bj = 0; bj < 2; ++bj) { const size_t o2 = off + bj * HALF;
;                     f32x4 a0, a1;
;                     if constexpr (XF32) { a0 = a[m][bj][0]; a1 = a[m][bj][1]; }
;                     else { const u32x4 w = __builtin_bit_cast(u32x4, a[m][bj][0]);
;                         a0 = (f32x4){__uint_as_float(w.x << 16), __uint_as_float(w.x & 0xffff0000u), __uint_as_float(w.y << 16), __uint_as_float(w.y & 0xffff0000u)};
;                         a1 = (f32x4){__uint_as_float(w.z << 16), __uint_as_float(w.z & 0xffff0000u), __uint_as_float(w.w << 16), __uint_as_float(w.w & 0xffff0000u)}; }
;                     const f32x4 v0 = a0 + acc[ai][bj][m][0] * sc, v1 = a1 + acc[ai][bj][m][1] * sc;
;                     q += ((v0[0] * v0[0] + v0[1] * v0[1]) + (v0[2] * v0[2] + v0[3] * v0[3])) + ((v1[0] * v1[0] + v1[1] * v1[1]) + (v1[2] * v1[2] + v1[3] * v1[3]));
;                     u32x4 wo; wo.x = cvt_pk_bf16(v0[0], v0[1]); wo.y = cvt_pk_bf16(v0[2], v0[3]); wo.z = cvt_pk_bf16(v1[0], v1[1]); wo.w = cvt_pk_bf16(v1[2], v1[3]);
;                     *(u32x4*)(xb + o2) = wo;
;                     if (x8) { u32x2 w8; w8.x = pk4_fp8(v0[0], v0[1], v0[2], v0[3]); w8.y = pk4_fp8(v1[0], v1[1], v1[2], v1[3]); *(u32x2*)(x8 + o2) = w8; } }
;                 q += __shfl_xor(q, 16); q += __shfl_xor(q, 32);
;                 if (fq == 0) unsafeAtomicAdd(ss + row, q);
.LBB0_2362:
	v_lshl_or_b32 v26, s24, 8, v189
	v_lshl_add_u32 v30, s22, 8, v1
	v_ashrrev_i32_e32 v27, 31, v26
	v_lshlrev_b64 v[204:205], 1, v[26:27]
	v_ashrrev_i32_e32 v31, 31, v30
	v_lshl_add_u64 v[28:29], s[66:67], 0, v[204:205]
	v_lshlrev_b64 v[194:195], 13, v[30:31]
	s_nop 15
	s_nop 15
	v_lshl_add_u64 v[2:3], v[28:29], 0, v[194:195]
	global_load_dwordx4 v[196:199], v[2:3], off
	global_load_dwordx4 v[200:203], v[2:3], off offset:256
	v_or_b32_e32 v184, 16, v30
	v_or_b32_e32 v180, 32, v30
	v_or_b32_e32 v32, 48, v30
	v_ashrrev_i32_e32 v185, 31, v184
	v_ashrrev_i32_e32 v181, 31, v180
	v_ashrrev_i32_e32 v33, 31, v32
	v_lshlrev_b64 v[186:187], 13, v[184:185]
	v_lshlrev_b64 v[182:183], 13, v[180:181]
	v_lshlrev_b64 v[178:179], 13, v[32:33]
	v_lshl_add_u64 v[2:3], v[28:29], 0, v[186:187]
	v_lshl_add_u64 v[4:5], v[28:29], 0, v[182:183]
	v_lshl_add_u64 v[206:207], v[28:29], 0, v[178:179]
	global_load_dwordx4 v[22:25], v[2:3], off
	global_load_dwordx4 v[18:21], v[2:3], off offset:256
	global_load_dwordx4 v[14:17], v[4:5], off
	global_load_dwordx4 v[10:13], v[4:5], off offset:256
	global_load_dwordx4 v[6:9], v[206:207], off
	s_nop 0
	global_load_dwordx4 v[2:5], v[206:207], off offset:256
	v_and_b32_e32 v207, 64, v193
	v_xor_b32_e32 v206, 16, v193
	v_add_u32_e32 v207, 64, v207
	v_xor_b32_e32 v208, 32, v193
	v_cmp_lt_i32_e32 vcc, v206, v207
	s_waitcnt vmcnt(0)
	v_lshlrev_b32_e32 v210, 16, v200
	v_cndmask_b32_e32 v209, v193, v206, vcc
	v_cmp_lt_i32_e32 vcc, v208, v207
	v_lshl_add_u64 v[206:207], s[66:67], 0, v[194:195]
	v_lshlrev_b32_e32 v194, 2, v209
	v_cndmask_b32_e32 v214, v193, v208, vcc
	v_lshl_add_u64 v[204:205], v[206:207], 0, v[204:205]
	v_lshlrev_b32_e32 v206, 16, v196
	v_and_b32_e32 v207, 0xffff0000, v196
	v_lshlrev_b32_e32 v196, 16, v197
	v_and_b32_e32 v197, 0xffff0000, v197
	v_lshlrev_b32_e32 v208, 16, v198
	v_and_b32_e32 v209, 0xffff0000, v198
	v_lshlrev_b32_e32 v198, 16, v199
	v_and_b32_e32 v199, 0xffff0000, v199
	v_and_b32_e32 v211, 0xffff0000, v200
	v_lshlrev_b32_e32 v200, 16, v201
	v_and_b32_e32 v201, 0xffff0000, v201
	v_lshlrev_b32_e32 v212, 16, v202
	v_and_b32_e32 v213, 0xffff0000, v202
	v_lshlrev_b32_e32 v202, 16, v203
	v_and_b32_e32 v203, 0xffff0000, v203
	v_pk_fma_f32 v[160:161], v[160:161], s[12:13], v[196:197] op_sel_hi:[1,0,1]
	v_pk_fma_f32 v[158:159], v[158:159], s[12:13], v[206:207] op_sel_hi:[1,0,1]
	v_pk_fma_f32 v[156:157], v[156:157], s[12:13], v[198:199] op_sel_hi:[1,0,1]
	v_pk_fma_f32 v[154:155], v[154:155], s[12:13], v[208:209] op_sel_hi:[1,0,1]
	v_pk_fma_f32 v[152:153], v[152:153], s[12:13], v[200:201] op_sel_hi:[1,0,1]
	v_pk_fma_f32 v[150:151], v[150:151], s[12:13], v[210:211] op_sel_hi:[1,0,1]
	v_pk_fma_f32 v[196:197], v[148:149], s[12:13], v[202:203] op_sel_hi:[1,0,1]
	v_pk_fma_f32 v[198:199], v[146:147], s[12:13], v[212:213] op_sel_hi:[1,0,1]
	v_mul_f32_e32 v148, v159, v159
	v_mul_f32_e32 v149, v161, v161
	v_mul_f32_e32 v195, v155, v155
	v_mul_f32_e32 v200, v157, v157
	v_cvt_pk_bf16_f32 v146, v158, v159
	v_cvt_pk_bf16_f32 v147, v160, v161
	v_mul_f32_e32 v159, v151, v151
	v_mul_f32_e32 v161, v153, v153
	v_mul_f32_e32 v201, v199, v199
	v_mul_f32_e32 v202, v197, v197
	v_fmac_f32_e32 v148, v158, v158
	v_fmac_f32_e32 v149, v160, v160
	v_fmac_f32_e32 v195, v154, v154
	v_fmac_f32_e32 v200, v156, v156
	v_fmac_f32_e32 v159, v150, v150
	v_fmac_f32_e32 v161, v152, v152
	v_fmac_f32_e32 v201, v198, v198
	v_fmac_f32_e32 v202, v196, v196
	v_add_f32_e32 v148, v148, v149
	v_add_f32_e32 v149, v195, v200
	v_add_f32_e32 v158, v159, v161
	v_add_f32_e32 v159, v201, v202
	v_add_f32_e32 v148, v148, v149
	v_add_f32_e32 v149, v158, v159
	v_add_f32_e32 v158, v148, v149
	v_mov_b32_e32 v159, v158
	v_mov_b32_e32 v194, v158
	s_nop 1
	v_permlane16_swap_b32_e32 v159, v194
	v_cvt_pk_bf16_f32 v148, v154, v155
	v_cvt_pk_bf16_f32 v149, v156, v157
	global_store_dwordx4 v[204:205], v[146:149], off
	v_cvt_pk_bf16_f32 v150, v150, v151
	v_cvt_pk_bf16_f32 v151, v152, v153
	v_cvt_pk_bf16_f32 v152, v198, v199
	v_cvt_pk_bf16_f32 v153, v196, v197
	global_store_dwordx4 v[204:205], v[150:153], off offset:256
	s_waitcnt lgkmcnt(0)
	v_add_f32_e32 v147, v194, v159
	v_lshlrev_b32_e32 v146, 2, v214
	v_mov_b32_e32 v148, v147
	v_mov_b32_e32 v146, v147
	s_nop 1
	v_permlane32_swap_b32_e32 v148, v146
	s_and_saveexec_b64 s[22:23], s[0:1]
	s_cbranch_execz .LBB0_2364
	v_lshl_add_u64 v[150:151], v[30:31], 2, s[6:7]
	s_waitcnt lgkmcnt(0)
	v_add_f32_e32 v31, v146, v148
	global_atomic_add_f32 v[150:151], v31, off
; __device__ __forceinline__ unsigned cvt_pk_bf16(float lo, float hi) { unsigned r; asm volatile("v_cvt_pk_bf16_f32 %0, %1, %2" : "=v"(r) : "v"(lo), "v"(hi)); return r; }
;     __device__ __forceinline__ void operator()(const f32x4 (&acc)[2][2][4][2], const Unit& u, int wr, int wc, int fr, int fq) const {
;     ...
;             for (int m = 0; m < 4; ++m) {
;                 const int row = row0 + ai * HALF + m * 16; const size_t off = (size_t)row * DM + col0; float q = 0.f;
; #pragma unroll
;                 for (int bj = 0; bj < 2; ++bj) { const size_t o2 = off + bj * HALF;
;                     f32x4 a0, a1;
;                     if constexpr (XF32) { a0 = a[m][bj][0]; a1 = a[m][bj][1]; }
;                     else { const u32x4 w = __builtin_bit_cast(u32x4, a[m][bj][0]);
;                         a0 = (f32x4){__uint_as_float(w.x << 16), __uint_as_float(w.x & 0xffff0000u), __uint_as_float(w.y << 16), __uint_as_float(w.y & 0xffff0000u)};
;                         a1 = (f32x4){__uint_as_float(w.z << 16), __uint_as_float(w.z & 0xffff0000u), __uint_as_float(w.w << 16), __uint_as_float(w.w & 0xffff0000u)}; }
;                     const f32x4 v0 = a0 + acc[ai][bj][m][0] * sc, v1 = a1 + acc[ai][bj][m][1] * sc;
;                     q += ((v0[0] * v0[0] + v0[1] * v0[1]) + (v0[2] * v0[2] + v0[3] * v0[3])) + ((v1[0] * v1[0] + v1[1] * v1[1]) + (v1[2] * v1[2] + v1[3] * v1[3]));
;                     u32x4 wo; wo.x = cvt_pk_bf16(v0[0], v0[1]); wo.y = cvt_pk_bf16(v0[2], v0[3]); wo.z = cvt_pk_bf16(v1[0], v1[1]); wo.w = cvt_pk_bf16(v1[2], v1[3]);
;                     *(u32x4*)(xb + o2) = wo;
;                     if (x8) { u32x2 w8; w8.x = pk4_fp8(v0[0], v0[1], v0[2], v0[3]); w8.y = pk4_fp8(v1[0], v1[1], v1[2], v1[3]); *(u32x2*)(x8 + o2) = w8; } }
;                 q += __shfl_xor(q, 16); q += __shfl_xor(q, 32);
;                 if (fq == 0) unsafeAtomicAdd(ss + row, q);
.LBB0_2364:
	s_or_b64 exec, exec, s[22:23]
	s_waitcnt lgkmcnt(0)
	v_lshlrev_b32_e32 v148, 16, v22
	v_and_b32_e32 v149, 0xffff0000, v22
	v_lshlrev_b32_e32 v22, 16, v23
	v_and_b32_e32 v23, 0xffff0000, v23
	v_lshlrev_b32_e32 v150, 16, v24
	v_and_b32_e32 v151, 0xffff0000, v24
	v_lshlrev_b32_e32 v24, 16, v25
	v_and_b32_e32 v25, 0xffff0000, v25
	v_pk_fma_f32 v[144:145], v[144:145], s[12:13], v[22:23] op_sel_hi:[1,0,1]
	v_pk_fma_f32 v[22:23], v[142:143], s[12:13], v[148:149] op_sel_hi:[1,0,1]
	v_pk_fma_f32 v[140:141], v[140:141], s[12:13], v[24:25] op_sel_hi:[1,0,1]
	v_pk_fma_f32 v[24:25], v[138:139], s[12:13], v[150:151] op_sel_hi:[1,0,1]
	v_mul_f32_e32 v31, v23, v23
	v_mul_f32_e32 v138, v145, v145
	v_fmac_f32_e32 v31, v22, v22
	v_fmac_f32_e32 v138, v144, v144
	v_add_f32_e32 v31, v31, v138
	v_mul_f32_e32 v138, v25, v25
	v_mul_f32_e32 v139, v141, v141
	v_fmac_f32_e32 v138, v24, v24
	v_fmac_f32_e32 v139, v140, v140
	v_add_f32_e32 v138, v138, v139
	v_add_f32_e32 v31, v31, v138
	v_lshlrev_b32_e32 v138, 16, v18
	v_and_b32_e32 v139, 0xffff0000, v18
	v_lshlrev_b32_e32 v18, 16, v19
	v_and_b32_e32 v19, 0xffff0000, v19
	v_cvt_pk_bf16_f32 v22, v22, v23
	v_cvt_pk_bf16_f32 v23, v144, v145
	v_cvt_pk_bf16_f32 v24, v24, v25
	v_cvt_pk_bf16_f32 v25, v140, v141
	v_lshlrev_b32_e32 v140, 16, v20
	v_and_b32_e32 v141, 0xffff0000, v20
	v_lshlrev_b32_e32 v20, 16, v21
	v_and_b32_e32 v21, 0xffff0000, v21
	v_pk_fma_f32 v[136:137], v[136:137], s[12:13], v[18:19] op_sel_hi:[1,0,1]
	v_pk_fma_f32 v[18:19], v[134:135], s[12:13], v[138:139] op_sel_hi:[1,0,1]
	v_pk_fma_f32 v[132:133], v[132:133], s[12:13], v[20:21] op_sel_hi:[1,0,1]
	v_mul_f32_e32 v20, v19, v19
	v_mul_f32_e32 v21, v137, v137
	v_pk_fma_f32 v[130:131], v[130:131], s[12:13], v[140:141] op_sel_hi:[1,0,1]
	v_fmac_f32_e32 v20, v18, v18
	v_fmac_f32_e32 v21, v136, v136
	v_add_f32_e32 v20, v20, v21
	v_mul_f32_e32 v21, v131, v131
	v_mul_f32_e32 v134, v133, v133
	v_fmac_f32_e32 v21, v130, v130
	v_fmac_f32_e32 v134, v132, v132
	v_add_f32_e32 v21, v21, v134
	v_add_f32_e32 v20, v20, v21
	v_add_f32_e32 v31, v31, v20
	v_mov_b32_e32 v138, v31
	v_mov_b32_e32 v194, v31
	s_nop 1
	v_permlane16_swap_b32_e32 v138, v194
	v_lshl_add_u64 v[20:21], s[66:67], 0, v[186:187]
	v_lshl_add_u64 v[134:135], v[26:27], 1, v[20:21]
	global_store_dwordx4 v[134:135], v[22:25], off
	v_cvt_pk_bf16_f32 v20, v18, v19
	s_waitcnt lgkmcnt(0)
	v_add_f32_e32 v18, v194, v138
	v_mov_b32_e32 v19, v18
	s_nop 1
	v_permlane32_swap_b32_e32 v18, v19
	v_cvt_pk_bf16_f32 v21, v136, v137
	v_cvt_pk_bf16_f32 v22, v130, v131
	v_cvt_pk_bf16_f32 v23, v132, v133
	global_store_dwordx4 v[134:135], v[20:23], off offset:256
	s_and_saveexec_b64 s[22:23], s[0:1]
	s_cbranch_execz .LBB0_2366
	v_lshl_add_u64 v[20:21], v[184:185], 2, s[6:7]
	s_waitcnt lgkmcnt(0)
	v_add_f32_e32 v18, v18, v19
	global_atomic_add_f32 v[20:21], v18, off
.LBB0_2366:
	s_or_b64 exec, exec, s[22:23]
	v_lshlrev_b32_e32 v18, 16, v14
	s_waitcnt lgkmcnt(0)
	v_and_b32_e32 v19, 0xffff0000, v14
	v_lshlrev_b32_e32 v14, 16, v15
	v_and_b32_e32 v15, 0xffff0000, v15
	v_lshlrev_b32_e32 v20, 16, v16
	v_and_b32_e32 v21, 0xffff0000, v16
	v_lshlrev_b32_e32 v16, 16, v17
	v_and_b32_e32 v17, 0xffff0000, v17
	v_pk_fma_f32 v[22:23], v[128:129], s[12:13], v[14:15] op_sel_hi:[1,0,1]
	v_pk_fma_f32 v[14:15], v[126:127], s[12:13], v[18:19] op_sel_hi:[1,0,1]
	v_pk_fma_f32 v[18:19], v[124:125], s[12:13], v[16:17] op_sel_hi:[1,0,1]
	v_pk_fma_f32 v[16:17], v[122:123], s[12:13], v[20:21] op_sel_hi:[1,0,1]
	v_mul_f32_e32 v20, v15, v15
	v_mul_f32_e32 v21, v23, v23
	v_fmac_f32_e32 v20, v14, v14
	v_fmac_f32_e32 v21, v22, v22
	v_add_f32_e32 v20, v20, v21
	v_mul_f32_e32 v21, v17, v17
	v_mul_f32_e32 v24, v19, v19
	v_fmac_f32_e32 v21, v16, v16
	v_fmac_f32_e32 v24, v18, v18
	v_add_f32_e32 v21, v21, v24
	v_cvt_pk_bf16_f32 v14, v14, v15
	v_cvt_pk_bf16_f32 v15, v22, v23
	v_cvt_pk_bf16_f32 v16, v16, v17
	v_cvt_pk_bf16_f32 v17, v18, v19
	v_lshlrev_b32_e32 v18, 16, v10
	v_and_b32_e32 v19, 0xffff0000, v10
	v_lshlrev_b32_e32 v10, 16, v11
	v_and_b32_e32 v11, 0xffff0000, v11
	v_add_f32_e32 v24, v20, v21
	v_lshlrev_b32_e32 v20, 16, v12
	v_and_b32_e32 v21, 0xffff0000, v12
	v_lshlrev_b32_e32 v12, 16, v13
	v_and_b32_e32 v13, 0xffff0000, v13
	v_pk_fma_f32 v[22:23], v[120:121], s[12:13], v[10:11] op_sel_hi:[1,0,1]
	v_pk_fma_f32 v[10:11], v[118:119], s[12:13], v[18:19] op_sel_hi:[1,0,1]
	v_pk_fma_f32 v[18:19], v[116:117], s[12:13], v[12:13] op_sel_hi:[1,0,1]
	v_mul_f32_e32 v12, v11, v11
	v_mul_f32_e32 v13, v23, v23
	v_pk_fma_f32 v[20:21], v[114:115], s[12:13], v[20:21] op_sel_hi:[1,0,1]
	v_fmac_f32_e32 v12, v10, v10
	v_fmac_f32_e32 v13, v22, v22
	v_add_f32_e32 v12, v12, v13
	v_mul_f32_e32 v13, v21, v21
	v_mul_f32_e32 v25, v19, v19
	v_fmac_f32_e32 v13, v20, v20
	v_fmac_f32_e32 v25, v18, v18
	v_add_f32_e32 v13, v13, v25
	v_add_f32_e32 v12, v12, v13
	v_add_f32_e32 v31, v24, v12
	v_mov_b32_e32 v114, v31
	v_mov_b32_e32 v194, v31
	s_nop 1
	v_permlane16_swap_b32_e32 v114, v194
	v_lshl_add_u64 v[12:13], s[66:67], 0, v[182:183]
	v_lshl_add_u64 v[24:25], v[26:27], 1, v[12:13]
	global_store_dwordx4 v[24:25], v[14:17], off
	v_cvt_pk_bf16_f32 v12, v10, v11
	s_waitcnt lgkmcnt(0)
	v_add_f32_e32 v10, v194, v114
	v_mov_b32_e32 v11, v10
	s_nop 1
	v_permlane32_swap_b32_e32 v10, v11
	v_cvt_pk_bf16_f32 v13, v22, v23
	v_cvt_pk_bf16_f32 v14, v20, v21
	v_cvt_pk_bf16_f32 v15, v18, v19
	global_store_dwordx4 v[24:25], v[12:15], off offset:256
	s_and_saveexec_b64 s[22:23], s[0:1]
	s_cbranch_execz .LBB0_2368
	v_lshl_add_u64 v[12:13], v[180:181], 2, s[6:7]
	s_waitcnt lgkmcnt(0)
	v_add_f32_e32 v10, v10, v11
	global_atomic_add_f32 v[12:13], v10, off
; __device__ __forceinline__ unsigned cvt_pk_bf16(float lo, float hi) { unsigned r; asm volatile("v_cvt_pk_bf16_f32 %0, %1, %2" : "=v"(r) : "v"(lo), "v"(hi)); return r; }
;     __device__ __forceinline__ void operator()(const f32x4 (&acc)[2][2][4][2], const Unit& u, int wr, int wc, int fr, int fq) const {
;     ...
;                 for (int bj = 0; bj < 2; ++bj) { const size_t o2 = (size_t)(row0 + ai * HALF + m * 16) * DM + col0 + bj * HALF;
;                     if constexpr (XF32) { a[m][bj][0] = *(const f32x4*)((const float*)xin + o2); a[m][bj][1] = *(const f32x4*)((const float*)xin + o2 + 4); }
;                     else { const u32x4 w = *(const u32x4*)((const bf16_t*)xin + o2); a[m][bj][0] = __builtin_bit_cast(f32x4, w); } }
; #pragma unroll
;             for (int m = 0; m < 4; ++m) {
;                 const int row = row0 + ai * HALF + m * 16; const size_t off = (size_t)row * DM + col0; float q = 0.f;
; #pragma unroll
;                 for (int bj = 0; bj < 2; ++bj) { const size_t o2 = off + bj * HALF;
;                     f32x4 a0, a1;
;                     if constexpr (XF32) { a0 = a[m][bj][0]; a1 = a[m][bj][1]; }
;                     else { const u32x4 w = __builtin_bit_cast(u32x4, a[m][bj][0]);
;                         a0 = (f32x4){__uint_as_float(w.x << 16), __uint_as_float(w.x & 0xffff0000u), __uint_as_float(w.y << 16), __uint_as_float(w.y & 0xffff0000u)};
;                         a1 = (f32x4){__uint_as_float(w.z << 16), __uint_as_float(w.z & 0xffff0000u), __uint_as_float(w.w << 16), __uint_as_float(w.w & 0xffff0000u)}; }
;                     const f32x4 v0 = a0 + acc[ai][bj][m][0] * sc, v1 = a1 + acc[ai][bj][m][1] * sc;
;                     q += ((v0[0] * v0[0] + v0[1] * v0[1]) + (v0[2] * v0[2] + v0[3] * v0[3])) + ((v1[0] * v1[0] + v1[1] * v1[1]) + (v1[2] * v1[2] + v1[3] * v1[3]));
;                     u32x4 wo; wo.x = cvt_pk_bf16(v0[0], v0[1]); wo.y = cvt_pk_bf16(v0[2], v0[3]); wo.z = cvt_pk_bf16(v1[0], v1[1]); wo.w = cvt_pk_bf16(v1[2], v1[3]);
;                     *(u32x4*)(xb + o2) = wo;
;                     if (x8) { u32x2 w8; w8.x = pk4_fp8(v0[0], v0[1], v0[2], v0[3]); w8.y = pk4_fp8(v1[0], v1[1], v1[2], v1[3]); *(u32x2*)(x8 + o2) = w8; } }
;                 q += __shfl_xor(q, 16); q += __shfl_xor(q, 32);
;                 if (fq == 0) unsafeAtomicAdd(ss + row, q);
.LBB0_2368:
	s_or_b64 exec, exec, s[22:23]
	v_lshlrev_b32_e32 v10, 16, v6
	s_waitcnt lgkmcnt(0)
	v_and_b32_e32 v11, 0xffff0000, v6
	v_lshlrev_b32_e32 v6, 16, v7
	v_and_b32_e32 v7, 0xffff0000, v7
	v_lshlrev_b32_e32 v12, 16, v8
	v_and_b32_e32 v13, 0xffff0000, v8
	v_lshlrev_b32_e32 v8, 16, v9
	v_and_b32_e32 v9, 0xffff0000, v9
	v_pk_fma_f32 v[14:15], v[112:113], s[12:13], v[6:7] op_sel_hi:[1,0,1]
	v_pk_fma_f32 v[6:7], v[110:111], s[12:13], v[10:11] op_sel_hi:[1,0,1]
	v_pk_fma_f32 v[10:11], v[108:109], s[12:13], v[8:9] op_sel_hi:[1,0,1]
	v_pk_fma_f32 v[8:9], v[106:107], s[12:13], v[12:13] op_sel_hi:[1,0,1]
	v_mul_f32_e32 v12, v7, v7
	v_mul_f32_e32 v13, v15, v15
	v_fmac_f32_e32 v12, v6, v6
	v_fmac_f32_e32 v13, v14, v14
	v_add_f32_e32 v12, v12, v13
	v_mul_f32_e32 v13, v9, v9
	v_mul_f32_e32 v16, v11, v11
	v_fmac_f32_e32 v13, v8, v8
	v_fmac_f32_e32 v16, v10, v10
	v_add_f32_e32 v13, v13, v16
	v_cvt_pk_bf16_f32 v6, v6, v7
	v_cvt_pk_bf16_f32 v7, v14, v15
	v_cvt_pk_bf16_f32 v8, v8, v9
	v_cvt_pk_bf16_f32 v9, v10, v11
	v_lshlrev_b32_e32 v10, 16, v2
	v_and_b32_e32 v11, 0xffff0000, v2
	v_lshlrev_b32_e32 v2, 16, v3
	v_and_b32_e32 v3, 0xffff0000, v3
	v_add_f32_e32 v16, v12, v13
	v_lshlrev_b32_e32 v12, 16, v4
	v_and_b32_e32 v13, 0xffff0000, v4
	v_lshlrev_b32_e32 v4, 16, v5
	v_and_b32_e32 v5, 0xffff0000, v5
	v_pk_fma_f32 v[14:15], v[104:105], s[12:13], v[2:3] op_sel_hi:[1,0,1]
	v_pk_fma_f32 v[2:3], v[102:103], s[12:13], v[10:11] op_sel_hi:[1,0,1]
	v_pk_fma_f32 v[10:11], v[100:101], s[12:13], v[4:5] op_sel_hi:[1,0,1]
	v_mul_f32_e32 v4, v3, v3
	v_mul_f32_e32 v5, v15, v15
	v_pk_fma_f32 v[12:13], v[98:99], s[12:13], v[12:13] op_sel_hi:[1,0,1]
	v_fmac_f32_e32 v4, v2, v2
	v_fmac_f32_e32 v5, v14, v14
	v_add_f32_e32 v4, v4, v5
	v_mul_f32_e32 v5, v13, v13
	v_mul_f32_e32 v17, v11, v11
	v_fmac_f32_e32 v5, v12, v12
	v_fmac_f32_e32 v17, v10, v10
	v_add_f32_e32 v5, v5, v17
	v_add_f32_e32 v4, v4, v5
	v_add_f32_e32 v18, v16, v4
	v_mov_b32_e32 v19, v18
	v_mov_b32_e32 v194, v18
	s_nop 1
	v_permlane16_swap_b32_e32 v19, v194
	v_lshl_add_u64 v[4:5], s[66:67], 0, v[178:179]
	v_lshl_add_u64 v[16:17], v[26:27], 1, v[4:5]
	global_store_dwordx4 v[16:17], v[6:9], off
	v_cvt_pk_bf16_f32 v4, v2, v3
	s_waitcnt lgkmcnt(0)
	v_add_f32_e32 v2, v194, v19
	v_mov_b32_e32 v3, v2
	s_nop 1
	v_permlane32_swap_b32_e32 v2, v3
	v_cvt_pk_bf16_f32 v5, v14, v15
	v_cvt_pk_bf16_f32 v6, v12, v13
	v_cvt_pk_bf16_f32 v7, v10, v11
	global_store_dwordx4 v[16:17], v[4:7], off offset:256
	s_and_saveexec_b64 s[22:23], s[0:1]
	s_cbranch_execz .LBB0_2370
	v_lshl_add_u64 v[4:5], v[32:33], 2, s[6:7]
	s_waitcnt lgkmcnt(0)
	v_add_f32_e32 v2, v2, v3
	global_atomic_add_f32 v[4:5], v2, off
.LBB0_2370:
	s_or_b64 exec, exec, s[22:23]
	v_add_u32_e32 v106, 0x80, v30
	v_ashrrev_i32_e32 v107, 31, v106
	v_lshlrev_b64 v[116:117], 13, v[106:107]
	s_waitcnt lgkmcnt(0)
	v_lshl_add_u64 v[2:3], v[28:29], 0, v[116:117]
	global_load_dwordx4 v[108:111], v[2:3], off
	global_load_dwordx4 v[112:115], v[2:3], off offset:256
	v_add_u32_e32 v102, 0x90, v30
	v_add_u32_e32 v98, 0xa0, v30
	v_add_u32_e32 v30, 0xb0, v30
	v_ashrrev_i32_e32 v103, 31, v102
	v_ashrrev_i32_e32 v99, 31, v98
	v_ashrrev_i32_e32 v31, 31, v30
	v_lshlrev_b64 v[104:105], 13, v[102:103]
	v_lshlrev_b64 v[100:101], 13, v[98:99]
	v_lshlrev_b64 v[32:33], 13, v[30:31]
	v_lshl_add_u64 v[2:3], v[28:29], 0, v[104:105]
	v_lshl_add_u64 v[4:5], v[28:29], 0, v[100:101]
	v_lshl_add_u64 v[28:29], v[28:29], 0, v[32:33]
	global_load_dwordx4 v[22:25], v[2:3], off
	global_load_dwordx4 v[18:21], v[2:3], off offset:256
	global_load_dwordx4 v[14:17], v[4:5], off
	global_load_dwordx4 v[10:13], v[4:5], off offset:256
	global_load_dwordx4 v[6:9], v[28:29], off
	s_nop 0
	global_load_dwordx4 v[2:5], v[28:29], off offset:256
	s_waitcnt vmcnt(7)
	v_lshlrev_b32_e32 v28, 16, v108
	v_and_b32_e32 v29, 0xffff0000, v108
	v_lshlrev_b32_e32 v108, 16, v109
	v_and_b32_e32 v109, 0xffff0000, v109
	v_lshlrev_b32_e32 v118, 16, v110
	v_and_b32_e32 v119, 0xffff0000, v110
	v_lshlrev_b32_e32 v110, 16, v111
	v_and_b32_e32 v111, 0xffff0000, v111
	s_waitcnt vmcnt(6)
	v_lshlrev_b32_e32 v120, 16, v112
	v_and_b32_e32 v121, 0xffff0000, v112
	v_lshlrev_b32_e32 v112, 16, v113
	v_and_b32_e32 v113, 0xffff0000, v113
	v_lshlrev_b32_e32 v122, 16, v114
	v_and_b32_e32 v123, 0xffff0000, v114
	v_lshlrev_b32_e32 v114, 16, v115
	v_and_b32_e32 v115, 0xffff0000, v115
	v_pk_fma_f32 v[96:97], v[96:97], s[12:13], v[108:109] op_sel_hi:[1,0,1]
	v_pk_fma_f32 v[28:29], v[94:95], s[12:13], v[28:29] op_sel_hi:[1,0,1]
	v_pk_fma_f32 v[92:93], v[92:93], s[12:13], v[110:111] op_sel_hi:[1,0,1]
	v_pk_fma_f32 v[90:91], v[90:91], s[12:13], v[118:119] op_sel_hi:[1,0,1]
	v_pk_fma_f32 v[88:89], v[88:89], s[12:13], v[112:113] op_sel_hi:[1,0,1]
	v_pk_fma_f32 v[86:87], v[86:87], s[12:13], v[120:121] op_sel_hi:[1,0,1]
	v_pk_fma_f32 v[94:95], v[84:85], s[12:13], v[114:115] op_sel_hi:[1,0,1]
	v_pk_fma_f32 v[108:109], v[82:83], s[12:13], v[122:123] op_sel_hi:[1,0,1]
	v_mul_f32_e32 v110, v29, v29
	v_mul_f32_e32 v111, v97, v97
	v_mul_f32_e32 v112, v91, v91
	v_mul_f32_e32 v113, v93, v93
	v_cvt_pk_bf16_f32 v82, v28, v29
	v_cvt_pk_bf16_f32 v83, v96, v97
	v_cvt_pk_bf16_f32 v84, v90, v91
	v_cvt_pk_bf16_f32 v85, v92, v93
	v_mul_f32_e32 v29, v87, v87
	v_mul_f32_e32 v91, v89, v89
	v_mul_f32_e32 v93, v109, v109
	v_mul_f32_e32 v97, v95, v95
	v_fmac_f32_e32 v110, v28, v28
	v_fmac_f32_e32 v111, v96, v96
	v_fmac_f32_e32 v112, v90, v90
	v_fmac_f32_e32 v113, v92, v92
	v_fmac_f32_e32 v29, v86, v86
	v_fmac_f32_e32 v91, v88, v88
	v_fmac_f32_e32 v93, v108, v108
	v_fmac_f32_e32 v97, v94, v94
	v_add_f32_e32 v28, v110, v111
	v_add_f32_e32 v90, v112, v113
	v_add_f32_e32 v29, v29, v91
	v_add_f32_e32 v91, v93, v97
	v_add_f32_e32 v28, v28, v90
	v_add_f32_e32 v29, v29, v91
	v_add_f32_e32 v92, v28, v29
	v_mov_b32_e32 v93, v92
	v_mov_b32_e32 v194, v92
	s_nop 1
	v_permlane16_swap_b32_e32 v93, v194
	v_lshl_add_u64 v[28:29], s[66:67], 0, v[116:117]
	v_lshl_add_u64 v[90:91], v[26:27], 1, v[28:29]
	global_store_dwordx4 v[90:91], v[82:85], off
	s_waitcnt lgkmcnt(0)
	v_add_f32_e32 v28, v194, v93
	v_mov_b32_e32 v29, v28
	s_nop 1
	v_permlane32_swap_b32_e32 v28, v29
	v_cvt_pk_bf16_f32 v82, v86, v87
	v_cvt_pk_bf16_f32 v83, v88, v89
	v_cvt_pk_bf16_f32 v84, v108, v109
	v_cvt_pk_bf16_f32 v85, v94, v95
	global_store_dwordx4 v[90:91], v[82:85], off offset:256
	s_and_saveexec_b64 s[22:23], s[0:1]
	s_cbranch_execz .LBB0_2372
	v_lshl_add_u64 v[82:83], v[106:107], 2, s[6:7]
	s_waitcnt lgkmcnt(0)
	v_add_f32_e32 v28, v28, v29
	global_atomic_add_f32 v[82:83], v28, off
; __device__ __forceinline__ unsigned cvt_pk_bf16(float lo, float hi) { unsigned r; asm volatile("v_cvt_pk_bf16_f32 %0, %1, %2" : "=v"(r) : "v"(lo), "v"(hi)); return r; }
;     __device__ __forceinline__ void operator()(const f32x4 (&acc)[2][2][4][2], const Unit& u, int wr, int wc, int fr, int fq) const {
;     ...
;             for (int m = 0; m < 4; ++m) {
;                 const int row = row0 + ai * HALF + m * 16; const size_t off = (size_t)row * DM + col0; float q = 0.f;
; #pragma unroll
;                 for (int bj = 0; bj < 2; ++bj) { const size_t o2 = off + bj * HALF;
;                     f32x4 a0, a1;
;                     if constexpr (XF32) { a0 = a[m][bj][0]; a1 = a[m][bj][1]; }
;                     else { const u32x4 w = __builtin_bit_cast(u32x4, a[m][bj][0]);
;                         a0 = (f32x4){__uint_as_float(w.x << 16), __uint_as_float(w.x & 0xffff0000u), __uint_as_float(w.y << 16), __uint_as_float(w.y & 0xffff0000u)};
;                         a1 = (f32x4){__uint_as_float(w.z << 16), __uint_as_float(w.z & 0xffff0000u), __uint_as_float(w.w << 16), __uint_as_float(w.w & 0xffff0000u)}; }
;                     const f32x4 v0 = a0 + acc[ai][bj][m][0] * sc, v1 = a1 + acc[ai][bj][m][1] * sc;
;                     q += ((v0[0] * v0[0] + v0[1] * v0[1]) + (v0[2] * v0[2] + v0[3] * v0[3])) + ((v1[0] * v1[0] + v1[1] * v1[1]) + (v1[2] * v1[2] + v1[3] * v1[3]));
;                     u32x4 wo; wo.x = cvt_pk_bf16(v0[0], v0[1]); wo.y = cvt_pk_bf16(v0[2], v0[3]); wo.z = cvt_pk_bf16(v1[0], v1[1]); wo.w = cvt_pk_bf16(v1[2], v1[3]);
;                     *(u32x4*)(xb + o2) = wo;
;                     if (x8) { u32x2 w8; w8.x = pk4_fp8(v0[0], v0[1], v0[2], v0[3]); w8.y = pk4_fp8(v1[0], v1[1], v1[2], v1[3]); *(u32x2*)(x8 + o2) = w8; } }
;                 q += __shfl_xor(q, 16); q += __shfl_xor(q, 32);
;                 if (fq == 0) unsafeAtomicAdd(ss + row, q);
.LBB0_2372:
	s_or_b64 exec, exec, s[22:23]
	s_waitcnt vmcnt(7)
	v_lshlrev_b32_e32 v28, 16, v22
	s_waitcnt lgkmcnt(0)
	v_and_b32_e32 v29, 0xffff0000, v22
	v_lshlrev_b32_e32 v22, 16, v23
	v_and_b32_e32 v23, 0xffff0000, v23
	v_lshlrev_b32_e32 v82, 16, v24
	v_and_b32_e32 v83, 0xffff0000, v24
	v_lshlrev_b32_e32 v24, 16, v25
	v_and_b32_e32 v25, 0xffff0000, v25
	v_pk_fma_f32 v[80:81], v[80:81], s[12:13], v[22:23] op_sel_hi:[1,0,1]
	v_pk_fma_f32 v[22:23], v[78:79], s[12:13], v[28:29] op_sel_hi:[1,0,1]
	v_pk_fma_f32 v[28:29], v[76:77], s[12:13], v[24:25] op_sel_hi:[1,0,1]
	v_pk_fma_f32 v[24:25], v[74:75], s[12:13], v[82:83] op_sel_hi:[1,0,1]
	v_mul_f32_e32 v74, v23, v23
	v_mul_f32_e32 v75, v81, v81
	v_fmac_f32_e32 v74, v22, v22
	v_fmac_f32_e32 v75, v80, v80
	v_add_f32_e32 v74, v74, v75
	v_mul_f32_e32 v75, v25, v25
	v_mul_f32_e32 v76, v29, v29
	v_fmac_f32_e32 v75, v24, v24
	v_fmac_f32_e32 v76, v28, v28
	v_add_f32_e32 v75, v75, v76
	v_cvt_pk_bf16_f32 v22, v22, v23
	v_cvt_pk_bf16_f32 v23, v80, v81
	v_cvt_pk_bf16_f32 v24, v24, v25
	v_cvt_pk_bf16_f32 v25, v28, v29
	s_waitcnt vmcnt(6)
	v_lshlrev_b32_e32 v28, 16, v18
	v_and_b32_e32 v29, 0xffff0000, v18
	v_lshlrev_b32_e32 v18, 16, v19
	v_and_b32_e32 v19, 0xffff0000, v19
	v_add_f32_e32 v76, v74, v75
	v_lshlrev_b32_e32 v74, 16, v20
	v_and_b32_e32 v75, 0xffff0000, v20
	v_lshlrev_b32_e32 v20, 16, v21
	v_and_b32_e32 v21, 0xffff0000, v21
	v_pk_fma_f32 v[72:73], v[72:73], s[12:13], v[18:19] op_sel_hi:[1,0,1]
	v_pk_fma_f32 v[18:19], v[70:71], s[12:13], v[28:29] op_sel_hi:[1,0,1]
	v_pk_fma_f32 v[28:29], v[68:69], s[12:13], v[20:21] op_sel_hi:[1,0,1]
	v_mul_f32_e32 v20, v19, v19
	v_mul_f32_e32 v21, v73, v73
	v_pk_fma_f32 v[66:67], v[66:67], s[12:13], v[74:75] op_sel_hi:[1,0,1]
	v_fmac_f32_e32 v20, v18, v18
	v_fmac_f32_e32 v21, v72, v72
	v_add_f32_e32 v20, v20, v21
	v_mul_f32_e32 v21, v67, v67
	v_mul_f32_e32 v68, v29, v29
	v_fmac_f32_e32 v21, v66, v66
	v_fmac_f32_e32 v68, v28, v28
	v_add_f32_e32 v21, v21, v68
	v_add_f32_e32 v20, v20, v21
	v_add_f32_e32 v70, v76, v20
	v_mov_b32_e32 v71, v70
	v_mov_b32_e32 v194, v70
	s_nop 1
	v_permlane16_swap_b32_e32 v71, v194
	v_lshl_add_u64 v[20:21], s[66:67], 0, v[104:105]
	v_lshl_add_u64 v[68:69], v[26:27], 1, v[20:21]
	global_store_dwordx4 v[68:69], v[22:25], off
	v_cvt_pk_bf16_f32 v20, v18, v19
	s_waitcnt lgkmcnt(0)
	v_add_f32_e32 v18, v194, v71
	v_mov_b32_e32 v19, v18
	s_nop 1
	v_permlane32_swap_b32_e32 v18, v19
	v_cvt_pk_bf16_f32 v21, v72, v73
	v_cvt_pk_bf16_f32 v22, v66, v67
	v_cvt_pk_bf16_f32 v23, v28, v29
	global_store_dwordx4 v[68:69], v[20:23], off offset:256
	s_and_saveexec_b64 s[22:23], s[0:1]
	s_cbranch_execz .LBB0_2374
	v_lshl_add_u64 v[20:21], v[102:103], 2, s[6:7]
	s_waitcnt lgkmcnt(0)
	v_add_f32_e32 v18, v18, v19
	global_atomic_add_f32 v[20:21], v18, off
; __device__ __forceinline__ unsigned cvt_pk_bf16(float lo, float hi) { unsigned r; asm volatile("v_cvt_pk_bf16_f32 %0, %1, %2" : "=v"(r) : "v"(lo), "v"(hi)); return r; }
;     __device__ __forceinline__ void operator()(const f32x4 (&acc)[2][2][4][2], const Unit& u, int wr, int wc, int fr, int fq) const {
;     ...
;             for (int m = 0; m < 4; ++m) {
;                 const int row = row0 + ai * HALF + m * 16; const size_t off = (size_t)row * DM + col0; float q = 0.f;
; #pragma unroll
;                 for (int bj = 0; bj < 2; ++bj) { const size_t o2 = off + bj * HALF;
;                     f32x4 a0, a1;
;                     if constexpr (XF32) { a0 = a[m][bj][0]; a1 = a[m][bj][1]; }
;                     else { const u32x4 w = __builtin_bit_cast(u32x4, a[m][bj][0]);
;                         a0 = (f32x4){__uint_as_float(w.x << 16), __uint_as_float(w.x & 0xffff0000u), __uint_as_float(w.y << 16), __uint_as_float(w.y & 0xffff0000u)};
;                         a1 = (f32x4){__uint_as_float(w.z << 16), __uint_as_float(w.z & 0xffff0000u), __uint_as_float(w.w << 16), __uint_as_float(w.w & 0xffff0000u)}; }
;                     const f32x4 v0 = a0 + acc[ai][bj][m][0] * sc, v1 = a1 + acc[ai][bj][m][1] * sc;
;                     q += ((v0[0] * v0[0] + v0[1] * v0[1]) + (v0[2] * v0[2] + v0[3] * v0[3])) + ((v1[0] * v1[0] + v1[1] * v1[1]) + (v1[2] * v1[2] + v1[3] * v1[3]));
;                     u32x4 wo; wo.x = cvt_pk_bf16(v0[0], v0[1]); wo.y = cvt_pk_bf16(v0[2], v0[3]); wo.z = cvt_pk_bf16(v1[0], v1[1]); wo.w = cvt_pk_bf16(v1[2], v1[3]);
;                     *(u32x4*)(xb + o2) = wo;
;                     if (x8) { u32x2 w8; w8.x = pk4_fp8(v0[0], v0[1], v0[2], v0[3]); w8.y = pk4_fp8(v1[0], v1[1], v1[2], v1[3]); *(u32x2*)(x8 + o2) = w8; } }
;                 q += __shfl_xor(q, 16); q += __shfl_xor(q, 32);
;                 if (fq == 0) unsafeAtomicAdd(ss + row, q);
.LBB0_2374:
	s_or_b64 exec, exec, s[22:23]
	s_waitcnt vmcnt(7)
	v_lshlrev_b32_e32 v18, 16, v14
	s_waitcnt lgkmcnt(0)
	v_and_b32_e32 v19, 0xffff0000, v14
	v_lshlrev_b32_e32 v14, 16, v15
	v_and_b32_e32 v15, 0xffff0000, v15
	v_lshlrev_b32_e32 v20, 16, v16
	v_and_b32_e32 v21, 0xffff0000, v16
	v_lshlrev_b32_e32 v16, 16, v17
	v_and_b32_e32 v17, 0xffff0000, v17
	v_pk_fma_f32 v[22:23], v[64:65], s[12:13], v[14:15] op_sel_hi:[1,0,1]
	v_pk_fma_f32 v[14:15], v[62:63], s[12:13], v[18:19] op_sel_hi:[1,0,1]
	v_pk_fma_f32 v[18:19], v[60:61], s[12:13], v[16:17] op_sel_hi:[1,0,1]
	v_pk_fma_f32 v[16:17], v[58:59], s[12:13], v[20:21] op_sel_hi:[1,0,1]
	v_mul_f32_e32 v20, v15, v15
	v_mul_f32_e32 v21, v23, v23
	v_fmac_f32_e32 v20, v14, v14
	v_fmac_f32_e32 v21, v22, v22
	v_add_f32_e32 v20, v20, v21
	v_mul_f32_e32 v21, v17, v17
	v_mul_f32_e32 v24, v19, v19
	v_fmac_f32_e32 v21, v16, v16
	v_fmac_f32_e32 v24, v18, v18
	v_add_f32_e32 v21, v21, v24
	v_cvt_pk_bf16_f32 v14, v14, v15
	v_cvt_pk_bf16_f32 v15, v22, v23
	v_cvt_pk_bf16_f32 v16, v16, v17
	v_cvt_pk_bf16_f32 v17, v18, v19
	s_waitcnt vmcnt(6)
	v_lshlrev_b32_e32 v18, 16, v10
	v_and_b32_e32 v19, 0xffff0000, v10
	v_lshlrev_b32_e32 v10, 16, v11
	v_and_b32_e32 v11, 0xffff0000, v11
	v_add_f32_e32 v24, v20, v21
	v_lshlrev_b32_e32 v20, 16, v12
	v_and_b32_e32 v21, 0xffff0000, v12
	v_lshlrev_b32_e32 v12, 16, v13
	v_and_b32_e32 v13, 0xffff0000, v13
	v_pk_fma_f32 v[22:23], v[56:57], s[12:13], v[10:11] op_sel_hi:[1,0,1]
	v_pk_fma_f32 v[10:11], v[54:55], s[12:13], v[18:19] op_sel_hi:[1,0,1]
	v_pk_fma_f32 v[18:19], v[52:53], s[12:13], v[12:13] op_sel_hi:[1,0,1]
	v_mul_f32_e32 v12, v11, v11
	v_mul_f32_e32 v13, v23, v23
	v_pk_fma_f32 v[20:21], v[50:51], s[12:13], v[20:21] op_sel_hi:[1,0,1]
	v_fmac_f32_e32 v12, v10, v10
	v_fmac_f32_e32 v13, v22, v22
	v_add_f32_e32 v12, v12, v13
	v_mul_f32_e32 v13, v21, v21
	v_mul_f32_e32 v25, v19, v19
	v_fmac_f32_e32 v13, v20, v20
	v_fmac_f32_e32 v25, v18, v18
	v_add_f32_e32 v13, v13, v25
	v_add_f32_e32 v12, v12, v13
	v_add_f32_e32 v28, v24, v12
	v_mov_b32_e32 v29, v28
	v_mov_b32_e32 v194, v28
	s_nop 1
	v_permlane16_swap_b32_e32 v29, v194
	v_lshl_add_u64 v[12:13], s[66:67], 0, v[100:101]
	v_lshl_add_u64 v[24:25], v[26:27], 1, v[12:13]
	global_store_dwordx4 v[24:25], v[14:17], off
	v_cvt_pk_bf16_f32 v12, v10, v11
	s_waitcnt lgkmcnt(0)
	v_add_f32_e32 v10, v194, v29
	v_mov_b32_e32 v11, v10
	s_nop 1
	v_permlane32_swap_b32_e32 v10, v11
	v_cvt_pk_bf16_f32 v13, v22, v23
	v_cvt_pk_bf16_f32 v14, v20, v21
	v_cvt_pk_bf16_f32 v15, v18, v19
	global_store_dwordx4 v[24:25], v[12:15], off offset:256
	s_and_saveexec_b64 s[22:23], s[0:1]
	s_cbranch_execz .LBB0_2376
	v_lshl_add_u64 v[12:13], v[98:99], 2, s[6:7]
	s_waitcnt lgkmcnt(0)
	v_add_f32_e32 v10, v10, v11
	global_atomic_add_f32 v[12:13], v10, off
.LBB0_2376:
	s_or_b64 exec, exec, s[22:23]
	s_waitcnt vmcnt(7)
	v_lshlrev_b32_e32 v10, 16, v6
	s_waitcnt lgkmcnt(0)
	v_and_b32_e32 v11, 0xffff0000, v6
	v_lshlrev_b32_e32 v6, 16, v7
	v_and_b32_e32 v7, 0xffff0000, v7
	v_lshlrev_b32_e32 v12, 16, v8
	v_and_b32_e32 v13, 0xffff0000, v8
	v_lshlrev_b32_e32 v8, 16, v9
	v_and_b32_e32 v9, 0xffff0000, v9
	v_pk_fma_f32 v[14:15], v[48:49], s[12:13], v[6:7] op_sel_hi:[1,0,1]
	v_pk_fma_f32 v[6:7], v[46:47], s[12:13], v[10:11] op_sel_hi:[1,0,1]
	v_pk_fma_f32 v[10:11], v[44:45], s[12:13], v[8:9] op_sel_hi:[1,0,1]
	v_pk_fma_f32 v[8:9], v[42:43], s[12:13], v[12:13] op_sel_hi:[1,0,1]
	v_mul_f32_e32 v12, v7, v7
	v_mul_f32_e32 v13, v15, v15
	v_fmac_f32_e32 v12, v6, v6
	v_fmac_f32_e32 v13, v14, v14
	v_add_f32_e32 v12, v12, v13
	v_mul_f32_e32 v13, v9, v9
	v_mul_f32_e32 v16, v11, v11
	v_fmac_f32_e32 v13, v8, v8
	v_fmac_f32_e32 v16, v10, v10
	v_add_f32_e32 v13, v13, v16
	v_cvt_pk_bf16_f32 v6, v6, v7
	v_cvt_pk_bf16_f32 v7, v14, v15
	v_cvt_pk_bf16_f32 v8, v8, v9
	v_cvt_pk_bf16_f32 v9, v10, v11
	s_waitcnt vmcnt(6)
	v_lshlrev_b32_e32 v10, 16, v2
	v_and_b32_e32 v11, 0xffff0000, v2
	v_lshlrev_b32_e32 v2, 16, v3
	v_and_b32_e32 v3, 0xffff0000, v3
	v_add_f32_e32 v16, v12, v13
	v_lshlrev_b32_e32 v12, 16, v4
	v_and_b32_e32 v13, 0xffff0000, v4
	v_lshlrev_b32_e32 v4, 16, v5
	v_and_b32_e32 v5, 0xffff0000, v5
	v_pk_fma_f32 v[14:15], v[40:41], s[12:13], v[2:3] op_sel_hi:[1,0,1]
	v_pk_fma_f32 v[2:3], v[38:39], s[12:13], v[10:11] op_sel_hi:[1,0,1]
	v_pk_fma_f32 v[10:11], v[36:37], s[12:13], v[4:5] op_sel_hi:[1,0,1]
	v_mul_f32_e32 v4, v3, v3
	v_mul_f32_e32 v5, v15, v15
	v_pk_fma_f32 v[12:13], v[34:35], s[12:13], v[12:13] op_sel_hi:[1,0,1]
	v_fmac_f32_e32 v4, v2, v2
	v_fmac_f32_e32 v5, v14, v14
	v_add_f32_e32 v4, v4, v5
	v_mul_f32_e32 v5, v13, v13
	v_mul_f32_e32 v17, v11, v11
	v_fmac_f32_e32 v5, v12, v12
	v_fmac_f32_e32 v17, v10, v10
	v_add_f32_e32 v5, v5, v17
	v_add_f32_e32 v4, v4, v5
	v_add_f32_e32 v18, v16, v4
	v_mov_b32_e32 v19, v18
	v_mov_b32_e32 v194, v18
	s_nop 1
	v_permlane16_swap_b32_e32 v19, v194
	v_lshl_add_u64 v[4:5], s[66:67], 0, v[32:33]
	v_lshl_add_u64 v[16:17], v[26:27], 1, v[4:5]
	global_store_dwordx4 v[16:17], v[6:9], off
	v_cvt_pk_bf16_f32 v4, v2, v3
	s_waitcnt lgkmcnt(0)
	v_add_f32_e32 v2, v194, v19
	v_mov_b32_e32 v3, v2
	s_nop 1
	v_permlane32_swap_b32_e32 v2, v3
	v_cvt_pk_bf16_f32 v5, v14, v15
	v_cvt_pk_bf16_f32 v6, v12, v13
	v_cvt_pk_bf16_f32 v7, v10, v11
	global_store_dwordx4 v[16:17], v[4:7], off offset:256
	s_and_saveexec_b64 s[22:23], s[0:1]
	s_cbranch_execz .LBB0_2378
	v_lshl_add_u64 v[4:5], v[30:31], 2, s[6:7]
	s_waitcnt lgkmcnt(0)
	v_add_f32_e32 v2, v2, v3
	global_atomic_add_f32 v[4:5], v2, off
